# RG-LRU gate block: sqrtf expansion slimmed to v_sqrt_f32 + correction step (denormal scaling and class test can never fire for 1-a*a; bit-identical), redundant s_nop pads dropped; attention loop s_nop
# speedup vs baseline: 1.0139x; 1.0139x over previous
; __device__ __forceinline__ void ph_lru(const Ptrs& P, unsigned char* lds, int mode, int item0) {
;     ...
;         const int trow = 16 * wid + fr;
;         const bf16x8 af0 = *(const bf16x8*)(XB + trow * 128 + ((fq ^ ((trow >> 1) & 7)) << 4));
;         const bf16x8 af1 = *(const bf16x8*)(XB + trow * 128 + (((4 + fq) ^ ((trow >> 1) & 7)) << 4));
;         float av[2][4][4], uv[2][4][4], Ae[2][4], He[2][4];
; #pragma unroll
;         for (int dir = 0; dir < 2; ++dir) {
;             const unsigned char* wa = WL + (dir * 2 + 0) * 8192; const unsigned char* wx = WL + (dir * 2 + 1) * 8192;
; #pragma unroll
;             for (int ct = 0; ct < 4; ++ct) {
;                 const int e = 16 * ct + fr, ky = (e >> 1) & 7;
;                 const bf16x8 wa0 = *(const bf16x8*)(wa + e * 128 + ((fq ^ ky) << 4)), wa1 = *(const bf16x8*)(wa + e * 128 + (((4 + fq) ^ ky) << 4));
;                 const bf16x8 wx0 = *(const bf16x8*)(wx + e * 128 + ((fq ^ ky) << 4)), wx1 = *(const bf16x8*)(wx + e * 128 + (((4 + fq) ^ ky) << 4));
;                 f32x4 ga = {0.f, 0.f, 0.f, 0.f}, gx = {0.f, 0.f, 0.f, 0.f};
;                 ga = __builtin_amdgcn_mfma_f32_16x16x32_bf16(af0, wa0, ga, 0, 0, 0); ga = __builtin_amdgcn_mfma_f32_16x16x32_bf16(af1, wa1, ga, 0, 0, 0);
;                 gx = __builtin_amdgcn_mfma_f32_16x16x32_bf16(af0, wx0, gx, 0, 0, 0); gx = __builtin_amdgcn_mfma_f32_16x16x32_bf16(af1, wx1, gx, 0, 0, 0);
;                 const float bav = GBL[dir * 64 + e], bxv = GBL[128 + dir * 64 + e], c8 = GBL[256 + dir * 64 + e];
; #pragma unroll
;                 for (int j = 0; j < 4; ++j) {
;                     const float r = fsigmoid(ga[j] + bav), ig = fsigmoid(gx[j] + bxv);
;                     const float a = __builtin_amdgcn_exp2f(-c8 * r);
;                     av[dir][ct][j] = a; uv[dir][ct][j] = sqrtf(fmaxf(1.f - a * a, 0.f)) * ig * X[(16 * wid + 4 * fq + j) * 68 + e];
;                 }
;                 float Al = av[dir][ct][0] * av[dir][ct][1] * av[dir][ct][2] * av[dir][ct][3], Hl;
;                 if (dir == 0) Hl = ((uv[dir][ct][0] * av[dir][ct][1] + uv[dir][ct][1]) * av[dir][ct][2] + uv[dir][ct][2]) * av[dir][ct][3] + uv[dir][ct][3];
;                 else Hl = ((uv[dir][ct][3] * av[dir][ct][2] + uv[dir][ct][2]) * av[dir][ct][1] + uv[dir][ct][1]) * av[dir][ct][0] + uv[dir][ct][0];
;                 const int pq = dir == 0 ? fq : 3 - fq;
;                 {
.LBB0_885:
	v_add_u32_e32 v34, v47, v52
	s_waitcnt lgkmcnt(0)
	s_barrier
	ds_read_b128 v[38:41], v34 offset:34816
	v_add_u32_e32 v34, v47, v53
	v_add_u32_e32 v48, v56, v52
	ds_read_b128 v[34:37], v34 offset:34816
	ds_read_b128 v[100:103], v48 offset:59904
	v_add_u32_e32 v48, v56, v53
	ds_read_b128 v[104:107], v48 offset:59904
	ds_read_b32 v48, v58 offset:1024
	s_waitcnt lgkmcnt(2)
	v_mfma_f32_16x16x32_bf16 v[100:103], v[38:41], v[100:103], 0
	v_add_u32_e32 v50, v57, v52
	ds_read_b128 v[108:111], v50
	ds_read2st64_b32 v[50:51], v58 offset1:2
	s_waitcnt lgkmcnt(3)
	v_mfma_f32_16x16x32_bf16 v[100:103], v[34:37], v[104:107], v[100:103]
	s_waitcnt lgkmcnt(1)
	v_mfma_f32_16x16x32_bf16 v[108:111], v[38:41], v[108:111], 0
	s_waitcnt lgkmcnt(0)
	s_nop 4
	v_add_f32_e32 v99, v100, v50
	v_mul_f32_e32 v99, 0xbfb8aa3b, v99
	v_exp_f32_e32 v99, v99
	v_add_u32_e32 v100, v57, v53
	ds_read_b128 v[104:107], v100
	s_waitcnt lgkmcnt(0)
	v_mfma_f32_16x16x32_bf16 v[104:107], v[34:37], v[104:107], v[108:111]
	v_add_f32_e32 v99, 1.0, v99
	v_rcp_f32_e32 v99, v99
	v_add_f32_e32 v101, v101, v50
	s_nop 4
	v_add_f32_e32 v100, v104, v51
	v_mul_f32_e32 v101, 0xbfb8aa3b, v101
	v_mul_f32_e64 v99, v99, -v48
	v_exp_f32_e32 v99, v99
	v_exp_f32_e32 v101, v101
	v_mul_f32_e32 v100, 0xbfb8aa3b, v100
	v_exp_f32_e32 v100, v100
	v_fma_f32 v104, -v99, v99, 1.0
	v_max_f32_e32 v104, 0, v104
	v_add_f32_e32 v101, 1.0, v101
	v_add_f32_e32 v100, 1.0, v100
	v_sqrt_f32_e32 v108, v104
	v_rcp_f32_e32 v100, v100
	v_add_f32_e32 v102, v102, v50
	v_mul_f32_e32 v102, 0xbfb8aa3b, v102
	v_add_u32_e32 v109, -1, v108
	v_add_u32_e32 v110, 1, v108
	v_fma_f32 v111, -v109, v108, v104
	v_fma_f32 v112, -v110, v108, v104
	v_cmp_ge_f32_e64 s[0:1], 0, v111
	v_add_f32_e32 v105, v105, v51
	v_exp_f32_e32 v102, v102
	v_cndmask_b32_e64 v108, v108, v109, s[0:1]
	v_cmp_lt_f32_e64 s[0:1], 0, v112
	v_mul_f32_e32 v105, 0xbfb8aa3b, v105
	v_exp_f32_e32 v105, v105
	v_cndmask_b32_e64 v108, v108, v110, s[0:1]
	v_rcp_f32_e32 v109, v101
	v_add_f32_e32 v102, 1.0, v102
	v_rcp_f32_e32 v102, v102
	v_mov_b32_e32 v101, v108
	v_mul_f32_e64 v108, v109, -v48
	v_exp_f32_e32 v108, v108
	v_mul_f32_e32 v104, v100, v101
	ds_read2_b32 v[100:101], v98 offset1:68
	v_mul_f32_e64 v102, v102, -v48
	v_fma_f32 v109, -v108, v108, 1.0
	v_max_f32_e32 v109, 0, v109
	s_waitcnt lgkmcnt(0)
	v_mul_f32_e32 v100, v100, v104
	v_add_f32_e32 v104, 1.0, v105
	v_sqrt_f32_e32 v110, v109
	v_exp_f32_e32 v102, v102
	v_add_f32_e32 v50, v103, v50
	v_add_f32_e32 v106, v106, v51
	v_add_u32_e32 v105, -1, v110
	v_fma_f32 v111, -v105, v110, v109
	v_cmp_ge_f32_e64 s[0:1], 0, v111
	v_add_u32_e32 v111, 1, v110
	v_mul_f32_e32 v50, 0xbfb8aa3b, v50
	v_cndmask_b32_e64 v105, v110, v105, s[0:1]
	v_fma_f32 v110, -v111, v110, v109
	v_cmp_lt_f32_e64 s[0:1], 0, v110
	v_mul_f32_e32 v106, 0xbfb8aa3b, v106
	v_exp_f32_e32 v50, v50
	v_cndmask_b32_e64 v105, v105, v111, s[0:1]
	v_rcp_f32_e32 v104, v104
	v_exp_f32_e32 v106, v106
	v_fma_f32 v109, -v102, v102, 1.0
	v_max_f32_e32 v109, 0, v109
	v_add_f32_e32 v50, 1.0, v50
	v_mul_f32_e32 v104, v104, v105
	v_sqrt_f32_e32 v110, v109
	v_add_f32_e32 v105, 1.0, v106
	v_rcp_f32_e32 v50, v50
	v_rcp_f32_e32 v105, v105
	v_add_u32_e32 v106, -1, v110
	v_fma_f32 v111, -v106, v110, v109
	v_cmp_ge_f32_e64 s[0:1], 0, v111
	v_add_u32_e32 v111, 1, v110
	v_mul_f32_e64 v48, v50, -v48
	v_cndmask_b32_e64 v106, v110, v106, s[0:1]
	v_fma_f32 v110, -v111, v110, v109
	v_cmp_lt_f32_e64 s[0:1], 0, v110
	v_exp_f32_e32 v48, v48
	v_add_f32_e32 v50, v107, v51
	v_cndmask_b32_e64 v103, v106, v111, s[0:1]
	v_mul_f32_e32 v50, 0xbfb8aa3b, v50
	v_mul_f32_e32 v100, v108, v100
	v_mul_f32_e32 v103, v105, v103
	v_exp_f32_e32 v105, v50
	v_fma_f32 v50, -v48, v48, 1.0
	v_max_f32_e32 v50, 0, v50
	v_add_f32_e32 v105, 1.0, v105
	v_rcp_f32_e32 v105, v105
	v_mov_b32_e32 v106, v50
	v_sqrt_f32_e32 v107, v106
	ds_read2_b32 v[50:51], v98 offset0:136 offset1:204
	v_fmac_f32_e32 v100, v101, v104
	v_mul_f32_e32 v99, v99, v108
	v_add_u32_e32 v109, -1, v107
	v_fma_f32 v110, -v109, v107, v106
	v_cmp_ge_f32_e64 s[0:1], 0, v110
	v_add_u32_e32 v110, 1, v107
	v_mul_f32_e32 v100, v102, v100
	v_cndmask_b32_e64 v109, v107, v109, s[0:1]
	v_fma_f32 v107, -v110, v107, v106
	v_cmp_lt_f32_e64 s[0:1], 0, v107
	v_mul_f32_e32 v99, v102, v99
	s_waitcnt lgkmcnt(0)
	v_fmac_f32_e32 v100, v50, v103
	v_cndmask_b32_e64 v107, v109, v110, s[0:1]
	v_mul_f32_e32 v99, v48, v99
	v_mul_f32_e32 v48, v48, v100
	v_mov_b32_e32 v106, v107
	v_mul_f32_e32 v105, v105, v106
	v_fmac_f32_e32 v48, v51, v105
	v_mov_b32_e32 v50, v99
	v_mov_b32_e32 v51, v99
	s_nop 1
	v_permlane16_swap_b32_e32 v50, v51
	v_cndmask_b32_e64 v51, v50, v51, s[4:5]
	v_mov_b32_e32 v100, v51
	s_nop 1
	v_permlane32_swap_b32_e32 v51, v100
	v_cndmask_b32_e64 v51, v51, v100, s[6:7]
	v_cndmask_b32_e64 v50, v50, v51, s[4:5]
	v_mov_b32_e32 v51, v48
	v_mov_b32_e32 v100, v48
	s_nop 1
	v_permlane16_swap_b32_e32 v51, v100
	v_cndmask_b32_e64 v100, v51, v100, s[4:5]
	v_mov_b32_e32 v101, v100
	s_nop 1
	v_permlane32_swap_b32_e32 v100, v101
	v_cndmask_b32_e64 v100, v100, v101, s[6:7]
	v_cndmask_b32_e64 v51, v51, v100, s[4:5]
	v_fma_f32 v51, v99, v51, v48
	v_mul_f32_e32 v50, v99, v50
	v_cndmask_b32_e64 v51, v51, v48, s[8:9]
	v_cndmask_b32_e64 v48, v50, v99, s[8:9]
	v_mov_b32_e32 v50, v48
	v_mov_b32_e32 v99, v48
	v_mov_b32_e32 v100, v51
	v_mov_b32_e32 v101, v51
	v_permlane32_swap_b32_e32 v50, v99
	s_nop 0
	v_permlane32_swap_b32_e32 v100, v101
	s_and_saveexec_b64 s[0:1], s[10:11]
	v_cndmask_b32_e64 v50, v50, v99, s[6:7]
	v_cndmask_b32_e64 v99, v100, v101, s[6:7]
	v_mul_f32_e32 v50, v48, v50
	v_fmac_f32_e32 v51, v48, v99
	ds_write_b64 v86, v[50:51] offset:51200
	s_or_b64 exec, exec, s[0:1]
	v_add_u32_e32 v48, v59, v52
	ds_read_b128 v[100:103], v48 offset:59904
	ds_read_b32 v99, v61 offset:1024
	v_add_u32_e32 v48, v60, v52
	ds_read_b128 v[104:107], v48
	v_add_u32_e32 v48, v59, v53
	ds_read_b128 v[108:111], v48 offset:59904
	s_waitcnt lgkmcnt(3)
; __device__ __forceinline__ void ph_lru(const Ptrs& P, unsigned char* lds, int mode, int item0) {
;     ...
;             for (int ct = 0; ct < 4; ++ct) {
;                 const int e = 16 * ct + fr, ky = (e >> 1) & 7;
;                 const bf16x8 wa0 = *(const bf16x8*)(wa + e * 128 + ((fq ^ ky) << 4)), wa1 = *(const bf16x8*)(wa + e * 128 + (((4 + fq) ^ ky) << 4));
;                 const bf16x8 wx0 = *(const bf16x8*)(wx + e * 128 + ((fq ^ ky) << 4)), wx1 = *(const bf16x8*)(wx + e * 128 + (((4 + fq) ^ ky) << 4));
;                 f32x4 ga = {0.f, 0.f, 0.f, 0.f}, gx = {0.f, 0.f, 0.f, 0.f};
;                 ga = __builtin_amdgcn_mfma_f32_16x16x32_bf16(af0, wa0, ga, 0, 0, 0); ga = __builtin_amdgcn_mfma_f32_16x16x32_bf16(af1, wa1, ga, 0, 0, 0);
;                 gx = __builtin_amdgcn_mfma_f32_16x16x32_bf16(af0, wx0, gx, 0, 0, 0); gx = __builtin_amdgcn_mfma_f32_16x16x32_bf16(af1, wx1, gx, 0, 0, 0);
;                 const float bav = GBL[dir * 64 + e], bxv = GBL[128 + dir * 64 + e], c8 = GBL[256 + dir * 64 + e];
; #pragma unroll
;                 for (int j = 0; j < 4; ++j) {
;                     const float r = fsigmoid(ga[j] + bav), ig = fsigmoid(gx[j] + bxv);
;                     const float a = __builtin_amdgcn_exp2f(-c8 * r);
;                     av[dir][ct][j] = a; uv[dir][ct][j] = sqrtf(fmaxf(1.f - a * a, 0.f)) * ig * X[(16 * wid + 4 * fq + j) * 68 + e];
;                 }
;                 float Al = av[dir][ct][0] * av[dir][ct][1] * av[dir][ct][2] * av[dir][ct][3], Hl;
;                 if (dir == 0) Hl = ((uv[dir][ct][0] * av[dir][ct][1] + uv[dir][ct][1]) * av[dir][ct][2] + uv[dir][ct][2]) * av[dir][ct][3] + uv[dir][ct][3];
;                 else Hl = ((uv[dir][ct][3] * av[dir][ct][2] + uv[dir][ct][2]) * av[dir][ct][1] + uv[dir][ct][1]) * av[dir][ct][0] + uv[dir][ct][0];
;                 const int pq = dir == 0 ? fq : 3 - fq;
;                 {
;                     const float Ap = lane_shift16(Al, dir == 0), Hp = lane_shift16(Hl, dir == 0);
;                     if (pq >= 1) { Hl = Al * Hp + Hl; Al = Al * Ap; }
;                 }
;                 {
;                     const float Ap = lane_xor32(Al), Hp = lane_xor32(Hl);
;                     if (pq >= 2) { Hl = Al * Hp + Hl; Al = Al * Ap; }
;                 }
;                 {
;                     const float Ap = lane_shift16(Al, dir == 0), Hp = lane_shift16(Hl, dir == 0);
	v_mfma_f32_16x16x32_bf16 v[100:103], v[38:41], v[100:103], 0
	ds_read2st64_b32 v[50:51], v61 offset1:2
	v_add_u32_e32 v48, v60, v53
	s_waitcnt lgkmcnt(1)
	v_mfma_f32_16x16x32_bf16 v[100:103], v[34:37], v[108:111], v[100:103]
	ds_read_b128 v[108:111], v48
	v_mfma_f32_16x16x32_bf16 v[104:107], v[38:41], v[104:107], 0
	s_waitcnt lgkmcnt(0)
	v_mfma_f32_16x16x32_bf16 v[104:107], v[34:37], v[108:111], v[104:107]
	s_nop 3
	v_add_f32_e32 v100, v100, v50
	v_mul_f32_e32 v100, 0xbfb8aa3b, v100
	v_exp_f32_e32 v100, v100
	v_add_f32_e32 v101, v101, v50
	v_mul_f32_e32 v101, 0xbfb8aa3b, v101
	v_exp_f32_e32 v101, v101
	v_add_f32_e32 v48, 1.0, v100
	v_rcp_f32_e32 v48, v48
	v_add_f32_e32 v100, v104, v51
	v_add_f32_e32 v101, 1.0, v101
	v_mul_f32_e32 v100, 0xbfb8aa3b, v100
	v_mul_f32_e64 v48, v48, -v99
	v_exp_f32_e32 v48, v48
	v_exp_f32_e32 v100, v100
	v_add_f32_e32 v102, v102, v50
	v_mul_f32_e32 v102, 0xbfb8aa3b, v102
	v_fma_f32 v104, -v48, v48, 1.0
	v_max_f32_e32 v104, 0, v104
	v_add_f32_e32 v100, 1.0, v100
	v_rcp_f32_e32 v100, v100
	v_sqrt_f32_e32 v108, v104
	v_add_f32_e32 v105, v105, v51
	v_exp_f32_e32 v102, v102
	v_mul_f32_e32 v105, 0xbfb8aa3b, v105
	v_add_u32_e32 v109, -1, v108
	v_add_u32_e32 v110, 1, v108
	v_fma_f32 v111, -v109, v108, v104
	v_fma_f32 v112, -v110, v108, v104
	v_cmp_ge_f32_e64 s[0:1], 0, v111
	v_exp_f32_e32 v105, v105
	v_add_f32_e32 v102, 1.0, v102
	v_cndmask_b32_e64 v108, v108, v109, s[0:1]
	v_cmp_lt_f32_e64 s[0:1], 0, v112
	v_rcp_f32_e32 v102, v102
	v_add_f32_e32 v50, v103, v50
	v_cndmask_b32_e64 v108, v108, v110, s[0:1]
	v_rcp_f32_e32 v109, v101
	v_mul_f32_e64 v102, v102, -v99
	v_exp_f32_e32 v102, v102
	v_mov_b32_e32 v101, v108
	v_mul_f32_e64 v108, v109, -v99
	v_exp_f32_e32 v108, v108
	v_mul_f32_e32 v104, v100, v101
	ds_read2_b32 v[100:101], v98 offset0:16 offset1:84
	v_add_f32_e32 v106, v106, v51
	v_fma_f32 v109, -v108, v108, 1.0
	v_max_f32_e32 v109, 0, v109
	s_waitcnt lgkmcnt(0)
	v_mul_f32_e32 v100, v100, v104
	v_add_f32_e32 v104, 1.0, v105
	v_sqrt_f32_e32 v110, v109
	v_mul_f32_e32 v50, 0xbfb8aa3b, v50
	v_mul_f32_e32 v106, 0xbfb8aa3b, v106
	v_exp_f32_e32 v50, v50
	v_add_u32_e32 v105, -1, v110
	v_fma_f32 v111, -v105, v110, v109
	v_cmp_ge_f32_e64 s[0:1], 0, v111
	v_add_u32_e32 v111, 1, v110
	v_rcp_f32_e32 v104, v104
	v_cndmask_b32_e64 v105, v110, v105, s[0:1]
	v_fma_f32 v110, -v111, v110, v109
	v_cmp_lt_f32_e64 s[0:1], 0, v110
	v_exp_f32_e32 v106, v106
	v_add_f32_e32 v50, 1.0, v50
	v_cndmask_b32_e64 v105, v105, v111, s[0:1]
	v_rcp_f32_e32 v50, v50
	v_mul_f32_e32 v100, v108, v100
	v_fma_f32 v109, -v102, v102, 1.0
	v_max_f32_e32 v109, 0, v109
	v_mul_f32_e32 v104, v104, v105
	v_add_f32_e32 v105, 1.0, v106
	v_sqrt_f32_e32 v110, v109
	v_mul_f32_e64 v50, v50, -v99
	v_rcp_f32_e32 v105, v105
	v_exp_f32_e32 v99, v50
	v_add_u32_e32 v106, -1, v110
	v_fma_f32 v111, -v106, v110, v109
	v_cmp_ge_f32_e64 s[0:1], 0, v111
	v_add_u32_e32 v111, 1, v110
	v_add_f32_e32 v50, v107, v51
	v_cndmask_b32_e64 v106, v110, v106, s[0:1]
	v_fma_f32 v110, -v111, v110, v109
	v_cmp_lt_f32_e64 s[0:1], 0, v110
	v_mul_f32_e32 v50, 0xbfb8aa3b, v50
	v_fmac_f32_e32 v100, v101, v104
	v_cndmask_b32_e64 v103, v106, v111, s[0:1]
	v_mul_f32_e32 v48, v48, v108
	v_mul_f32_e32 v100, v102, v100
	v_mul_f32_e32 v103, v105, v103
	v_exp_f32_e32 v105, v50
	v_fma_f32 v50, -v99, v99, 1.0
	v_max_f32_e32 v50, 0, v50
	v_add_f32_e32 v105, 1.0, v105
	v_rcp_f32_e32 v105, v105
	v_mov_b32_e32 v106, v50
	v_sqrt_f32_e32 v107, v106
	ds_read2_b32 v[50:51], v98 offset0:152 offset1:220
	v_mul_f32_e32 v48, v102, v48
	v_mul_f32_e32 v48, v99, v48
	v_add_u32_e32 v109, -1, v107
	v_fma_f32 v110, -v109, v107, v106
	v_cmp_ge_f32_e64 s[0:1], 0, v110
	v_add_u32_e32 v110, 1, v107
	s_waitcnt lgkmcnt(0)
	v_fmac_f32_e32 v100, v50, v103
	v_cndmask_b32_e64 v109, v107, v109, s[0:1]
	v_fma_f32 v107, -v110, v107, v106
	v_cmp_lt_f32_e64 s[0:1], 0, v107
	v_mul_f32_e32 v50, v99, v100
	v_mov_b32_e32 v99, v48
	v_cndmask_b32_e64 v107, v109, v110, s[0:1]
	v_mov_b32_e32 v106, v107
	v_mul_f32_e32 v105, v105, v106
	v_fmac_f32_e32 v50, v51, v105
	v_mov_b32_e32 v51, v48
	s_nop 1
	v_permlane16_swap_b32_e32 v51, v99
	v_cndmask_b32_e64 v99, v51, v99, s[4:5]
	v_mov_b32_e32 v100, v99
	s_nop 1
	v_permlane32_swap_b32_e32 v99, v100
	v_cndmask_b32_e64 v99, v99, v100, s[6:7]
	v_cndmask_b32_e64 v51, v51, v99, s[4:5]
	v_mov_b32_e32 v99, v50
	v_mov_b32_e32 v100, v50
	s_nop 1
	v_permlane16_swap_b32_e32 v99, v100
	v_cndmask_b32_e64 v100, v99, v100, s[4:5]
	v_mov_b32_e32 v101, v100
	s_nop 1
	v_permlane32_swap_b32_e32 v100, v101
	v_cndmask_b32_e64 v100, v100, v101, s[6:7]
	v_cndmask_b32_e64 v99, v99, v100, s[4:5]
	v_fma_f32 v99, v48, v99, v50
	v_mul_f32_e32 v100, v48, v51
	v_cndmask_b32_e64 v51, v99, v50, s[8:9]
	v_cndmask_b32_e64 v48, v100, v48, s[8:9]
	v_mov_b32_e32 v50, v48
	v_mov_b32_e32 v99, v48
	v_mov_b32_e32 v100, v51
	v_mov_b32_e32 v101, v51
	v_permlane32_swap_b32_e32 v50, v99
	s_nop 0
	v_permlane32_swap_b32_e32 v100, v101
	s_and_saveexec_b64 s[0:1], s[10:11]
	v_cndmask_b32_e64 v50, v50, v99, s[6:7]
	v_cndmask_b32_e64 v99, v100, v101, s[6:7]
	v_mul_f32_e32 v50, v48, v50
	v_fmac_f32_e32 v51, v48, v99
	ds_write_b64 v87, v[50:51] offset:51200
	s_or_b64 exec, exec, s[0:1]
	v_add_u32_e32 v48, v62, v52
	ds_read_b128 v[100:103], v48 offset:59904
	ds_read_b32 v99, v64 offset:1024
	v_add_u32_e32 v48, v63, v52
	ds_read_b128 v[104:107], v48
	v_add_u32_e32 v48, v62, v53
	ds_read_b128 v[108:111], v48 offset:59904
	s_waitcnt lgkmcnt(3)
	v_mfma_f32_16x16x32_bf16 v[100:103], v[38:41], v[100:103], 0
	ds_read2st64_b32 v[50:51], v64 offset1:2
	v_add_u32_e32 v48, v63, v53
	s_waitcnt lgkmcnt(1)
; __device__ __forceinline__ void ph_lru(const Ptrs& P, unsigned char* lds, int mode, int item0) {
;     ...
;             for (int ct = 0; ct < 4; ++ct) {
;                 const int e = 16 * ct + fr, ky = (e >> 1) & 7;
;                 const bf16x8 wa0 = *(const bf16x8*)(wa + e * 128 + ((fq ^ ky) << 4)), wa1 = *(const bf16x8*)(wa + e * 128 + (((4 + fq) ^ ky) << 4));
;                 const bf16x8 wx0 = *(const bf16x8*)(wx + e * 128 + ((fq ^ ky) << 4)), wx1 = *(const bf16x8*)(wx + e * 128 + (((4 + fq) ^ ky) << 4));
;                 f32x4 ga = {0.f, 0.f, 0.f, 0.f}, gx = {0.f, 0.f, 0.f, 0.f};
;                 ga = __builtin_amdgcn_mfma_f32_16x16x32_bf16(af0, wa0, ga, 0, 0, 0); ga = __builtin_amdgcn_mfma_f32_16x16x32_bf16(af1, wa1, ga, 0, 0, 0);
;                 gx = __builtin_amdgcn_mfma_f32_16x16x32_bf16(af0, wx0, gx, 0, 0, 0); gx = __builtin_amdgcn_mfma_f32_16x16x32_bf16(af1, wx1, gx, 0, 0, 0);
;                 const float bav = GBL[dir * 64 + e], bxv = GBL[128 + dir * 64 + e], c8 = GBL[256 + dir * 64 + e];
; #pragma unroll
;                 for (int j = 0; j < 4; ++j) {
;                     const float r = fsigmoid(ga[j] + bav), ig = fsigmoid(gx[j] + bxv);
;                     const float a = __builtin_amdgcn_exp2f(-c8 * r);
;                     av[dir][ct][j] = a; uv[dir][ct][j] = sqrtf(fmaxf(1.f - a * a, 0.f)) * ig * X[(16 * wid + 4 * fq + j) * 68 + e];
;                 }
;                 float Al = av[dir][ct][0] * av[dir][ct][1] * av[dir][ct][2] * av[dir][ct][3], Hl;
;                 if (dir == 0) Hl = ((uv[dir][ct][0] * av[dir][ct][1] + uv[dir][ct][1]) * av[dir][ct][2] + uv[dir][ct][2]) * av[dir][ct][3] + uv[dir][ct][3];
;                 else Hl = ((uv[dir][ct][3] * av[dir][ct][2] + uv[dir][ct][2]) * av[dir][ct][1] + uv[dir][ct][1]) * av[dir][ct][0] + uv[dir][ct][0];
;                 const int pq = dir == 0 ? fq : 3 - fq;
;                 {
;                     const float Ap = lane_shift16(Al, dir == 0), Hp = lane_shift16(Hl, dir == 0);
;                     if (pq >= 1) { Hl = Al * Hp + Hl; Al = Al * Ap; }
;                 }
;                 {
;                     const float Ap = lane_xor32(Al), Hp = lane_xor32(Hl);
;                     if (pq >= 2) { Hl = Al * Hp + Hl; Al = Al * Ap; }
;                 }
;                 {
;                     const float Ap = lane_shift16(Al, dir == 0), Hp = lane_shift16(Hl, dir == 0);
	v_mfma_f32_16x16x32_bf16 v[100:103], v[34:37], v[108:111], v[100:103]
	ds_read_b128 v[108:111], v48
	v_mfma_f32_16x16x32_bf16 v[104:107], v[38:41], v[104:107], 0
	s_waitcnt lgkmcnt(0)
	v_mfma_f32_16x16x32_bf16 v[104:107], v[34:37], v[108:111], v[104:107]
	s_nop 3
	v_add_f32_e32 v100, v100, v50
	v_mul_f32_e32 v100, 0xbfb8aa3b, v100
	v_exp_f32_e32 v100, v100
	v_add_f32_e32 v101, v101, v50
	v_mul_f32_e32 v101, 0xbfb8aa3b, v101
	v_exp_f32_e32 v101, v101
	v_add_f32_e32 v48, 1.0, v100
	v_rcp_f32_e32 v48, v48
	v_add_f32_e32 v100, v104, v51
	v_add_f32_e32 v101, 1.0, v101
	v_mul_f32_e32 v100, 0xbfb8aa3b, v100
	v_mul_f32_e64 v48, v48, -v99
	v_exp_f32_e32 v48, v48
	v_exp_f32_e32 v100, v100
	v_add_f32_e32 v102, v102, v50
	v_mul_f32_e32 v102, 0xbfb8aa3b, v102
	v_fma_f32 v104, -v48, v48, 1.0
	v_max_f32_e32 v104, 0, v104
	v_add_f32_e32 v100, 1.0, v100
	v_rcp_f32_e32 v100, v100
	v_sqrt_f32_e32 v108, v104
	v_add_f32_e32 v105, v105, v51
	v_exp_f32_e32 v102, v102
	v_mul_f32_e32 v105, 0xbfb8aa3b, v105
	v_add_u32_e32 v109, -1, v108
	v_add_u32_e32 v110, 1, v108
	v_fma_f32 v111, -v109, v108, v104
	v_fma_f32 v112, -v110, v108, v104
	v_cmp_ge_f32_e64 s[0:1], 0, v111
	v_exp_f32_e32 v105, v105
	v_add_f32_e32 v102, 1.0, v102
	v_cndmask_b32_e64 v108, v108, v109, s[0:1]
	v_cmp_lt_f32_e64 s[0:1], 0, v112
	v_rcp_f32_e32 v102, v102
	v_add_f32_e32 v50, v103, v50
	v_cndmask_b32_e64 v108, v108, v110, s[0:1]
	v_rcp_f32_e32 v109, v101
	v_mul_f32_e64 v102, v102, -v99
	v_exp_f32_e32 v102, v102
	v_mov_b32_e32 v101, v108
	v_mul_f32_e64 v108, v109, -v99
	v_exp_f32_e32 v108, v108
	v_mul_f32_e32 v104, v100, v101
	ds_read2_b32 v[100:101], v98 offset0:32 offset1:100
	v_add_f32_e32 v106, v106, v51
	v_fma_f32 v109, -v108, v108, 1.0
	v_max_f32_e32 v109, 0, v109
	s_waitcnt lgkmcnt(0)
	v_mul_f32_e32 v100, v100, v104
	v_add_f32_e32 v104, 1.0, v105
	v_sqrt_f32_e32 v110, v109
	v_mul_f32_e32 v50, 0xbfb8aa3b, v50
	v_mul_f32_e32 v106, 0xbfb8aa3b, v106
	v_exp_f32_e32 v50, v50
	v_add_u32_e32 v105, -1, v110
	v_fma_f32 v111, -v105, v110, v109
	v_cmp_ge_f32_e64 s[0:1], 0, v111
	v_add_u32_e32 v111, 1, v110
	v_rcp_f32_e32 v104, v104
	v_cndmask_b32_e64 v105, v110, v105, s[0:1]
	v_fma_f32 v110, -v111, v110, v109
	v_cmp_lt_f32_e64 s[0:1], 0, v110
	v_exp_f32_e32 v106, v106
	v_add_f32_e32 v50, 1.0, v50
	v_cndmask_b32_e64 v105, v105, v111, s[0:1]
	v_rcp_f32_e32 v50, v50
	v_mul_f32_e32 v100, v108, v100
	v_fma_f32 v109, -v102, v102, 1.0
	v_max_f32_e32 v109, 0, v109
	v_mul_f32_e32 v104, v104, v105
	v_add_f32_e32 v105, 1.0, v106
	v_sqrt_f32_e32 v110, v109
	v_mul_f32_e64 v50, v50, -v99
	v_rcp_f32_e32 v105, v105
	v_exp_f32_e32 v99, v50
	v_add_u32_e32 v106, -1, v110
	v_fma_f32 v111, -v106, v110, v109
	v_cmp_ge_f32_e64 s[0:1], 0, v111
	v_add_u32_e32 v111, 1, v110
	v_add_f32_e32 v50, v107, v51
	v_cndmask_b32_e64 v106, v110, v106, s[0:1]
	v_fma_f32 v110, -v111, v110, v109
	v_cmp_lt_f32_e64 s[0:1], 0, v110
	v_mul_f32_e32 v50, 0xbfb8aa3b, v50
	v_fmac_f32_e32 v100, v101, v104
	v_cndmask_b32_e64 v103, v106, v111, s[0:1]
	v_mul_f32_e32 v48, v48, v108
	v_mul_f32_e32 v100, v102, v100
	v_mul_f32_e32 v103, v105, v103
	v_exp_f32_e32 v105, v50
	v_fma_f32 v50, -v99, v99, 1.0
	v_max_f32_e32 v50, 0, v50
	v_add_f32_e32 v105, 1.0, v105
	v_rcp_f32_e32 v105, v105
	v_mov_b32_e32 v106, v50
	v_sqrt_f32_e32 v107, v106
	ds_read2_b32 v[50:51], v98 offset0:168 offset1:236
	v_mul_f32_e32 v48, v102, v48
	v_mul_f32_e32 v48, v99, v48
	v_add_u32_e32 v109, -1, v107
	v_fma_f32 v110, -v109, v107, v106
	v_cmp_ge_f32_e64 s[0:1], 0, v110
	v_add_u32_e32 v110, 1, v107
	s_waitcnt lgkmcnt(0)
	v_fmac_f32_e32 v100, v50, v103
	v_cndmask_b32_e64 v109, v107, v109, s[0:1]
	v_fma_f32 v107, -v110, v107, v106
	v_cmp_lt_f32_e64 s[0:1], 0, v107
	v_mul_f32_e32 v50, v99, v100
	v_mov_b32_e32 v99, v48
	v_cndmask_b32_e64 v107, v109, v110, s[0:1]
	v_mov_b32_e32 v106, v107
	v_mul_f32_e32 v105, v105, v106
	v_fmac_f32_e32 v50, v51, v105
	v_mov_b32_e32 v51, v48
	s_nop 1
	v_permlane16_swap_b32_e32 v51, v99
	v_cndmask_b32_e64 v99, v51, v99, s[4:5]
	v_mov_b32_e32 v100, v99
	s_nop 1
	v_permlane32_swap_b32_e32 v99, v100
	v_cndmask_b32_e64 v99, v99, v100, s[6:7]
	v_cndmask_b32_e64 v51, v51, v99, s[4:5]
	v_mov_b32_e32 v99, v50
	v_mov_b32_e32 v100, v50
	s_nop 1
	v_permlane16_swap_b32_e32 v99, v100
	v_cndmask_b32_e64 v100, v99, v100, s[4:5]
	v_mov_b32_e32 v101, v100
	s_nop 1
	v_permlane32_swap_b32_e32 v100, v101
	v_cndmask_b32_e64 v100, v100, v101, s[6:7]
	v_cndmask_b32_e64 v99, v99, v100, s[4:5]
	v_fma_f32 v99, v48, v99, v50
	v_mul_f32_e32 v100, v48, v51
	v_cndmask_b32_e64 v51, v99, v50, s[8:9]
	v_cndmask_b32_e64 v48, v100, v48, s[8:9]
	v_mov_b32_e32 v50, v48
	v_mov_b32_e32 v99, v48
	v_mov_b32_e32 v100, v51
	v_mov_b32_e32 v101, v51
	v_permlane32_swap_b32_e32 v50, v99
	s_nop 0
	v_permlane32_swap_b32_e32 v100, v101
	s_and_saveexec_b64 s[0:1], s[10:11]
	v_cndmask_b32_e64 v50, v50, v99, s[6:7]
	v_cndmask_b32_e64 v99, v100, v101, s[6:7]
	v_mul_f32_e32 v50, v48, v50
	v_fmac_f32_e32 v51, v48, v99
	ds_write_b64 v88, v[50:51] offset:51200
	s_or_b64 exec, exec, s[0:1]
	v_add_u32_e32 v48, v65, v52
	ds_read_b128 v[100:103], v48 offset:59904
	ds_read_b32 v99, v67 offset:1024
	v_add_u32_e32 v48, v66, v52
	ds_read_b128 v[104:107], v48
	v_add_u32_e32 v48, v65, v53
	ds_read_b128 v[108:111], v48 offset:59904
	s_waitcnt lgkmcnt(3)
	v_mfma_f32_16x16x32_bf16 v[100:103], v[38:41], v[100:103], 0
	ds_read2st64_b32 v[50:51], v67 offset1:2
	v_add_u32_e32 v48, v66, v53
	s_waitcnt lgkmcnt(1)
	v_mfma_f32_16x16x32_bf16 v[100:103], v[34:37], v[108:111], v[100:103]
	ds_read_b128 v[108:111], v48
	v_mfma_f32_16x16x32_bf16 v[104:107], v[38:41], v[104:107], 0
	s_waitcnt lgkmcnt(0)
; __device__ __forceinline__ void ph_lru(const Ptrs& P, unsigned char* lds, int mode, int item0) {
;     ...
;             for (int ct = 0; ct < 4; ++ct) {
;                 const int e = 16 * ct + fr, ky = (e >> 1) & 7;
;                 const bf16x8 wa0 = *(const bf16x8*)(wa + e * 128 + ((fq ^ ky) << 4)), wa1 = *(const bf16x8*)(wa + e * 128 + (((4 + fq) ^ ky) << 4));
;                 const bf16x8 wx0 = *(const bf16x8*)(wx + e * 128 + ((fq ^ ky) << 4)), wx1 = *(const bf16x8*)(wx + e * 128 + (((4 + fq) ^ ky) << 4));
;                 f32x4 ga = {0.f, 0.f, 0.f, 0.f}, gx = {0.f, 0.f, 0.f, 0.f};
;                 ga = __builtin_amdgcn_mfma_f32_16x16x32_bf16(af0, wa0, ga, 0, 0, 0); ga = __builtin_amdgcn_mfma_f32_16x16x32_bf16(af1, wa1, ga, 0, 0, 0);
;                 gx = __builtin_amdgcn_mfma_f32_16x16x32_bf16(af0, wx0, gx, 0, 0, 0); gx = __builtin_amdgcn_mfma_f32_16x16x32_bf16(af1, wx1, gx, 0, 0, 0);
;                 const float bav = GBL[dir * 64 + e], bxv = GBL[128 + dir * 64 + e], c8 = GBL[256 + dir * 64 + e];
; #pragma unroll
;                 for (int j = 0; j < 4; ++j) {
;                     const float r = fsigmoid(ga[j] + bav), ig = fsigmoid(gx[j] + bxv);
;                     const float a = __builtin_amdgcn_exp2f(-c8 * r);
;                     av[dir][ct][j] = a; uv[dir][ct][j] = sqrtf(fmaxf(1.f - a * a, 0.f)) * ig * X[(16 * wid + 4 * fq + j) * 68 + e];
;                 }
;                 float Al = av[dir][ct][0] * av[dir][ct][1] * av[dir][ct][2] * av[dir][ct][3], Hl;
;                 if (dir == 0) Hl = ((uv[dir][ct][0] * av[dir][ct][1] + uv[dir][ct][1]) * av[dir][ct][2] + uv[dir][ct][2]) * av[dir][ct][3] + uv[dir][ct][3];
;                 else Hl = ((uv[dir][ct][3] * av[dir][ct][2] + uv[dir][ct][2]) * av[dir][ct][1] + uv[dir][ct][1]) * av[dir][ct][0] + uv[dir][ct][0];
;                 const int pq = dir == 0 ? fq : 3 - fq;
;                 {
;                     const float Ap = lane_shift16(Al, dir == 0), Hp = lane_shift16(Hl, dir == 0);
;                     if (pq >= 1) { Hl = Al * Hp + Hl; Al = Al * Ap; }
;                 }
;                 {
;                     const float Ap = lane_xor32(Al), Hp = lane_xor32(Hl);
;                     if (pq >= 2) { Hl = Al * Hp + Hl; Al = Al * Ap; }
;                 }
;                 {
;                     const float Ap = lane_shift16(Al, dir == 0), Hp = lane_shift16(Hl, dir == 0);
	v_mfma_f32_16x16x32_bf16 v[104:107], v[34:37], v[108:111], v[104:107]
	s_nop 3
	v_add_f32_e32 v100, v100, v50
	v_mul_f32_e32 v100, 0xbfb8aa3b, v100
	v_exp_f32_e32 v100, v100
	v_add_f32_e32 v101, v101, v50
	v_mul_f32_e32 v101, 0xbfb8aa3b, v101
	v_exp_f32_e32 v101, v101
	v_add_f32_e32 v48, 1.0, v100
	v_rcp_f32_e32 v48, v48
	v_add_f32_e32 v100, v104, v51
	v_add_f32_e32 v101, 1.0, v101
	v_mul_f32_e32 v100, 0xbfb8aa3b, v100
	v_mul_f32_e64 v48, v48, -v99
	v_exp_f32_e32 v48, v48
	v_exp_f32_e32 v100, v100
	v_add_f32_e32 v102, v102, v50
	v_mul_f32_e32 v102, 0xbfb8aa3b, v102
	v_fma_f32 v104, -v48, v48, 1.0
	v_max_f32_e32 v104, 0, v104
	v_add_f32_e32 v100, 1.0, v100
	v_rcp_f32_e32 v100, v100
	v_sqrt_f32_e32 v108, v104
	v_add_f32_e32 v105, v105, v51
	v_exp_f32_e32 v102, v102
	v_mul_f32_e32 v105, 0xbfb8aa3b, v105
	v_add_u32_e32 v109, -1, v108
	v_add_u32_e32 v110, 1, v108
	v_fma_f32 v111, -v109, v108, v104
	v_fma_f32 v112, -v110, v108, v104
	v_cmp_ge_f32_e64 s[0:1], 0, v111
	v_exp_f32_e32 v105, v105
	v_add_f32_e32 v102, 1.0, v102
	v_cndmask_b32_e64 v108, v108, v109, s[0:1]
	v_cmp_lt_f32_e64 s[0:1], 0, v112
	v_rcp_f32_e32 v102, v102
	v_add_f32_e32 v50, v103, v50
	v_cndmask_b32_e64 v108, v108, v110, s[0:1]
	v_rcp_f32_e32 v109, v101
	v_mul_f32_e64 v102, v102, -v99
	v_exp_f32_e32 v102, v102
	v_mov_b32_e32 v101, v108
	v_mul_f32_e64 v108, v109, -v99
	v_exp_f32_e32 v108, v108
	v_mul_f32_e32 v104, v100, v101
	ds_read2_b32 v[100:101], v98 offset0:48 offset1:116
	v_add_f32_e32 v106, v106, v51
	v_fma_f32 v109, -v108, v108, 1.0
	v_max_f32_e32 v109, 0, v109
	s_waitcnt lgkmcnt(0)
	v_mul_f32_e32 v100, v100, v104
	v_add_f32_e32 v104, 1.0, v105
	v_sqrt_f32_e32 v110, v109
	v_mul_f32_e32 v50, 0xbfb8aa3b, v50
	v_mul_f32_e32 v106, 0xbfb8aa3b, v106
	v_exp_f32_e32 v50, v50
	v_add_u32_e32 v105, -1, v110
	v_fma_f32 v111, -v105, v110, v109
	v_cmp_ge_f32_e64 s[0:1], 0, v111
	v_add_u32_e32 v111, 1, v110
	v_rcp_f32_e32 v104, v104
	v_cndmask_b32_e64 v105, v110, v105, s[0:1]
	v_fma_f32 v110, -v111, v110, v109
	v_cmp_lt_f32_e64 s[0:1], 0, v110
	v_exp_f32_e32 v106, v106
	v_add_f32_e32 v50, 1.0, v50
	v_cndmask_b32_e64 v105, v105, v111, s[0:1]
	v_rcp_f32_e32 v50, v50
	v_mul_f32_e32 v100, v108, v100
	v_fma_f32 v109, -v102, v102, 1.0
	v_max_f32_e32 v109, 0, v109
	v_mul_f32_e32 v104, v104, v105
	v_add_f32_e32 v105, 1.0, v106
	v_sqrt_f32_e32 v110, v109
	v_mul_f32_e64 v50, v50, -v99
	v_rcp_f32_e32 v105, v105
	v_exp_f32_e32 v99, v50
	v_add_u32_e32 v106, -1, v110
	v_fma_f32 v111, -v106, v110, v109
	v_cmp_ge_f32_e64 s[0:1], 0, v111
	v_add_u32_e32 v111, 1, v110
	v_add_f32_e32 v50, v107, v51
	v_cndmask_b32_e64 v106, v110, v106, s[0:1]
	v_fma_f32 v110, -v111, v110, v109
	v_cmp_lt_f32_e64 s[0:1], 0, v110
	v_mul_f32_e32 v50, 0xbfb8aa3b, v50
	v_fmac_f32_e32 v100, v101, v104
	v_cndmask_b32_e64 v103, v106, v111, s[0:1]
	v_mul_f32_e32 v48, v48, v108
	v_mul_f32_e32 v100, v102, v100
	v_mul_f32_e32 v103, v105, v103
	v_exp_f32_e32 v105, v50
	v_fma_f32 v50, -v99, v99, 1.0
	v_max_f32_e32 v50, 0, v50
	v_add_f32_e32 v105, 1.0, v105
	v_rcp_f32_e32 v105, v105
	v_mov_b32_e32 v106, v50
	v_sqrt_f32_e32 v107, v106
	ds_read2_b32 v[50:51], v98 offset0:184 offset1:252
	v_mul_f32_e32 v48, v102, v48
	v_mul_f32_e32 v48, v99, v48
	v_add_u32_e32 v109, -1, v107
	v_fma_f32 v110, -v109, v107, v106
	v_cmp_ge_f32_e64 s[0:1], 0, v110
	v_add_u32_e32 v110, 1, v107
	s_waitcnt lgkmcnt(0)
	v_fmac_f32_e32 v100, v50, v103
	v_cndmask_b32_e64 v109, v107, v109, s[0:1]
	v_fma_f32 v107, -v110, v107, v106
	v_cmp_lt_f32_e64 s[0:1], 0, v107
	v_mul_f32_e32 v50, v99, v100
	v_mov_b32_e32 v99, v48
	v_cndmask_b32_e64 v107, v109, v110, s[0:1]
	v_mov_b32_e32 v106, v107
	v_mul_f32_e32 v105, v105, v106
	v_fmac_f32_e32 v50, v51, v105
	v_mov_b32_e32 v51, v48
	s_nop 1
	v_permlane16_swap_b32_e32 v51, v99
	v_cndmask_b32_e64 v99, v51, v99, s[4:5]
	v_mov_b32_e32 v100, v99
	s_nop 1
	v_permlane32_swap_b32_e32 v99, v100
	v_cndmask_b32_e64 v99, v99, v100, s[6:7]
	v_cndmask_b32_e64 v51, v51, v99, s[4:5]
	v_mov_b32_e32 v99, v50
	v_mov_b32_e32 v100, v50
	s_nop 1
	v_permlane16_swap_b32_e32 v99, v100
	v_cndmask_b32_e64 v100, v99, v100, s[4:5]
	v_mov_b32_e32 v101, v100
	s_nop 1
	v_permlane32_swap_b32_e32 v100, v101
	v_cndmask_b32_e64 v100, v100, v101, s[6:7]
	v_cndmask_b32_e64 v99, v99, v100, s[4:5]
	v_fma_f32 v99, v48, v99, v50
	v_mul_f32_e32 v100, v48, v51
	v_cndmask_b32_e64 v51, v99, v50, s[8:9]
	v_cndmask_b32_e64 v48, v100, v48, s[8:9]
	v_mov_b32_e32 v50, v48
	v_mov_b32_e32 v99, v48
	v_mov_b32_e32 v100, v51
	v_mov_b32_e32 v101, v51
	v_permlane32_swap_b32_e32 v50, v99
	s_nop 0
	v_permlane32_swap_b32_e32 v100, v101
	s_and_saveexec_b64 s[0:1], s[10:11]
	v_cndmask_b32_e64 v50, v50, v99, s[6:7]
	v_cndmask_b32_e64 v99, v100, v101, s[6:7]
	v_mul_f32_e32 v50, v48, v50
	v_fmac_f32_e32 v51, v48, v99
	ds_write_b64 v89, v[50:51] offset:51200
	s_or_b64 exec, exec, s[0:1]
	v_add_u32_e32 v48, v68, v52
	ds_read_b128 v[100:103], v48
	ds_read_b32 v99, v70 offset:1024
	v_add_u32_e32 v48, v69, v52
	ds_read_b128 v[104:107], v48
	v_add_u32_e32 v48, v68, v53
	ds_read_b128 v[108:111], v48
	s_waitcnt lgkmcnt(3)
	v_mfma_f32_16x16x32_bf16 v[100:103], v[38:41], v[100:103], 0
	ds_read2st64_b32 v[50:51], v70 offset1:2
	v_add_u32_e32 v48, v69, v53
	s_waitcnt lgkmcnt(1)
	v_mfma_f32_16x16x32_bf16 v[100:103], v[34:37], v[108:111], v[100:103]
	ds_read_b128 v[108:111], v48
	v_mfma_f32_16x16x32_bf16 v[104:107], v[38:41], v[104:107], 0
	s_waitcnt lgkmcnt(0)
; __device__ __forceinline__ void ph_lru(const Ptrs& P, unsigned char* lds, int mode, int item0) {
;     ...
;             for (int ct = 0; ct < 4; ++ct) {
;                 const int e = 16 * ct + fr, ky = (e >> 1) & 7;
;                 const bf16x8 wa0 = *(const bf16x8*)(wa + e * 128 + ((fq ^ ky) << 4)), wa1 = *(const bf16x8*)(wa + e * 128 + (((4 + fq) ^ ky) << 4));
;                 const bf16x8 wx0 = *(const bf16x8*)(wx + e * 128 + ((fq ^ ky) << 4)), wx1 = *(const bf16x8*)(wx + e * 128 + (((4 + fq) ^ ky) << 4));
;                 f32x4 ga = {0.f, 0.f, 0.f, 0.f}, gx = {0.f, 0.f, 0.f, 0.f};
;                 ga = __builtin_amdgcn_mfma_f32_16x16x32_bf16(af0, wa0, ga, 0, 0, 0); ga = __builtin_amdgcn_mfma_f32_16x16x32_bf16(af1, wa1, ga, 0, 0, 0);
;                 gx = __builtin_amdgcn_mfma_f32_16x16x32_bf16(af0, wx0, gx, 0, 0, 0); gx = __builtin_amdgcn_mfma_f32_16x16x32_bf16(af1, wx1, gx, 0, 0, 0);
;                 const float bav = GBL[dir * 64 + e], bxv = GBL[128 + dir * 64 + e], c8 = GBL[256 + dir * 64 + e];
; #pragma unroll
;                 for (int j = 0; j < 4; ++j) {
;                     const float r = fsigmoid(ga[j] + bav), ig = fsigmoid(gx[j] + bxv);
;                     const float a = __builtin_amdgcn_exp2f(-c8 * r);
;                     av[dir][ct][j] = a; uv[dir][ct][j] = sqrtf(fmaxf(1.f - a * a, 0.f)) * ig * X[(16 * wid + 4 * fq + j) * 68 + e];
;                 }
;                 float Al = av[dir][ct][0] * av[dir][ct][1] * av[dir][ct][2] * av[dir][ct][3], Hl;
;                 if (dir == 0) Hl = ((uv[dir][ct][0] * av[dir][ct][1] + uv[dir][ct][1]) * av[dir][ct][2] + uv[dir][ct][2]) * av[dir][ct][3] + uv[dir][ct][3];
;                 else Hl = ((uv[dir][ct][3] * av[dir][ct][2] + uv[dir][ct][2]) * av[dir][ct][1] + uv[dir][ct][1]) * av[dir][ct][0] + uv[dir][ct][0];
;                 const int pq = dir == 0 ? fq : 3 - fq;
;                 {
;                     const float Ap = lane_shift16(Al, dir == 0), Hp = lane_shift16(Hl, dir == 0);
;                     if (pq >= 1) { Hl = Al * Hp + Hl; Al = Al * Ap; }
;                 }
;                 {
;                     const float Ap = lane_xor32(Al), Hp = lane_xor32(Hl);
;                     if (pq >= 2) { Hl = Al * Hp + Hl; Al = Al * Ap; }
;                 }
;                 {
;                     const float Ap = lane_shift16(Al, dir == 0), Hp = lane_shift16(Hl, dir == 0);
	v_mfma_f32_16x16x32_bf16 v[104:107], v[34:37], v[108:111], v[104:107]
	s_nop 3
	v_add_f32_e32 v100, v100, v50
	v_mul_f32_e32 v100, 0xbfb8aa3b, v100
	v_exp_f32_e32 v100, v100
	v_add_f32_e32 v101, v101, v50
	v_mul_f32_e32 v101, 0xbfb8aa3b, v101
	v_exp_f32_e32 v101, v101
	v_add_f32_e32 v48, 1.0, v100
	v_rcp_f32_e32 v48, v48
	v_add_f32_e32 v100, v104, v51
	v_mul_f32_e32 v100, 0xbfb8aa3b, v100
	v_exp_f32_e32 v100, v100
	v_mul_f32_e64 v48, v48, -v99
	v_exp_f32_e32 v48, v48
	v_add_f32_e32 v101, 1.0, v101
	v_add_f32_e32 v100, 1.0, v100
	v_rcp_f32_e32 v100, v100
	v_fma_f32 v104, -v48, v48, 1.0
	v_max_f32_e32 v104, 0, v104
	v_rcp_f32_e32 v101, v101
	v_add_f32_e32 v102, v102, v50
	v_sqrt_f32_e32 v108, v104
	v_mul_f32_e32 v102, 0xbfb8aa3b, v102
	v_exp_f32_e32 v102, v102
	v_add_f32_e32 v50, v103, v50
	v_add_u32_e32 v109, -1, v108
	v_add_u32_e32 v110, 1, v108
	v_fma_f32 v111, -v109, v108, v104
	v_fma_f32 v112, -v110, v108, v104
	v_cmp_ge_f32_e64 s[0:1], 0, v111
	v_add_f32_e32 v102, 1.0, v102
	v_rcp_f32_e32 v102, v102
	v_cndmask_b32_e64 v108, v108, v109, s[0:1]
	v_cmp_lt_f32_e64 s[0:1], 0, v112
	v_mul_f32_e32 v50, 0xbfb8aa3b, v50
	v_mul_f32_e64 v102, v102, -v99
	v_cndmask_b32_e64 v108, v108, v110, s[0:1]
	v_exp_f32_e32 v102, v102
	v_exp_f32_e32 v50, v50
	v_mov_b32_e32 v104, v108
	v_mul_f32_e32 v104, v100, v104
	v_mul_f32_e64 v100, v101, -v99
	v_exp_f32_e32 v108, v100
	v_add_f32_e32 v100, v105, v51
	v_mul_f32_e32 v100, 0xbfb8aa3b, v100
	v_exp_f32_e32 v105, v100
	v_fma_f32 v100, -v108, v108, 1.0
	v_max_f32_e32 v100, 0, v100
	v_add_f32_e32 v105, 1.0, v105
	v_rcp_f32_e32 v105, v105
	v_mov_b32_e32 v109, v100
	v_sqrt_f32_e32 v110, v109
	v_add_f32_e32 v106, v106, v51
	v_mul_f32_e32 v106, 0xbfb8aa3b, v106
	v_add_f32_e32 v50, 1.0, v50
	v_add_u32_e32 v111, -1, v110
	v_fma_f32 v112, -v111, v110, v109
	v_cmp_ge_f32_e64 s[0:1], 0, v112
	v_add_u32_e32 v112, 1, v110
	v_exp_f32_e32 v106, v106
	v_cndmask_b32_e64 v111, v110, v111, s[0:1]
	v_fma_f32 v110, -v112, v110, v109
	v_cmp_lt_f32_e64 s[0:1], 0, v110
	v_rcp_f32_e32 v50, v50
	v_add_f32_e32 v106, 1.0, v106
	v_cndmask_b32_e64 v110, v111, v112, s[0:1]
	v_mul_f32_e64 v50, v50, -v99
	v_rcp_f32_e32 v106, v106
	v_mov_b32_e32 v109, v110
	v_fma_f32 v110, -v102, v102, 1.0
	v_max_f32_e32 v110, 0, v110
	v_mul_f32_e32 v105, v105, v109
	v_exp_f32_e32 v99, v50
	v_sqrt_f32_e32 v111, v110
	v_add_f32_e32 v50, v107, v51
	v_mul_f32_e32 v50, 0xbfb8aa3b, v50
	ds_read2_b32 v[100:101], v98 offset1:68
	v_add_u32_e32 v109, -1, v111
	v_fma_f32 v112, -v109, v111, v110
	v_cmp_ge_f32_e64 s[0:1], 0, v112
	v_add_u32_e32 v112, 1, v111
	s_nop 0
	v_cndmask_b32_e64 v109, v111, v109, s[0:1]
	v_fma_f32 v111, -v112, v111, v110
	v_cmp_lt_f32_e64 s[0:1], 0, v111
	s_nop 1
	v_cndmask_b32_e64 v103, v109, v112, s[0:1]
	v_mul_f32_e32 v103, v106, v103
	v_exp_f32_e32 v106, v50
	v_fma_f32 v50, -v99, v99, 1.0
	v_max_f32_e32 v50, 0, v50
	v_add_f32_e32 v106, 1.0, v106
	v_rcp_f32_e32 v106, v106
	v_mov_b32_e32 v107, v50
	v_sqrt_f32_e32 v109, v107
	ds_read2_b32 v[50:51], v98 offset0:136 offset1:204
	v_add_u32_e32 v110, -1, v109
	v_fma_f32 v111, -v110, v109, v107
	v_cmp_ge_f32_e64 s[0:1], 0, v111
	v_add_u32_e32 v111, 1, v109
	s_nop 0
	v_cndmask_b32_e64 v110, v109, v110, s[0:1]
	v_fma_f32 v109, -v111, v109, v107
	v_cmp_lt_f32_e64 s[0:1], 0, v109
	s_nop 1
	v_cndmask_b32_e64 v109, v110, v111, s[0:1]
	v_mov_b32_e32 v107, v109
	v_mul_f32_e32 v106, v106, v107
	s_waitcnt lgkmcnt(0)
	v_mul_f32_e32 v51, v51, v106
	v_mul_f32_e32 v51, v102, v51
	v_mul_f32_e32 v106, v48, v108
	v_fmac_f32_e32 v51, v50, v103
	v_mul_f32_e32 v106, v102, v106
	v_mul_f32_e32 v50, v108, v51
	v_mul_f32_e32 v99, v99, v106
	v_fmac_f32_e32 v50, v101, v105
	v_mul_f32_e32 v48, v48, v50
	v_mov_b32_e32 v50, v99
	v_mov_b32_e32 v51, v99
	s_nop 1
	v_permlane16_swap_b32_e32 v50, v51
	v_cndmask_b32_e64 v50, v50, v51, s[4:5]
	v_fmac_f32_e32 v48, v100, v104
	v_mov_b32_e32 v100, v50
	s_nop 1
	v_permlane32_swap_b32_e32 v50, v100
	v_cndmask_b32_e64 v50, v50, v100, s[6:7]
	v_cndmask_b32_e64 v50, v50, v51, s[4:5]
	v_mov_b32_e32 v51, v48
	v_mov_b32_e32 v100, v48
	s_nop 1
	v_permlane16_swap_b32_e32 v51, v100
	v_cndmask_b32_e64 v51, v51, v100, s[4:5]
	v_mov_b32_e32 v101, v51
	s_nop 1
	v_permlane32_swap_b32_e32 v51, v101
	v_cndmask_b32_e64 v51, v51, v101, s[6:7]
	v_cndmask_b32_e64 v51, v51, v100, s[4:5]
	v_fma_f32 v51, v99, v51, v48
	v_mul_f32_e32 v50, v99, v50
	v_cndmask_b32_e64 v51, v51, v48, s[10:11]
	v_cndmask_b32_e64 v48, v50, v99, s[10:11]
	v_mov_b32_e32 v50, v48
	v_mov_b32_e32 v99, v48
	v_mov_b32_e32 v100, v51
	v_mov_b32_e32 v101, v51
	v_permlane32_swap_b32_e32 v50, v99
	s_nop 0
	v_permlane32_swap_b32_e32 v100, v101
	s_and_saveexec_b64 s[0:1], s[8:9]
	v_cndmask_b32_e64 v50, v50, v99, s[6:7]
	v_cndmask_b32_e64 v99, v100, v101, s[6:7]
	v_mul_f32_e32 v50, v48, v50
	v_fmac_f32_e32 v51, v48, v99
	ds_write_b64 v90, v[50:51] offset:51200
	s_or_b64 exec, exec, s[0:1]
	v_add_u32_e32 v48, v71, v52
	ds_read_b128 v[100:103], v48
	ds_read_b32 v99, v73 offset:1024
	v_add_u32_e32 v48, v72, v52
	ds_read_b128 v[104:107], v48
	v_add_u32_e32 v48, v71, v53
	ds_read_b128 v[108:111], v48
	s_waitcnt lgkmcnt(3)
	v_mfma_f32_16x16x32_bf16 v[100:103], v[38:41], v[100:103], 0
	ds_read2st64_b32 v[50:51], v73 offset1:2
	v_add_u32_e32 v48, v72, v53
	s_waitcnt lgkmcnt(1)
	v_mfma_f32_16x16x32_bf16 v[100:103], v[34:37], v[108:111], v[100:103]
	ds_read_b128 v[108:111], v48
	v_mfma_f32_16x16x32_bf16 v[104:107], v[38:41], v[104:107], 0
	s_waitcnt lgkmcnt(0)
; __device__ __forceinline__ void ph_lru(const Ptrs& P, unsigned char* lds, int mode, int item0) {
;     ...
;             for (int ct = 0; ct < 4; ++ct) {
;                 const int e = 16 * ct + fr, ky = (e >> 1) & 7;
;                 const bf16x8 wa0 = *(const bf16x8*)(wa + e * 128 + ((fq ^ ky) << 4)), wa1 = *(const bf16x8*)(wa + e * 128 + (((4 + fq) ^ ky) << 4));
;                 const bf16x8 wx0 = *(const bf16x8*)(wx + e * 128 + ((fq ^ ky) << 4)), wx1 = *(const bf16x8*)(wx + e * 128 + (((4 + fq) ^ ky) << 4));
;                 f32x4 ga = {0.f, 0.f, 0.f, 0.f}, gx = {0.f, 0.f, 0.f, 0.f};
;                 ga = __builtin_amdgcn_mfma_f32_16x16x32_bf16(af0, wa0, ga, 0, 0, 0); ga = __builtin_amdgcn_mfma_f32_16x16x32_bf16(af1, wa1, ga, 0, 0, 0);
;                 gx = __builtin_amdgcn_mfma_f32_16x16x32_bf16(af0, wx0, gx, 0, 0, 0); gx = __builtin_amdgcn_mfma_f32_16x16x32_bf16(af1, wx1, gx, 0, 0, 0);
;                 const float bav = GBL[dir * 64 + e], bxv = GBL[128 + dir * 64 + e], c8 = GBL[256 + dir * 64 + e];
; #pragma unroll
;                 for (int j = 0; j < 4; ++j) {
;                     const float r = fsigmoid(ga[j] + bav), ig = fsigmoid(gx[j] + bxv);
;                     const float a = __builtin_amdgcn_exp2f(-c8 * r);
;                     av[dir][ct][j] = a; uv[dir][ct][j] = sqrtf(fmaxf(1.f - a * a, 0.f)) * ig * X[(16 * wid + 4 * fq + j) * 68 + e];
;                 }
;                 float Al = av[dir][ct][0] * av[dir][ct][1] * av[dir][ct][2] * av[dir][ct][3], Hl;
;                 if (dir == 0) Hl = ((uv[dir][ct][0] * av[dir][ct][1] + uv[dir][ct][1]) * av[dir][ct][2] + uv[dir][ct][2]) * av[dir][ct][3] + uv[dir][ct][3];
;                 else Hl = ((uv[dir][ct][3] * av[dir][ct][2] + uv[dir][ct][2]) * av[dir][ct][1] + uv[dir][ct][1]) * av[dir][ct][0] + uv[dir][ct][0];
;                 const int pq = dir == 0 ? fq : 3 - fq;
;                 {
;                     const float Ap = lane_shift16(Al, dir == 0), Hp = lane_shift16(Hl, dir == 0);
;                     if (pq >= 1) { Hl = Al * Hp + Hl; Al = Al * Ap; }
;                 }
;                 {
;                     const float Ap = lane_xor32(Al), Hp = lane_xor32(Hl);
;                     if (pq >= 2) { Hl = Al * Hp + Hl; Al = Al * Ap; }
;                 }
;                 {
;                     const float Ap = lane_shift16(Al, dir == 0), Hp = lane_shift16(Hl, dir == 0);
	v_mfma_f32_16x16x32_bf16 v[104:107], v[34:37], v[108:111], v[104:107]
	s_nop 3
	v_add_f32_e32 v100, v100, v50
	v_mul_f32_e32 v100, 0xbfb8aa3b, v100
	v_exp_f32_e32 v100, v100
	v_add_f32_e32 v101, v101, v50
	v_mul_f32_e32 v101, 0xbfb8aa3b, v101
	v_exp_f32_e32 v101, v101
	v_add_f32_e32 v48, 1.0, v100
	v_rcp_f32_e32 v48, v48
	v_add_f32_e32 v100, v104, v51
	v_mul_f32_e32 v100, 0xbfb8aa3b, v100
	v_exp_f32_e32 v100, v100
	v_mul_f32_e64 v48, v48, -v99
	v_exp_f32_e32 v48, v48
	v_add_f32_e32 v101, 1.0, v101
	v_add_f32_e32 v100, 1.0, v100
	v_rcp_f32_e32 v100, v100
	v_fma_f32 v104, -v48, v48, 1.0
	v_max_f32_e32 v104, 0, v104
	v_rcp_f32_e32 v101, v101
	v_add_f32_e32 v102, v102, v50
	v_sqrt_f32_e32 v108, v104
	v_mul_f32_e32 v102, 0xbfb8aa3b, v102
	v_exp_f32_e32 v102, v102
	v_add_f32_e32 v50, v103, v50
	v_add_u32_e32 v109, -1, v108
	v_add_u32_e32 v110, 1, v108
	v_fma_f32 v111, -v109, v108, v104
	v_fma_f32 v112, -v110, v108, v104
	v_cmp_ge_f32_e64 s[0:1], 0, v111
	v_add_f32_e32 v102, 1.0, v102
	v_rcp_f32_e32 v102, v102
	v_cndmask_b32_e64 v108, v108, v109, s[0:1]
	v_cmp_lt_f32_e64 s[0:1], 0, v112
	v_mul_f32_e32 v50, 0xbfb8aa3b, v50
	v_mul_f32_e64 v102, v102, -v99
	v_cndmask_b32_e64 v108, v108, v110, s[0:1]
	v_exp_f32_e32 v102, v102
	v_exp_f32_e32 v50, v50
	v_mov_b32_e32 v104, v108
	v_mul_f32_e32 v104, v100, v104
	v_mul_f32_e64 v100, v101, -v99
	v_exp_f32_e32 v108, v100
	v_add_f32_e32 v100, v105, v51
	v_mul_f32_e32 v100, 0xbfb8aa3b, v100
	v_exp_f32_e32 v105, v100
	v_fma_f32 v100, -v108, v108, 1.0
	v_max_f32_e32 v100, 0, v100
	v_add_f32_e32 v105, 1.0, v105
	v_rcp_f32_e32 v105, v105
	v_mov_b32_e32 v109, v100
	v_sqrt_f32_e32 v110, v109
	v_add_f32_e32 v106, v106, v51
	v_mul_f32_e32 v106, 0xbfb8aa3b, v106
	v_add_f32_e32 v50, 1.0, v50
	v_add_u32_e32 v111, -1, v110
	v_fma_f32 v112, -v111, v110, v109
	v_cmp_ge_f32_e64 s[0:1], 0, v112
	v_add_u32_e32 v112, 1, v110
	v_exp_f32_e32 v106, v106
	v_cndmask_b32_e64 v111, v110, v111, s[0:1]
	v_fma_f32 v110, -v112, v110, v109
	v_cmp_lt_f32_e64 s[0:1], 0, v110
	v_rcp_f32_e32 v50, v50
	v_add_f32_e32 v106, 1.0, v106
	v_cndmask_b32_e64 v110, v111, v112, s[0:1]
	v_mul_f32_e64 v50, v50, -v99
	v_rcp_f32_e32 v106, v106
	v_mov_b32_e32 v109, v110
	v_fma_f32 v110, -v102, v102, 1.0
	v_max_f32_e32 v110, 0, v110
	v_mul_f32_e32 v105, v105, v109
	v_exp_f32_e32 v99, v50
	v_sqrt_f32_e32 v111, v110
	v_add_f32_e32 v50, v107, v51
	v_mul_f32_e32 v50, 0xbfb8aa3b, v50
	ds_read2_b32 v[100:101], v98 offset0:16 offset1:84
	v_add_u32_e32 v109, -1, v111
	v_fma_f32 v112, -v109, v111, v110
	v_cmp_ge_f32_e64 s[0:1], 0, v112
	v_add_u32_e32 v112, 1, v111
	s_nop 0
	v_cndmask_b32_e64 v109, v111, v109, s[0:1]
	v_fma_f32 v111, -v112, v111, v110
	v_cmp_lt_f32_e64 s[0:1], 0, v111
	s_nop 1
	v_cndmask_b32_e64 v103, v109, v112, s[0:1]
	v_mul_f32_e32 v103, v106, v103
	v_exp_f32_e32 v106, v50
	v_fma_f32 v50, -v99, v99, 1.0
	v_max_f32_e32 v50, 0, v50
	v_add_f32_e32 v106, 1.0, v106
	v_rcp_f32_e32 v106, v106
	v_mov_b32_e32 v107, v50
	v_sqrt_f32_e32 v109, v107
	ds_read2_b32 v[50:51], v98 offset0:152 offset1:220
	v_add_u32_e32 v110, -1, v109
	v_fma_f32 v111, -v110, v109, v107
	v_cmp_ge_f32_e64 s[0:1], 0, v111
	v_add_u32_e32 v111, 1, v109
	s_nop 0
	v_cndmask_b32_e64 v110, v109, v110, s[0:1]
	v_fma_f32 v109, -v111, v109, v107
	v_cmp_lt_f32_e64 s[0:1], 0, v109
	s_nop 1
	v_cndmask_b32_e64 v109, v110, v111, s[0:1]
	v_mov_b32_e32 v107, v109
	v_mul_f32_e32 v106, v106, v107
	s_waitcnt lgkmcnt(0)
	v_mul_f32_e32 v51, v51, v106
	v_mul_f32_e32 v51, v102, v51
	v_mul_f32_e32 v106, v48, v108
	v_fmac_f32_e32 v51, v50, v103
	v_mul_f32_e32 v106, v102, v106
	v_mul_f32_e32 v50, v108, v51
	v_mul_f32_e32 v99, v99, v106
	v_fmac_f32_e32 v50, v101, v105
	v_mul_f32_e32 v48, v48, v50
	v_mov_b32_e32 v50, v99
	v_mov_b32_e32 v51, v99
	s_nop 1
	v_permlane16_swap_b32_e32 v50, v51
	v_cndmask_b32_e64 v50, v50, v51, s[4:5]
	v_fmac_f32_e32 v48, v100, v104
	v_mov_b32_e32 v100, v50
	s_nop 1
	v_permlane32_swap_b32_e32 v50, v100
	v_cndmask_b32_e64 v50, v50, v100, s[6:7]
	v_cndmask_b32_e64 v50, v50, v51, s[4:5]
	v_mov_b32_e32 v51, v48
	v_mov_b32_e32 v100, v48
	s_nop 1
	v_permlane16_swap_b32_e32 v51, v100
	v_cndmask_b32_e64 v51, v51, v100, s[4:5]
	v_mov_b32_e32 v101, v51
	s_nop 1
	v_permlane32_swap_b32_e32 v51, v101
	v_cndmask_b32_e64 v51, v51, v101, s[6:7]
	v_cndmask_b32_e64 v51, v51, v100, s[4:5]
	v_fma_f32 v51, v99, v51, v48
	v_mul_f32_e32 v50, v99, v50
	v_cndmask_b32_e64 v51, v51, v48, s[10:11]
	v_cndmask_b32_e64 v48, v50, v99, s[10:11]
	v_mov_b32_e32 v50, v48
	v_mov_b32_e32 v99, v48
	v_mov_b32_e32 v100, v51
	v_mov_b32_e32 v101, v51
	v_permlane32_swap_b32_e32 v50, v99
	s_nop 0
	v_permlane32_swap_b32_e32 v100, v101
	s_and_saveexec_b64 s[0:1], s[8:9]
	v_cndmask_b32_e64 v50, v50, v99, s[6:7]
	v_cndmask_b32_e64 v99, v100, v101, s[6:7]
	v_mul_f32_e32 v50, v48, v50
	v_fmac_f32_e32 v51, v48, v99
	ds_write_b64 v91, v[50:51] offset:51200
	s_or_b64 exec, exec, s[0:1]
	v_add_u32_e32 v48, v74, v52
	ds_read_b128 v[100:103], v48
	ds_read_b32 v99, v76 offset:1024
	v_add_u32_e32 v48, v75, v52
	ds_read_b128 v[104:107], v48
	v_add_u32_e32 v48, v74, v53
	ds_read_b128 v[108:111], v48
	s_waitcnt lgkmcnt(3)
	v_mfma_f32_16x16x32_bf16 v[100:103], v[38:41], v[100:103], 0
	ds_read2st64_b32 v[50:51], v76 offset1:2
	v_add_u32_e32 v48, v75, v53
	s_waitcnt lgkmcnt(1)
	v_mfma_f32_16x16x32_bf16 v[100:103], v[34:37], v[108:111], v[100:103]
	ds_read_b128 v[108:111], v48
	v_mfma_f32_16x16x32_bf16 v[104:107], v[38:41], v[104:107], 0
	s_waitcnt lgkmcnt(0)
; __device__ __forceinline__ void ph_lru(const Ptrs& P, unsigned char* lds, int mode, int item0) {
;     ...
;             for (int ct = 0; ct < 4; ++ct) {
;                 const int e = 16 * ct + fr, ky = (e >> 1) & 7;
;                 const bf16x8 wa0 = *(const bf16x8*)(wa + e * 128 + ((fq ^ ky) << 4)), wa1 = *(const bf16x8*)(wa + e * 128 + (((4 + fq) ^ ky) << 4));
;                 const bf16x8 wx0 = *(const bf16x8*)(wx + e * 128 + ((fq ^ ky) << 4)), wx1 = *(const bf16x8*)(wx + e * 128 + (((4 + fq) ^ ky) << 4));
;                 f32x4 ga = {0.f, 0.f, 0.f, 0.f}, gx = {0.f, 0.f, 0.f, 0.f};
;                 ga = __builtin_amdgcn_mfma_f32_16x16x32_bf16(af0, wa0, ga, 0, 0, 0); ga = __builtin_amdgcn_mfma_f32_16x16x32_bf16(af1, wa1, ga, 0, 0, 0);
;                 gx = __builtin_amdgcn_mfma_f32_16x16x32_bf16(af0, wx0, gx, 0, 0, 0); gx = __builtin_amdgcn_mfma_f32_16x16x32_bf16(af1, wx1, gx, 0, 0, 0);
;                 const float bav = GBL[dir * 64 + e], bxv = GBL[128 + dir * 64 + e], c8 = GBL[256 + dir * 64 + e];
; #pragma unroll
;                 for (int j = 0; j < 4; ++j) {
;                     const float r = fsigmoid(ga[j] + bav), ig = fsigmoid(gx[j] + bxv);
;                     const float a = __builtin_amdgcn_exp2f(-c8 * r);
;                     av[dir][ct][j] = a; uv[dir][ct][j] = sqrtf(fmaxf(1.f - a * a, 0.f)) * ig * X[(16 * wid + 4 * fq + j) * 68 + e];
;                 }
;                 float Al = av[dir][ct][0] * av[dir][ct][1] * av[dir][ct][2] * av[dir][ct][3], Hl;
;                 if (dir == 0) Hl = ((uv[dir][ct][0] * av[dir][ct][1] + uv[dir][ct][1]) * av[dir][ct][2] + uv[dir][ct][2]) * av[dir][ct][3] + uv[dir][ct][3];
;                 else Hl = ((uv[dir][ct][3] * av[dir][ct][2] + uv[dir][ct][2]) * av[dir][ct][1] + uv[dir][ct][1]) * av[dir][ct][0] + uv[dir][ct][0];
;                 const int pq = dir == 0 ? fq : 3 - fq;
;                 {
;                     const float Ap = lane_shift16(Al, dir == 0), Hp = lane_shift16(Hl, dir == 0);
;                     if (pq >= 1) { Hl = Al * Hp + Hl; Al = Al * Ap; }
;                 }
;                 {
;                     const float Ap = lane_xor32(Al), Hp = lane_xor32(Hl);
;                     if (pq >= 2) { Hl = Al * Hp + Hl; Al = Al * Ap; }
;                 }
;                 {
;                     const float Ap = lane_shift16(Al, dir == 0), Hp = lane_shift16(Hl, dir == 0);
	v_mfma_f32_16x16x32_bf16 v[104:107], v[34:37], v[108:111], v[104:107]
	s_nop 3
	v_add_f32_e32 v100, v100, v50
	v_mul_f32_e32 v100, 0xbfb8aa3b, v100
	v_exp_f32_e32 v100, v100
	v_add_f32_e32 v101, v101, v50
	v_mul_f32_e32 v101, 0xbfb8aa3b, v101
	v_exp_f32_e32 v101, v101
	v_add_f32_e32 v48, 1.0, v100
	v_rcp_f32_e32 v48, v48
	v_add_f32_e32 v100, v104, v51
	v_mul_f32_e32 v100, 0xbfb8aa3b, v100
	v_exp_f32_e32 v100, v100
	v_mul_f32_e64 v48, v48, -v99
	v_exp_f32_e32 v48, v48
	v_add_f32_e32 v101, 1.0, v101
	v_add_f32_e32 v100, 1.0, v100
	v_rcp_f32_e32 v100, v100
	v_fma_f32 v104, -v48, v48, 1.0
	v_max_f32_e32 v104, 0, v104
	v_rcp_f32_e32 v101, v101
	v_add_f32_e32 v102, v102, v50
	v_sqrt_f32_e32 v108, v104
	v_mul_f32_e32 v102, 0xbfb8aa3b, v102
	v_exp_f32_e32 v102, v102
	v_add_f32_e32 v50, v103, v50
	v_add_u32_e32 v109, -1, v108
	v_add_u32_e32 v110, 1, v108
	v_fma_f32 v111, -v109, v108, v104
	v_fma_f32 v112, -v110, v108, v104
	v_cmp_ge_f32_e64 s[0:1], 0, v111
	v_add_f32_e32 v102, 1.0, v102
	v_rcp_f32_e32 v102, v102
	v_cndmask_b32_e64 v108, v108, v109, s[0:1]
	v_cmp_lt_f32_e64 s[0:1], 0, v112
	v_mul_f32_e32 v50, 0xbfb8aa3b, v50
	v_mul_f32_e64 v102, v102, -v99
	v_cndmask_b32_e64 v108, v108, v110, s[0:1]
	v_exp_f32_e32 v102, v102
	v_exp_f32_e32 v50, v50
	v_mov_b32_e32 v104, v108
	v_mul_f32_e32 v104, v100, v104
	v_mul_f32_e64 v100, v101, -v99
	v_exp_f32_e32 v108, v100
	v_add_f32_e32 v100, v105, v51
	v_mul_f32_e32 v100, 0xbfb8aa3b, v100
	v_exp_f32_e32 v105, v100
	v_fma_f32 v100, -v108, v108, 1.0
	v_max_f32_e32 v100, 0, v100
	v_add_f32_e32 v105, 1.0, v105
	v_rcp_f32_e32 v105, v105
	v_mov_b32_e32 v109, v100
	v_sqrt_f32_e32 v110, v109
	v_add_f32_e32 v106, v106, v51
	v_mul_f32_e32 v106, 0xbfb8aa3b, v106
	v_add_f32_e32 v50, 1.0, v50
	v_add_u32_e32 v111, -1, v110
	v_fma_f32 v112, -v111, v110, v109
	v_cmp_ge_f32_e64 s[0:1], 0, v112
	v_add_u32_e32 v112, 1, v110
	v_exp_f32_e32 v106, v106
	v_cndmask_b32_e64 v111, v110, v111, s[0:1]
	v_fma_f32 v110, -v112, v110, v109
	v_cmp_lt_f32_e64 s[0:1], 0, v110
	v_rcp_f32_e32 v50, v50
	v_add_f32_e32 v106, 1.0, v106
	v_cndmask_b32_e64 v110, v111, v112, s[0:1]
	v_mul_f32_e64 v50, v50, -v99
	v_rcp_f32_e32 v106, v106
	v_mov_b32_e32 v109, v110
	v_fma_f32 v110, -v102, v102, 1.0
	v_max_f32_e32 v110, 0, v110
	v_mul_f32_e32 v105, v105, v109
	v_exp_f32_e32 v99, v50
	v_sqrt_f32_e32 v111, v110
	v_add_f32_e32 v50, v107, v51
	v_mul_f32_e32 v50, 0xbfb8aa3b, v50
	ds_read2_b32 v[100:101], v98 offset0:32 offset1:100
	v_add_u32_e32 v109, -1, v111
	v_fma_f32 v112, -v109, v111, v110
	v_cmp_ge_f32_e64 s[0:1], 0, v112
	v_add_u32_e32 v112, 1, v111
	s_nop 0
	v_cndmask_b32_e64 v109, v111, v109, s[0:1]
	v_fma_f32 v111, -v112, v111, v110
	v_cmp_lt_f32_e64 s[0:1], 0, v111
	s_nop 1
	v_cndmask_b32_e64 v103, v109, v112, s[0:1]
	v_mul_f32_e32 v103, v106, v103
	v_exp_f32_e32 v106, v50
	v_fma_f32 v50, -v99, v99, 1.0
	v_max_f32_e32 v50, 0, v50
	v_add_f32_e32 v106, 1.0, v106
	v_rcp_f32_e32 v106, v106
	v_mov_b32_e32 v107, v50
	v_sqrt_f32_e32 v109, v107
	ds_read2_b32 v[50:51], v98 offset0:168 offset1:236
	v_add_u32_e32 v110, -1, v109
	v_fma_f32 v111, -v110, v109, v107
	v_cmp_ge_f32_e64 s[0:1], 0, v111
	v_add_u32_e32 v111, 1, v109
	s_nop 0
	v_cndmask_b32_e64 v110, v109, v110, s[0:1]
	v_fma_f32 v109, -v111, v109, v107
	v_cmp_lt_f32_e64 s[0:1], 0, v109
	s_nop 1
	v_cndmask_b32_e64 v109, v110, v111, s[0:1]
	v_mov_b32_e32 v107, v109
	v_mul_f32_e32 v106, v106, v107
	s_waitcnt lgkmcnt(0)
	v_mul_f32_e32 v51, v51, v106
	v_mul_f32_e32 v51, v102, v51
	v_mul_f32_e32 v106, v48, v108
	v_fmac_f32_e32 v51, v50, v103
	v_mul_f32_e32 v106, v102, v106
	v_mul_f32_e32 v50, v108, v51
	v_mul_f32_e32 v99, v99, v106
	v_fmac_f32_e32 v50, v101, v105
	v_mul_f32_e32 v48, v48, v50
	v_mov_b32_e32 v50, v99
	v_mov_b32_e32 v51, v99
	s_nop 1
	v_permlane16_swap_b32_e32 v50, v51
	v_cndmask_b32_e64 v50, v50, v51, s[4:5]
	v_fmac_f32_e32 v48, v100, v104
	v_mov_b32_e32 v100, v50
	s_nop 1
	v_permlane32_swap_b32_e32 v50, v100
	v_cndmask_b32_e64 v50, v50, v100, s[6:7]
	v_cndmask_b32_e64 v50, v50, v51, s[4:5]
	v_mov_b32_e32 v51, v48
	v_mov_b32_e32 v100, v48
	s_nop 1
	v_permlane16_swap_b32_e32 v51, v100
	v_cndmask_b32_e64 v51, v51, v100, s[4:5]
	v_mov_b32_e32 v101, v51
	s_nop 1
	v_permlane32_swap_b32_e32 v51, v101
	v_cndmask_b32_e64 v51, v51, v101, s[6:7]
	v_cndmask_b32_e64 v51, v51, v100, s[4:5]
	v_fma_f32 v51, v99, v51, v48
	v_mul_f32_e32 v50, v99, v50
	v_cndmask_b32_e64 v51, v51, v48, s[10:11]
	v_cndmask_b32_e64 v48, v50, v99, s[10:11]
	v_mov_b32_e32 v50, v48
	v_mov_b32_e32 v99, v48
	v_mov_b32_e32 v100, v51
	v_mov_b32_e32 v101, v51
	v_permlane32_swap_b32_e32 v50, v99
	s_nop 0
	v_permlane32_swap_b32_e32 v100, v101
	s_and_saveexec_b64 s[0:1], s[8:9]
	v_cndmask_b32_e64 v50, v50, v99, s[6:7]
	v_cndmask_b32_e64 v99, v100, v101, s[6:7]
	v_mul_f32_e32 v50, v48, v50
	v_fmac_f32_e32 v51, v48, v99
	ds_write_b64 v92, v[50:51] offset:51200
	s_or_b64 exec, exec, s[0:1]
	v_add_u32_e32 v48, v77, v52
	ds_read_b128 v[100:103], v48
	ds_read_b32 v99, v79 offset:1024
	v_add_u32_e32 v48, v78, v52
	ds_read_b128 v[104:107], v48
	v_add_u32_e32 v48, v77, v53
	ds_read_b128 v[108:111], v48
	s_waitcnt lgkmcnt(3)
	v_mfma_f32_16x16x32_bf16 v[100:103], v[38:41], v[100:103], 0
	ds_read2st64_b32 v[50:51], v79 offset1:2
	v_add_u32_e32 v48, v78, v53
	s_waitcnt lgkmcnt(1)
	v_mfma_f32_16x16x32_bf16 v[100:103], v[34:37], v[108:111], v[100:103]
	v_mfma_f32_16x16x32_bf16 v[38:41], v[38:41], v[104:107], 0
	ds_read_b128 v[104:107], v48
	s_waitcnt lgkmcnt(1)
	s_nop 4
	v_add_f32_e32 v100, v100, v50
	v_mul_f32_e32 v100, 0xbfb8aa3b, v100
	v_exp_f32_e32 v100, v100
	s_waitcnt lgkmcnt(0)
; __device__ __forceinline__ void ph_lru(const Ptrs& P, unsigned char* lds, int mode, int item0) {
;     ...
;             for (int ct = 0; ct < 4; ++ct) {
;                 const int e = 16 * ct + fr, ky = (e >> 1) & 7;
;                 const bf16x8 wa0 = *(const bf16x8*)(wa + e * 128 + ((fq ^ ky) << 4)), wa1 = *(const bf16x8*)(wa + e * 128 + (((4 + fq) ^ ky) << 4));
;                 const bf16x8 wx0 = *(const bf16x8*)(wx + e * 128 + ((fq ^ ky) << 4)), wx1 = *(const bf16x8*)(wx + e * 128 + (((4 + fq) ^ ky) << 4));
;                 f32x4 ga = {0.f, 0.f, 0.f, 0.f}, gx = {0.f, 0.f, 0.f, 0.f};
;                 ga = __builtin_amdgcn_mfma_f32_16x16x32_bf16(af0, wa0, ga, 0, 0, 0); ga = __builtin_amdgcn_mfma_f32_16x16x32_bf16(af1, wa1, ga, 0, 0, 0);
;                 gx = __builtin_amdgcn_mfma_f32_16x16x32_bf16(af0, wx0, gx, 0, 0, 0); gx = __builtin_amdgcn_mfma_f32_16x16x32_bf16(af1, wx1, gx, 0, 0, 0);
;                 const float bav = GBL[dir * 64 + e], bxv = GBL[128 + dir * 64 + e], c8 = GBL[256 + dir * 64 + e];
; #pragma unroll
;                 for (int j = 0; j < 4; ++j) {
;                     const float r = fsigmoid(ga[j] + bav), ig = fsigmoid(gx[j] + bxv);
;                     const float a = __builtin_amdgcn_exp2f(-c8 * r);
;                     av[dir][ct][j] = a; uv[dir][ct][j] = sqrtf(fmaxf(1.f - a * a, 0.f)) * ig * X[(16 * wid + 4 * fq + j) * 68 + e];
;                 }
;                 float Al = av[dir][ct][0] * av[dir][ct][1] * av[dir][ct][2] * av[dir][ct][3], Hl;
;                 if (dir == 0) Hl = ((uv[dir][ct][0] * av[dir][ct][1] + uv[dir][ct][1]) * av[dir][ct][2] + uv[dir][ct][2]) * av[dir][ct][3] + uv[dir][ct][3];
;                 else Hl = ((uv[dir][ct][3] * av[dir][ct][2] + uv[dir][ct][2]) * av[dir][ct][1] + uv[dir][ct][1]) * av[dir][ct][0] + uv[dir][ct][0];
;                 const int pq = dir == 0 ? fq : 3 - fq;
;                 {
;                     const float Ap = lane_shift16(Al, dir == 0), Hp = lane_shift16(Hl, dir == 0);
;                     if (pq >= 1) { Hl = Al * Hp + Hl; Al = Al * Ap; }
;                 }
;                 {
;                     const float Ap = lane_xor32(Al), Hp = lane_xor32(Hl);
;                     if (pq >= 2) { Hl = Al * Hp + Hl; Al = Al * Ap; }
;                 }
;                 {
;                     const float Ap = lane_shift16(Al, dir == 0), Hp = lane_shift16(Hl, dir == 0);
	v_mfma_f32_16x16x32_bf16 v[34:37], v[34:37], v[104:107], v[38:41]
	v_add_f32_e32 v102, v102, v50
	v_add_f32_e32 v48, 1.0, v100
	v_rcp_f32_e32 v48, v48
	v_add_f32_e32 v38, v101, v50
	s_nop 3
	v_add_f32_e32 v34, v34, v51
	v_mul_f32_e32 v34, 0xbfb8aa3b, v34
	v_mul_f32_e64 v39, v48, -v99
	v_exp_f32_e32 v39, v39
	v_mul_f32_e32 v38, 0xbfb8aa3b, v38
	v_exp_f32_e32 v34, v34
	v_exp_f32_e32 v38, v38
	v_fma_f32 v40, -v39, v39, 1.0
	v_max_f32_e32 v40, 0, v40
	v_add_f32_e32 v34, 1.0, v34
	v_add_f32_e32 v38, 1.0, v38
	v_sqrt_f32_e32 v41, v40
	v_rcp_f32_e32 v34, v34
	v_rcp_f32_e32 v38, v38
	v_mul_f32_e32 v102, 0xbfb8aa3b, v102
	v_add_u32_e32 v48, -1, v41
	v_add_u32_e32 v100, 1, v41
	v_fma_f32 v101, -v48, v41, v40
	v_fma_f32 v104, -v100, v41, v40
	v_cmp_ge_f32_e64 s[0:1], 0, v101
	v_exp_f32_e32 v102, v102
	v_add_f32_e32 v36, v36, v51
	v_cndmask_b32_e64 v41, v41, v48, s[0:1]
	v_cmp_lt_f32_e64 s[0:1], 0, v104
	v_add_f32_e32 v102, 1.0, v102
	v_rcp_f32_e32 v102, v102
	v_cndmask_b32_e64 v41, v41, v100, s[0:1]
	v_add_f32_e32 v50, v103, v50
	v_mul_f32_e32 v36, 0xbfb8aa3b, v36
	v_mov_b32_e32 v40, v41
	v_mul_f32_e32 v40, v34, v40
	v_mul_f32_e64 v34, v38, -v99
	v_exp_f32_e32 v38, v34
	v_add_f32_e32 v34, v35, v51
	v_mul_f32_e32 v34, 0xbfb8aa3b, v34
	v_exp_f32_e32 v41, v34
	v_fma_f32 v34, -v38, v38, 1.0
	v_max_f32_e32 v34, 0, v34
	v_add_f32_e32 v41, 1.0, v41
	v_rcp_f32_e32 v41, v41
	v_mov_b32_e32 v48, v34
	v_sqrt_f32_e32 v100, v48
	v_mul_f32_e32 v50, 0xbfb8aa3b, v50
	v_exp_f32_e32 v36, v36
	v_exp_f32_e32 v50, v50
	v_add_u32_e32 v101, -1, v100
	v_fma_f32 v104, -v101, v100, v48
	v_cmp_ge_f32_e64 s[0:1], 0, v104
	v_add_u32_e32 v104, 1, v100
	v_add_f32_e32 v36, 1.0, v36
	v_cndmask_b32_e64 v101, v100, v101, s[0:1]
	v_fma_f32 v100, -v104, v100, v48
	v_cmp_lt_f32_e64 s[0:1], 0, v100
	v_add_f32_e32 v50, 1.0, v50
	v_rcp_f32_e32 v36, v36
	v_cndmask_b32_e64 v100, v101, v104, s[0:1]
	v_rcp_f32_e32 v50, v50
	ds_read2_b32 v[34:35], v98 offset0:48 offset1:116
	v_mov_b32_e32 v48, v100
	v_mul_f32_e64 v100, v102, -v99
	v_exp_f32_e32 v100, v100
	v_mul_f32_e32 v41, v41, v48
	v_fma_f32 v101, -v100, v100, 1.0
	v_max_f32_e32 v101, 0, v101
	v_sqrt_f32_e32 v102, v101
	s_nop 0
	v_add_u32_e32 v48, -1, v102
	v_fma_f32 v104, -v48, v102, v101
	v_cmp_ge_f32_e64 s[0:1], 0, v104
	v_add_u32_e32 v104, 1, v102
	s_nop 0
	v_cndmask_b32_e64 v48, v102, v48, s[0:1]
	v_fma_f32 v102, -v104, v102, v101
	v_cmp_lt_f32_e64 s[0:1], 0, v102
	s_nop 1
	v_cndmask_b32_e64 v48, v48, v104, s[0:1]
	v_mul_f32_e32 v48, v36, v48
	v_mul_f32_e64 v36, v50, -v99
	v_exp_f32_e32 v50, v36
	v_add_f32_e32 v36, v37, v51
	v_mul_f32_e32 v36, 0xbfb8aa3b, v36
	v_exp_f32_e32 v51, v36
	v_fma_f32 v36, -v50, v50, 1.0
	v_max_f32_e32 v36, 0, v36
	v_add_f32_e32 v51, 1.0, v51
	v_rcp_f32_e32 v51, v51
	v_mov_b32_e32 v99, v36
	v_sqrt_f32_e32 v101, v99
	ds_read2_b32 v[36:37], v98 offset0:184 offset1:252
	v_add_u32_e32 v102, -1, v101
	v_fma_f32 v103, -v102, v101, v99
	v_cmp_ge_f32_e64 s[0:1], 0, v103
	v_add_u32_e32 v103, 1, v101
	s_nop 0
	v_cndmask_b32_e64 v102, v101, v102, s[0:1]
	v_fma_f32 v101, -v103, v101, v99
	v_cmp_lt_f32_e64 s[0:1], 0, v101
	s_nop 1
	v_cndmask_b32_e64 v101, v102, v103, s[0:1]
	v_mov_b32_e32 v99, v101
	v_mul_f32_e32 v51, v51, v99
	s_waitcnt lgkmcnt(0)
	v_mul_f32_e32 v37, v37, v51
	v_mul_f32_e32 v37, v100, v37
	v_fmac_f32_e32 v37, v36, v48
	v_mul_f32_e32 v51, v39, v38
	v_mul_f32_e32 v36, v38, v37
	v_mul_f32_e32 v51, v100, v51
	v_fmac_f32_e32 v36, v35, v41
	v_mul_f32_e32 v50, v50, v51
	v_mul_f32_e32 v35, v39, v36
	v_fmac_f32_e32 v35, v34, v40
	v_mov_b32_e32 v34, v50
	v_mov_b32_e32 v36, v50
	s_nop 1
	v_permlane16_swap_b32_e32 v34, v36
	v_cndmask_b32_e64 v34, v34, v36, s[4:5]
	v_mov_b32_e32 v37, v34
	s_nop 1
	v_permlane32_swap_b32_e32 v34, v37
	v_cndmask_b32_e64 v34, v34, v37, s[6:7]
	v_cndmask_b32_e64 v34, v34, v36, s[4:5]
	v_mov_b32_e32 v36, v35
	v_mov_b32_e32 v37, v35
	s_nop 1
	v_permlane16_swap_b32_e32 v36, v37
	v_cndmask_b32_e64 v36, v36, v37, s[4:5]
	v_mov_b32_e32 v38, v36
	s_nop 1
	v_permlane32_swap_b32_e32 v36, v38
	v_cndmask_b32_e64 v36, v36, v38, s[6:7]
	v_cndmask_b32_e64 v36, v36, v37, s[4:5]
	v_fma_f32 v36, v50, v36, v35
	v_mul_f32_e32 v34, v50, v34
	v_cndmask_b32_e64 v35, v36, v35, s[10:11]
	v_cndmask_b32_e64 v36, v34, v50, s[10:11]
	v_mov_b32_e32 v34, v36
	v_mov_b32_e32 v37, v36
	v_mov_b32_e32 v38, v35
	v_mov_b32_e32 v39, v35
	v_permlane32_swap_b32_e32 v34, v37
	s_nop 0
	v_permlane32_swap_b32_e32 v38, v39
	s_and_saveexec_b64 s[0:1], s[8:9]
	v_cndmask_b32_e64 v34, v34, v37, s[6:7]
	v_cndmask_b32_e64 v37, v38, v39, s[6:7]
	v_mul_f32_e32 v34, v36, v34
	v_fmac_f32_e32 v35, v36, v37
	ds_write_b64 v93, v[34:35] offset:51200
	s_or_b64 exec, exec, s[0:1]
	s_waitcnt lgkmcnt(0)
	s_barrier
	s_and_saveexec_b64 s[0:1], s[16:17]
	s_cbranch_execz .LBB0_864
; __device__ __forceinline__ void ph_lru(const Ptrs& P, unsigned char* lds, int mode, int item0) {
;     ...
;         for (int dir = 0; dir < 2; ++dir) {
; #pragma unroll
;             for (int ct = 0; ct < 4; ++ct) {
;                 const int e = 16 * ct + fr;
;                 if (mode == 0) {
;                     if (wid == 0 && fq == 0) {
;                         float Ac = 1.f, Hc = 0.f;
;                         for (int sI = 0; sI < 8; ++sI) { const int sg = dir == 0 ? sI : 7 - sI; const float2 sv = *(const float2*)(SEG + ((dir * 8 + sg) * 64 + e) * 2); Hc = sv.x * Hc + sv.y; Ac *= sv.x; }
;                         float2 o; o.x = Ac; o.y = Hc; *(float2*)(agg + ((((size_t)b * NCH + c) * 2 + dir) * 512 + n * 64 + e) * 2) = o;
;                     }
	ds_read2st64_b64 v[34:37], v94 offset0:100 offset1:101
	ds_read2st64_b64 v[38:41], v94 offset0:102 offset1:103
	ds_read2st64_b64 v[100:103], v94 offset0:104 offset1:105
	s_mul_hi_i32 s31, s48, 0x78787879
	s_lshr_b32 s33, s31, 31
	s_waitcnt lgkmcnt(2)
	v_fma_f32 v35, 0, v34, v35
	v_fmac_f32_e32 v37, v35, v36
	v_mul_f32_e32 v50, v34, v36
	s_waitcnt lgkmcnt(1)
	v_fma_f32 v34, v37, v38, v39
	v_fma_f32 v39, v34, v40, v41
	ds_read2st64_b64 v[34:37], v94 offset0:106 offset1:107
	s_waitcnt lgkmcnt(1)
	v_fma_f32 v51, v39, v100, v101
	v_mov_b32_e32 v39, v102
	v_pk_mul_f32 v[106:107], v[50:51], v[38:39]
	v_mov_b32_e32 v41, v103
	v_pk_mul_f32 v[40:41], v[106:107], v[40:41]
	v_pk_fma_f32 v[38:39], v[50:51], v[38:39], v[102:103]
	s_waitcnt lgkmcnt(0)
	v_mov_b32_e32 v101, v34
	v_mov_b32_e32 v41, v39
	s_ashr_i32 s31, s31, 7
	v_mov_b32_e32 v39, v34
	v_pk_mul_f32 v[50:51], v[40:41], v[100:101]
	s_add_i32 s31, s31, s33
	v_pk_mul_f32 v[50:51], v[50:51], v[102:103]
	v_pk_fma_f32 v[34:35], v[40:41], v[100:101], v[34:35]
	v_pk_mov_b32 v[100:101], v[38:39], v[36:37] op_sel:[1,0]
	s_mul_i32 s31, s31, 34
	v_pk_mul_f32 v[38:39], v[50:51], v[100:101]
	s_add_i32 s30, s31, s30
	s_lshl_b32 s33, s49, 9
	v_mov_b32_e32 v34, v50
	v_pk_mul_f32 v[50:51], v[38:39], v[36:37]
	ds_read2st64_b64 v[38:41], v95 offset0:100 offset1:101
	s_ashr_i32 s31, s30, 31
	s_sub_i32 s33, s3, s33
	v_pk_fma_f32 v[34:35], v[34:35], v[100:101], v[36:37]
	s_lshl_b64 s[30:31], s[30:31], 10
	s_ashr_i32 s48, s33, 31
	v_mov_b32_e32 v51, v35
	ds_read2st64_b64 v[34:37], v95 offset0:102 offset1:103
	s_add_u32 s30, s30, s33
	s_addc_u32 s31, s31, s48
	ds_read2st64_b64 v[100:103], v95 offset0:104 offset1:105
	v_mov_b32_e32 v105, s31
	v_or_b32_e32 v104, s30, v130
	s_waitcnt lgkmcnt(2)
	v_fma_f32 v39, 0, v38, v39
	v_lshl_add_u64 v[104:105], v[104:105], 3, s[14:15]
	v_fmac_f32_e32 v41, v39, v40
	global_store_dwordx2 v[104:105], v[50:51], off
	v_mul_f32_e32 v50, v38, v40
	s_waitcnt lgkmcnt(1)
	v_fma_f32 v35, v41, v34, v35
	ds_read2st64_b64 v[38:41], v95 offset0:106 offset1:107
	v_fma_f32 v35, v35, v36, v37
	s_waitcnt lgkmcnt(1)
	v_fma_f32 v51, v35, v100, v101
	v_mov_b32_e32 v35, v102
	v_pk_mul_f32 v[106:107], v[50:51], v[34:35]
	v_mov_b32_e32 v37, v103
	v_pk_mul_f32 v[36:37], v[106:107], v[36:37]
	v_pk_fma_f32 v[34:35], v[50:51], v[34:35], v[102:103]
	s_waitcnt lgkmcnt(0)
	v_mov_b32_e32 v101, v38
	v_mov_b32_e32 v37, v35
	v_mov_b32_e32 v35, v38
	v_pk_mul_f32 v[50:51], v[36:37], v[100:101]
	v_pk_fma_f32 v[38:39], v[36:37], v[100:101], v[38:39]
	v_pk_mul_f32 v[50:51], v[50:51], v[102:103]
	v_pk_mov_b32 v[100:101], v[34:35], v[40:41] op_sel:[1,0]
	v_mov_b32_e32 v38, v50
	v_pk_mul_f32 v[34:35], v[50:51], v[100:101]
	v_pk_fma_f32 v[38:39], v[38:39], v[100:101], v[40:41]
	v_pk_mul_f32 v[50:51], v[34:35], v[40:41]
	ds_read2st64_b64 v[34:37], v96 offset0:100 offset1:101
	v_mov_b32_e32 v51, v39
	ds_read2st64_b64 v[38:41], v96 offset0:102 offset1:103
	v_mov_b32_e32 v105, s31
	v_or_b32_e32 v104, s30, v42
	s_waitcnt lgkmcnt(1)
	v_fma_f32 v35, 0, v34, v35
	ds_read2st64_b64 v[100:103], v96 offset0:104 offset1:105
	v_lshl_add_u64 v[104:105], v[104:105], 3, s[14:15]
	v_fmac_f32_e32 v37, v35, v36
	global_store_dwordx2 v[104:105], v[50:51], off
	v_mul_f32_e32 v50, v34, v36
	s_waitcnt lgkmcnt(1)
	v_fma_f32 v34, v37, v38, v39
	v_fma_f32 v39, v34, v40, v41
	ds_read2st64_b64 v[34:37], v96 offset0:106 offset1:107
	s_waitcnt lgkmcnt(1)
	v_fma_f32 v51, v39, v100, v101
	v_mov_b32_e32 v39, v102
	v_pk_mul_f32 v[106:107], v[50:51], v[38:39]
	v_mov_b32_e32 v41, v103
	v_pk_mul_f32 v[40:41], v[106:107], v[40:41]
	v_pk_fma_f32 v[38:39], v[50:51], v[38:39], v[102:103]
	s_waitcnt lgkmcnt(0)
	v_mov_b32_e32 v101, v34
	v_mov_b32_e32 v41, v39
	v_mov_b32_e32 v39, v34
	v_pk_mul_f32 v[50:51], v[40:41], v[100:101]
	v_pk_fma_f32 v[34:35], v[40:41], v[100:101], v[34:35]
	v_pk_mul_f32 v[50:51], v[50:51], v[102:103]
	v_pk_mov_b32 v[100:101], v[38:39], v[36:37] op_sel:[1,0]
	v_mov_b32_e32 v34, v50
	v_pk_mul_f32 v[38:39], v[50:51], v[100:101]
	v_pk_fma_f32 v[34:35], v[34:35], v[100:101], v[36:37]
	v_pk_mul_f32 v[50:51], v[38:39], v[36:37]
	ds_read2st64_b64 v[38:41], v97 offset0:100 offset1:101
	v_mov_b32_e32 v51, v35
	ds_read2st64_b64 v[34:37], v97 offset0:102 offset1:103
	ds_read2st64_b64 v[100:103], v97 offset0:104 offset1:105
	v_mov_b32_e32 v105, s31
	v_or_b32_e32 v104, s30, v44
	s_waitcnt lgkmcnt(2)
	v_fma_f32 v39, 0, v38, v39
	v_lshl_add_u64 v[104:105], v[104:105], 3, s[14:15]
	v_fmac_f32_e32 v41, v39, v40
	global_store_dwordx2 v[104:105], v[50:51], off
	v_mul_f32_e32 v50, v38, v40
	s_waitcnt lgkmcnt(1)
	v_fma_f32 v35, v41, v34, v35
	ds_read2st64_b64 v[38:41], v97 offset0:106 offset1:107
	v_fma_f32 v35, v35, v36, v37
	s_waitcnt lgkmcnt(1)
	v_fma_f32 v51, v35, v100, v101
	v_mov_b32_e32 v35, v102
	v_pk_mul_f32 v[106:107], v[50:51], v[34:35]
	v_mov_b32_e32 v37, v103
	v_pk_mul_f32 v[36:37], v[106:107], v[36:37]
	v_pk_fma_f32 v[34:35], v[50:51], v[34:35], v[102:103]
	s_waitcnt lgkmcnt(0)
	v_mov_b32_e32 v101, v38
	v_mov_b32_e32 v37, v35
	v_mov_b32_e32 v35, v38
	v_pk_mul_f32 v[50:51], v[36:37], v[100:101]
	v_pk_fma_f32 v[36:37], v[36:37], v[100:101], v[38:39]
	v_pk_mul_f32 v[50:51], v[50:51], v[102:103]
	v_pk_mov_b32 v[34:35], v[34:35], v[40:41] op_sel:[1,0]
	v_mov_b32_e32 v36, v50
	v_pk_mul_f32 v[38:39], v[50:51], v[34:35]
	v_pk_fma_f32 v[34:35], v[36:37], v[34:35], v[40:41]
	v_pk_mul_f32 v[38:39], v[38:39], v[40:41]
	v_mov_b32_e32 v105, s31
	v_or_b32_e32 v104, s30, v46
	v_mov_b32_e32 v39, v35
	ds_read2st64_b64 v[34:37], v94 offset0:114 offset1:115
	v_lshl_add_u64 v[104:105], v[104:105], 3, s[14:15]
	global_store_dwordx2 v[104:105], v[38:39], off
	ds_read2st64_b64 v[38:41], v94 offset0:112 offset1:113
	ds_read2st64_b64 v[100:103], v94 offset0:110 offset1:111
	s_waitcnt lgkmcnt(2)
; __device__ __forceinline__ void ph_lru(const Ptrs& P, unsigned char* lds, int mode, int item0) {
;     ...
;         for (int dir = 0; dir < 2; ++dir) {
; #pragma unroll
;             for (int ct = 0; ct < 4; ++ct) {
;                 const int e = 16 * ct + fr;
;                 if (mode == 0) {
;                     if (wid == 0 && fq == 0) {
;                         float Ac = 1.f, Hc = 0.f;
;                         for (int sI = 0; sI < 8; ++sI) { const int sg = dir == 0 ? sI : 7 - sI; const float2 sv = *(const float2*)(SEG + ((dir * 8 + sg) * 64 + e) * 2); Hc = sv.x * Hc + sv.y; Ac *= sv.x; }
;                         float2 o; o.x = Ac; o.y = Hc; *(float2*)(agg + ((((size_t)b * NCH + c) * 2 + dir) * 512 + n * 64 + e) * 2) = o;
;                     }
	v_fma_f32 v37, 0, v36, v37
	v_fmac_f32_e32 v35, v37, v34
	v_mul_f32_e32 v50, v36, v34
	s_waitcnt lgkmcnt(1)
	v_fma_f32 v34, v35, v40, v41
	v_fma_f32 v39, v34, v38, v39
	ds_read2st64_b64 v[34:37], v94 offset0:108 offset1:109
	s_waitcnt lgkmcnt(1)
	v_fma_f32 v51, v39, v102, v103
	v_mov_b32_e32 v41, v100
	v_pk_mul_f32 v[106:107], v[50:51], v[40:41]
	v_mov_b32_e32 v39, v101
	v_pk_mul_f32 v[38:39], v[106:107], v[38:39]
	v_pk_fma_f32 v[40:41], v[50:51], v[40:41], v[100:101]
	s_waitcnt lgkmcnt(0)
	v_mov_b32_e32 v103, v36
	v_mov_b32_e32 v39, v41
	v_mov_b32_e32 v41, v36
	v_pk_mul_f32 v[50:51], v[38:39], v[102:103]
	v_pk_mov_b32 v[40:41], v[40:41], v[34:35] op_sel:[1,0]
	v_pk_mul_f32 v[50:51], v[50:51], v[100:101]
	v_pk_fma_f32 v[100:101], v[38:39], v[102:103], v[36:37]
	v_pk_mul_f32 v[36:37], v[50:51], v[40:41]
	v_mov_b32_e32 v100, v50
	v_pk_mul_f32 v[50:51], v[36:37], v[34:35]
	ds_read2st64_b64 v[36:39], v95 offset0:114 offset1:115
	s_add_u32 s30, s30, 0x200
	s_addc_u32 s31, s31, 0
	v_pk_fma_f32 v[34:35], v[100:101], v[40:41], v[34:35]
	ds_read2st64_b64 v[100:103], v95 offset0:112 offset1:113
	v_mov_b32_e32 v105, s31
	v_or_b32_e32 v104, s30, v130
	v_lshl_add_u64 v[104:105], v[104:105], 3, s[14:15]
	v_mov_b32_e32 v51, v35
	global_store_dwordx2 v[104:105], v[50:51], off
	s_waitcnt lgkmcnt(1)
	v_fma_f32 v34, 0, v38, v39
	v_mul_f32_e32 v50, v38, v36
	ds_read2st64_b64 v[38:41], v95 offset0:110 offset1:111
	v_fmac_f32_e32 v37, v34, v36
	s_waitcnt lgkmcnt(1)
	v_fma_f32 v34, v37, v102, v103
	v_fma_f32 v48, v34, v100, v101
	ds_read2st64_b64 v[34:37], v95 offset0:108 offset1:109
	s_waitcnt lgkmcnt(1)
	v_fma_f32 v51, v48, v40, v41
	v_mov_b32_e32 v103, v38
	v_pk_mul_f32 v[106:107], v[50:51], v[102:103]
	v_mov_b32_e32 v101, v39
	v_pk_mul_f32 v[100:101], v[106:107], v[100:101]
	v_pk_fma_f32 v[50:51], v[50:51], v[102:103], v[38:39]
	s_waitcnt lgkmcnt(0)
	v_mov_b32_e32 v41, v36
	v_mov_b32_e32 v101, v51
	v_mov_b32_e32 v51, v36
	v_pk_mul_f32 v[102:103], v[100:101], v[40:41]
	v_pk_fma_f32 v[40:41], v[100:101], v[40:41], v[36:37]
	v_pk_mul_f32 v[38:39], v[102:103], v[38:39]
	v_pk_mov_b32 v[50:51], v[50:51], v[34:35] op_sel:[1,0]
	v_mov_b32_e32 v40, v38
	v_pk_mul_f32 v[36:37], v[38:39], v[50:51]
	v_mov_b32_e32 v105, s31
	v_or_b32_e32 v104, s30, v42
	v_pk_mul_f32 v[100:101], v[36:37], v[34:35]
	ds_read2st64_b64 v[36:39], v96 offset0:114 offset1:115
	v_pk_fma_f32 v[34:35], v[40:41], v[50:51], v[34:35]
	v_lshl_add_u64 v[104:105], v[104:105], 3, s[14:15]
	v_mov_b32_e32 v101, v35
	global_store_dwordx2 v[104:105], v[100:101], off
	ds_read2st64_b64 v[100:103], v96 offset0:112 offset1:113
	s_waitcnt lgkmcnt(1)
	v_fma_f32 v34, 0, v38, v39
	v_mul_f32_e32 v50, v38, v36
	ds_read2st64_b64 v[38:41], v96 offset0:110 offset1:111
	v_fmac_f32_e32 v37, v34, v36
	s_waitcnt lgkmcnt(1)
	v_fma_f32 v34, v37, v102, v103
	v_fma_f32 v48, v34, v100, v101
	ds_read2st64_b64 v[34:37], v96 offset0:108 offset1:109
	s_waitcnt lgkmcnt(1)
	v_fma_f32 v51, v48, v40, v41
	v_mov_b32_e32 v103, v38
	v_pk_mul_f32 v[106:107], v[50:51], v[102:103]
	v_mov_b32_e32 v101, v39
	v_pk_mul_f32 v[100:101], v[106:107], v[100:101]
	v_pk_fma_f32 v[50:51], v[50:51], v[102:103], v[38:39]
	s_waitcnt lgkmcnt(0)
	v_mov_b32_e32 v41, v36
	v_mov_b32_e32 v101, v51
	v_mov_b32_e32 v51, v36
	v_pk_mul_f32 v[102:103], v[100:101], v[40:41]
	v_pk_fma_f32 v[40:41], v[100:101], v[40:41], v[36:37]
	v_pk_mul_f32 v[38:39], v[102:103], v[38:39]
	v_pk_mov_b32 v[50:51], v[50:51], v[34:35] op_sel:[1,0]
	v_mov_b32_e32 v40, v38
	v_pk_mul_f32 v[36:37], v[38:39], v[50:51]
	v_mov_b32_e32 v105, s31
	v_or_b32_e32 v104, s30, v44
	v_pk_mul_f32 v[100:101], v[36:37], v[34:35]
	ds_read2st64_b64 v[36:39], v97 offset0:114 offset1:115
	v_pk_fma_f32 v[34:35], v[40:41], v[50:51], v[34:35]
	v_lshl_add_u64 v[104:105], v[104:105], 3, s[14:15]
	v_mov_b32_e32 v101, v35
	global_store_dwordx2 v[104:105], v[100:101], off
	ds_read2st64_b64 v[100:103], v97 offset0:112 offset1:113
	s_waitcnt lgkmcnt(1)
	v_fma_f32 v34, 0, v38, v39
	v_mul_f32_e32 v50, v38, v36
	ds_read2st64_b64 v[38:41], v97 offset0:110 offset1:111
	v_fmac_f32_e32 v37, v34, v36
	s_waitcnt lgkmcnt(1)
	v_fma_f32 v34, v37, v102, v103
	v_fma_f32 v48, v34, v100, v101
	ds_read2st64_b64 v[34:37], v97 offset0:108 offset1:109
	s_waitcnt lgkmcnt(1)
	v_fma_f32 v51, v48, v40, v41
	v_mov_b32_e32 v103, v38
	v_pk_mul_f32 v[106:107], v[50:51], v[102:103]
	v_mov_b32_e32 v101, v39
	v_pk_mul_f32 v[100:101], v[106:107], v[100:101]
	v_pk_fma_f32 v[50:51], v[50:51], v[102:103], v[38:39]
	s_waitcnt lgkmcnt(0)
	v_mov_b32_e32 v41, v36
	v_mov_b32_e32 v101, v51
	v_mov_b32_e32 v51, v36
	v_pk_mul_f32 v[102:103], v[100:101], v[40:41]
	v_pk_fma_f32 v[36:37], v[100:101], v[40:41], v[36:37]
	v_pk_mul_f32 v[38:39], v[102:103], v[38:39]
	v_pk_mov_b32 v[40:41], v[50:51], v[34:35] op_sel:[1,0]
	v_mov_b32_e32 v36, v38
	v_pk_mul_f32 v[38:39], v[38:39], v[40:41]
	v_mov_b32_e32 v105, s31
	v_or_b32_e32 v104, s30, v46
	v_pk_mul_f32 v[38:39], v[38:39], v[34:35]
	v_pk_fma_f32 v[34:35], v[36:37], v[40:41], v[34:35]
	v_lshl_add_u64 v[104:105], v[104:105], 3, s[14:15]
	v_mov_b32_e32 v39, v35
	global_store_dwordx2 v[104:105], v[38:39], off
	s_branch .LBB0_864

; __device__ __forceinline__ void ph_lru(const Ptrs& P, unsigned char* lds, int mode, int item0) {
;     ...
;         __syncthreads();
;         const int trow = 16 * wid + fr;
;         const bf16x8 af0 = *(const bf16x8*)(XB + trow * 128 + ((fq ^ ((trow >> 1) & 7)) << 4));
;         const bf16x8 af1 = *(const bf16x8*)(XB + trow * 128 + (((4 + fq) ^ ((trow >> 1) & 7)) << 4));
;         float av[2][4][4], uv[2][4][4], Ae[2][4], He[2][4];
; #pragma unroll
;         for (int dir = 0; dir < 2; ++dir) {
;             const unsigned char* wa = WL + (dir * 2 + 0) * 8192; const unsigned char* wx = WL + (dir * 2 + 1) * 8192;
; #pragma unroll
;             for (int ct = 0; ct < 4; ++ct) {
;                 const int e = 16 * ct + fr, ky = (e >> 1) & 7;
;                 const bf16x8 wa0 = *(const bf16x8*)(wa + e * 128 + ((fq ^ ky) << 4)), wa1 = *(const bf16x8*)(wa + e * 128 + (((4 + fq) ^ ky) << 4));
;                 const bf16x8 wx0 = *(const bf16x8*)(wx + e * 128 + ((fq ^ ky) << 4)), wx1 = *(const bf16x8*)(wx + e * 128 + (((4 + fq) ^ ky) << 4));
;                 f32x4 ga = {0.f, 0.f, 0.f, 0.f}, gx = {0.f, 0.f, 0.f, 0.f};
;                 ga = __builtin_amdgcn_mfma_f32_16x16x32_bf16(af0, wa0, ga, 0, 0, 0); ga = __builtin_amdgcn_mfma_f32_16x16x32_bf16(af1, wa1, ga, 0, 0, 0);
;                 gx = __builtin_amdgcn_mfma_f32_16x16x32_bf16(af0, wx0, gx, 0, 0, 0); gx = __builtin_amdgcn_mfma_f32_16x16x32_bf16(af1, wx1, gx, 0, 0, 0);
;                 const float bav = GBL[dir * 64 + e], bxv = GBL[128 + dir * 64 + e], c8 = GBL[256 + dir * 64 + e];
; #pragma unroll
;                 for (int j = 0; j < 4; ++j) {
;                     const float r = fsigmoid(ga[j] + bav), ig = fsigmoid(gx[j] + bxv);
;                     const float a = __builtin_amdgcn_exp2f(-c8 * r);
;                     av[dir][ct][j] = a; uv[dir][ct][j] = sqrtf(fmaxf(1.f - a * a, 0.f)) * ig * X[(16 * wid + 4 * fq + j) * 68 + e];
;                 }
;                 float Al = av[dir][ct][0] * av[dir][ct][1] * av[dir][ct][2] * av[dir][ct][3], Hl;
;                 if (dir == 0) Hl = ((uv[dir][ct][0] * av[dir][ct][1] + uv[dir][ct][1]) * av[dir][ct][2] + uv[dir][ct][2]) * av[dir][ct][3] + uv[dir][ct][3];
;                 else Hl = ((uv[dir][ct][3] * av[dir][ct][2] + uv[dir][ct][2]) * av[dir][ct][1] + uv[dir][ct][1]) * av[dir][ct][0] + uv[dir][ct][0];
;                 const int pq = dir == 0 ? fq : 3 - fq;
.LBB0_1111:
	s_or_b64 exec, exec, s[0:1]
	v_add_u32_e32 v50, v80, v81
	s_waitcnt lgkmcnt(0)
	s_barrier
	ds_read_b128 v[54:57], v50 offset:34816
	v_add_u32_e32 v50, v80, v82
	v_add_u32_e32 v58, v84, v81
	ds_read_b128 v[50:53], v50 offset:34816
	ds_read_b128 v[58:61], v58 offset:59904
	v_add_u32_e32 v62, v84, v82
	ds_read_b128 v[62:65], v62 offset:59904
	ds_read_b32 v138, v86 offset:1024
	s_waitcnt lgkmcnt(2)
	v_mfma_f32_16x16x32_bf16 v[58:61], v[54:57], v[58:61], 0
	v_add_u32_e32 v66, v85, v81
	ds_read_b128 v[132:135], v66
	ds_read2st64_b32 v[136:137], v86 offset1:2
	s_waitcnt lgkmcnt(3)
	v_mfma_f32_16x16x32_bf16 v[58:61], v[50:53], v[62:65], v[58:61]
	v_add_u32_e32 v62, v85, v82
	ds_read_b128 v[62:65], v62
	s_waitcnt lgkmcnt(2)
	v_mfma_f32_16x16x32_bf16 v[132:135], v[54:57], v[132:135], 0
	s_waitcnt lgkmcnt(0)
	v_mfma_f32_16x16x32_bf16 v[62:65], v[50:53], v[62:65], v[132:135]
	s_nop 1
	v_add_f32_e32 v58, v58, v136
	v_mul_f32_e32 v58, 0xbfb8aa3b, v58
	v_exp_f32_e32 v58, v58
	v_add_f32_e32 v59, v59, v136
	v_mul_f32_e32 v59, 0xbfb8aa3b, v59
	v_exp_f32_e32 v59, v59
	v_add_f32_e32 v58, 1.0, v58
	v_rcp_f32_e32 v58, v58
	v_add_f32_e32 v63, v63, v137
	v_add_f32_e32 v59, 1.0, v59
	v_mul_f32_e32 v63, 0xbfb8aa3b, v63
	v_mul_f32_e64 v58, v58, -v138
	v_exp_f32_e32 v66, v58
	v_add_f32_e32 v58, v62, v137
	v_mul_f32_e32 v58, 0xbfb8aa3b, v58
	v_exp_f32_e32 v58, v58
	v_fma_f32 v62, -v66, v66, 1.0
	v_max_f32_e32 v62, 0, v62
	v_add_f32_e32 v58, 1.0, v58
	v_rcp_f32_e32 v58, v58
	v_sqrt_f32_e32 v132, v62
	v_add_f32_e32 v60, v60, v136
	v_exp_f32_e32 v63, v63
	v_mul_f32_e32 v60, 0xbfb8aa3b, v60
	v_add_u32_e32 v133, -1, v132
	v_add_u32_e32 v134, 1, v132
	v_fma_f32 v135, -v133, v132, v62
	v_fma_f32 v139, -v134, v132, v62
	v_cmp_ge_f32_e64 s[0:1], 0, v135
	v_exp_f32_e32 v60, v60
	v_add_f32_e32 v61, v61, v136
	v_cndmask_b32_e64 v132, v132, v133, s[0:1]
	v_cmp_lt_f32_e64 s[0:1], 0, v139
	v_add_f32_e32 v60, 1.0, v60
	v_rcp_f32_e32 v60, v60
	v_cndmask_b32_e64 v132, v132, v134, s[0:1]
	v_rcp_f32_e32 v133, v59
	v_mul_f32_e64 v60, v60, -v138
	v_mul_f32_e32 v61, 0xbfb8aa3b, v61
	v_mov_b32_e32 v59, v132
	v_mul_f32_e64 v132, v133, -v138
	v_exp_f32_e32 v132, v132
	v_mul_f32_e32 v62, v58, v59
	ds_read2_b32 v[58:59], v130 offset1:68
	v_exp_f32_e32 v61, v61
	v_fma_f32 v133, -v132, v132, 1.0
	v_max_f32_e32 v133, 0, v133
	v_mov_b32_e32 v134, v133
	v_sqrt_f32_e32 v135, v134
	s_waitcnt lgkmcnt(0)
	v_mul_f32_e32 v133, v58, v62
	v_add_f32_e32 v58, 1.0, v63
	v_rcp_f32_e32 v58, v58
	v_add_u32_e32 v62, -1, v135
	v_fma_f32 v63, -v62, v135, v134
	v_cmp_ge_f32_e64 s[0:1], 0, v63
	v_add_u32_e32 v63, 1, v135
	s_nop 0
	v_cndmask_b32_e64 v62, v135, v62, s[0:1]
	v_fma_f32 v135, -v63, v135, v134
	v_cmp_lt_f32_e64 s[0:1], 0, v135
	s_nop 1
	v_cndmask_b32_e64 v62, v62, v63, s[0:1]
	v_exp_f32_e32 v134, v60
	v_mul_f32_e32 v58, v58, v62
	v_add_f32_e32 v60, v64, v137
	v_mul_f32_e32 v60, 0xbfb8aa3b, v60
	v_fma_f32 v62, -v134, v134, 1.0
	v_max_f32_e32 v62, 0, v62
	v_exp_f32_e32 v60, v60
	v_mul_f32_e32 v135, v59, v58
	v_sqrt_f32_e32 v63, v62
	v_add_f32_e32 v58, 1.0, v60
	v_rcp_f32_e32 v58, v58
	v_add_u32_e32 v59, -1, v63
	v_fma_f32 v60, -v59, v63, v62
	v_cmp_ge_f32_e64 s[0:1], 0, v60
	v_add_u32_e32 v60, 1, v63
	s_nop 0
	v_cndmask_b32_e64 v59, v63, v59, s[0:1]
	v_fma_f32 v63, -v60, v63, v62
	v_cmp_lt_f32_e64 s[0:1], 0, v63
	s_nop 1
	v_cndmask_b32_e64 v59, v59, v60, s[0:1]
	v_add_f32_e32 v60, 1.0, v61
	v_rcp_f32_e32 v60, v60
	s_nop 0
	v_mul_f32_e64 v60, v60, -v138
	v_exp_f32_e32 v136, v60
	v_add_f32_e32 v60, v65, v137
	v_mul_f32_e32 v61, v58, v59
	v_fma_f32 v62, -v136, v136, 1.0
	v_max_f32_e32 v62, 0, v62
	ds_read2_b32 v[58:59], v130 offset0:136 offset1:204
	v_mul_f32_e32 v60, 0xbfb8aa3b, v60
	v_exp_f32_e32 v60, v60
	v_sqrt_f32_e32 v63, v62
	s_waitcnt lgkmcnt(0)
	v_mul_f32_e32 v137, v58, v61
	v_add_f32_e32 v58, 1.0, v60
	v_add_u32_e32 v60, -1, v63
	v_fma_f32 v61, -v60, v63, v62
	v_cmp_ge_f32_e64 s[0:1], 0, v61
	v_add_u32_e32 v61, 1, v63
	v_rcp_f32_e32 v58, v58
	v_cndmask_b32_e64 v60, v63, v60, s[0:1]
	v_fma_f32 v63, -v61, v63, v62
	v_cmp_lt_f32_e64 s[0:1], 0, v63
	s_nop 1
	v_cndmask_b32_e64 v60, v60, v61, s[0:1]
	v_mul_f32_e32 v58, v58, v60
	v_mul_f32_e32 v138, v59, v58
	v_mul_f32_e32 v58, v66, v132
	v_mul_f32_e32 v58, v134, v58
	v_mul_f32_e32 v58, v136, v58
	v_mov_b32_e32 v60, v58
	v_mov_b32_e32 v61, v58
	s_nop 1
	v_permlane16_swap_b32_e32 v60, v61
	v_cndmask_b32_e64 v61, v60, v61, s[6:7]
	v_fma_f32 v59, v132, v133, v135
	v_mov_b32_e32 v62, v61
	v_fma_f32 v59, v134, v59, v137
	s_nop 0
	v_permlane32_swap_b32_e32 v61, v62
	v_fma_f32 v59, v136, v59, v138
	v_cndmask_b32_e64 v61, v61, v62, s[8:9]
	v_cndmask_b32_e64 v60, v60, v61, s[6:7]
	v_mov_b32_e32 v61, v59
	v_mov_b32_e32 v62, v59
	s_nop 1
	v_permlane16_swap_b32_e32 v61, v62
	v_cndmask_b32_e64 v62, v61, v62, s[6:7]
	v_mov_b32_e32 v63, v62
	s_nop 1
	v_permlane32_swap_b32_e32 v62, v63
	v_cndmask_b32_e64 v62, v62, v63, s[8:9]
	v_cndmask_b32_e64 v61, v61, v62, s[6:7]
	v_mul_f32_e32 v60, v58, v60
	v_fma_f32 v61, v58, v61, v59
	v_cndmask_b32_e64 v60, v60, v58, s[10:11]
	v_cndmask_b32_e64 v61, v61, v59, s[10:11]
	v_mov_b32_e32 v58, v60
	v_mov_b32_e32 v59, v60
	s_nop 1
	v_permlane32_swap_b32_e32 v58, v59
	v_cndmask_b32_e64 v58, v58, v59, s[8:9]
	v_mov_b32_e32 v59, v61
	v_mov_b32_e32 v62, v61
	s_nop 1
	v_permlane32_swap_b32_e32 v59, v62
	v_mul_f32_e32 v58, v60, v58
	v_cndmask_b32_e64 v59, v59, v62, s[8:9]
	v_cndmask_b32_e64 v140, v60, v58, s[14:15]
	v_fma_f32 v59, v60, v59, v61
	v_mov_b32_e32 v60, v140
	v_cndmask_b32_e64 v139, v61, v59, s[14:15]
	s_nop 0
	v_permlane16_swap_b32_e32 v140, v60
	v_cndmask_b32_e64 v141, v140, v60, s[6:7]
	v_mov_b32_e32 v60, v139
	s_nop 1
	v_permlane16_swap_b32_e32 v139, v60
	v_cndmask_b32_e64 v143, v139, v60, s[6:7]
	v_mov_b32_e32 v142, v141
	v_mov_b32_e32 v144, v143
	s_nop 0
	v_permlane32_swap_b32_e32 v141, v142
	v_permlane32_swap_b32_e32 v143, v144
	s_and_saveexec_b64 s[0:1], s[16:17]
	ds_write_b64 v120, v[58:59] offset:51200
	s_or_b64 exec, exec, s[0:1]
	v_add_u32_e32 v58, v87, v81
	ds_read_b128 v[58:61], v58 offset:59904
	v_add_u32_e32 v145, v87, v82
	v_add_u32_e32 v62, v88, v81
	ds_read_b32 v152, v89 offset:1024
	ds_read_b128 v[146:149], v145 offset:59904
	ds_read_b128 v[62:65], v62
	s_waitcnt lgkmcnt(3)
; __device__ __forceinline__ void ph_lru(const Ptrs& P, unsigned char* lds, int mode, int item0) {
;     ...
;             for (int ct = 0; ct < 4; ++ct) {
;                 const int e = 16 * ct + fr, ky = (e >> 1) & 7;
;                 const bf16x8 wa0 = *(const bf16x8*)(wa + e * 128 + ((fq ^ ky) << 4)), wa1 = *(const bf16x8*)(wa + e * 128 + (((4 + fq) ^ ky) << 4));
;                 const bf16x8 wx0 = *(const bf16x8*)(wx + e * 128 + ((fq ^ ky) << 4)), wx1 = *(const bf16x8*)(wx + e * 128 + (((4 + fq) ^ ky) << 4));
;                 f32x4 ga = {0.f, 0.f, 0.f, 0.f}, gx = {0.f, 0.f, 0.f, 0.f};
;                 ga = __builtin_amdgcn_mfma_f32_16x16x32_bf16(af0, wa0, ga, 0, 0, 0); ga = __builtin_amdgcn_mfma_f32_16x16x32_bf16(af1, wa1, ga, 0, 0, 0);
;                 gx = __builtin_amdgcn_mfma_f32_16x16x32_bf16(af0, wx0, gx, 0, 0, 0); gx = __builtin_amdgcn_mfma_f32_16x16x32_bf16(af1, wx1, gx, 0, 0, 0);
;                 const float bav = GBL[dir * 64 + e], bxv = GBL[128 + dir * 64 + e], c8 = GBL[256 + dir * 64 + e];
; #pragma unroll
;                 for (int j = 0; j < 4; ++j) {
;                     const float r = fsigmoid(ga[j] + bav), ig = fsigmoid(gx[j] + bxv);
;                     const float a = __builtin_amdgcn_exp2f(-c8 * r);
;                     av[dir][ct][j] = a; uv[dir][ct][j] = sqrtf(fmaxf(1.f - a * a, 0.f)) * ig * X[(16 * wid + 4 * fq + j) * 68 + e];
;                 }
;                 float Al = av[dir][ct][0] * av[dir][ct][1] * av[dir][ct][2] * av[dir][ct][3], Hl;
;                 if (dir == 0) Hl = ((uv[dir][ct][0] * av[dir][ct][1] + uv[dir][ct][1]) * av[dir][ct][2] + uv[dir][ct][2]) * av[dir][ct][3] + uv[dir][ct][3];
;                 else Hl = ((uv[dir][ct][3] * av[dir][ct][2] + uv[dir][ct][2]) * av[dir][ct][1] + uv[dir][ct][1]) * av[dir][ct][0] + uv[dir][ct][0];
;                 const int pq = dir == 0 ? fq : 3 - fq;
;                 {
;                     const float Ap = lane_shift16(Al, dir == 0), Hp = lane_shift16(Hl, dir == 0);
;                     if (pq >= 1) { Hl = Al * Hp + Hl; Al = Al * Ap; }
;                 }
;                 {
;                     const float Ap = lane_xor32(Al), Hp = lane_xor32(Hl);
;                     if (pq >= 2) { Hl = Al * Hp + Hl; Al = Al * Ap; }
;                 }
;                 {
;                     const float Ap = lane_shift16(Al, dir == 0), Hp = lane_shift16(Hl, dir == 0);
	v_mfma_f32_16x16x32_bf16 v[58:61], v[54:57], v[58:61], 0
	ds_read2st64_b32 v[150:151], v89 offset1:2
	v_add_u32_e32 v145, v88, v82
	s_waitcnt lgkmcnt(2)
	v_mfma_f32_16x16x32_bf16 v[58:61], v[50:53], v[146:149], v[58:61]
	ds_read_b128 v[146:149], v145
	s_waitcnt lgkmcnt(2)
	v_mfma_f32_16x16x32_bf16 v[62:65], v[54:57], v[62:65], 0
	s_waitcnt lgkmcnt(0)
	v_mfma_f32_16x16x32_bf16 v[62:65], v[50:53], v[146:149], v[62:65]
	s_nop 2
	v_add_f32_e32 v58, v58, v150
	v_mul_f32_e32 v58, 0xbfb8aa3b, v58
	v_exp_f32_e32 v58, v58
	v_add_f32_e32 v59, v59, v150
	v_mul_f32_e32 v59, 0xbfb8aa3b, v59
	v_add_f32_e32 v62, v62, v151
	v_add_f32_e32 v58, 1.0, v58
	v_rcp_f32_e32 v58, v58
	v_exp_f32_e32 v59, v59
	v_add_f32_e32 v63, v63, v151
	v_mul_f32_e32 v63, 0xbfb8aa3b, v63
	v_mul_f32_e64 v58, v58, -v152
	v_exp_f32_e32 v145, v58
	v_mul_f32_e32 v58, 0xbfb8aa3b, v62
	v_add_f32_e32 v59, 1.0, v59
	v_exp_f32_e32 v58, v58
	v_fma_f32 v62, -v145, v145, 1.0
	v_max_f32_e32 v62, 0, v62
	v_add_f32_e32 v58, 1.0, v58
	v_rcp_f32_e32 v58, v58
	v_sqrt_f32_e32 v146, v62
	v_add_f32_e32 v60, v60, v150
	v_exp_f32_e32 v63, v63
	v_mul_f32_e32 v60, 0xbfb8aa3b, v60
	v_add_u32_e32 v147, -1, v146
	v_add_u32_e32 v148, 1, v146
	v_fma_f32 v149, -v147, v146, v62
	v_fma_f32 v153, -v148, v146, v62
	v_cmp_ge_f32_e64 s[0:1], 0, v149
	v_exp_f32_e32 v60, v60
	v_add_f32_e32 v61, v61, v150
	v_cndmask_b32_e64 v146, v146, v147, s[0:1]
	v_cmp_lt_f32_e64 s[0:1], 0, v153
	v_add_f32_e32 v60, 1.0, v60
	v_rcp_f32_e32 v60, v60
	v_cndmask_b32_e64 v146, v146, v148, s[0:1]
	v_rcp_f32_e32 v147, v59
	v_mul_f32_e64 v60, v60, -v152
	v_mul_f32_e32 v61, 0xbfb8aa3b, v61
	v_mov_b32_e32 v59, v146
	v_mul_f32_e64 v146, v147, -v152
	v_exp_f32_e32 v146, v146
	v_mul_f32_e32 v62, v58, v59
	ds_read2_b32 v[58:59], v130 offset0:16 offset1:84
	v_exp_f32_e32 v61, v61
	v_fma_f32 v147, -v146, v146, 1.0
	v_max_f32_e32 v147, 0, v147
	v_mov_b32_e32 v148, v147
	v_sqrt_f32_e32 v149, v148
	s_waitcnt lgkmcnt(0)
	v_mul_f32_e32 v147, v58, v62
	v_add_f32_e32 v58, 1.0, v63
	v_rcp_f32_e32 v58, v58
	v_add_u32_e32 v62, -1, v149
	v_fma_f32 v63, -v62, v149, v148
	v_cmp_ge_f32_e64 s[0:1], 0, v63
	v_add_u32_e32 v63, 1, v149
	s_nop 0
	v_cndmask_b32_e64 v62, v149, v62, s[0:1]
	v_fma_f32 v149, -v63, v149, v148
	v_cmp_lt_f32_e64 s[0:1], 0, v149
	s_nop 1
	v_cndmask_b32_e64 v62, v62, v63, s[0:1]
	v_exp_f32_e32 v148, v60
	v_mul_f32_e32 v58, v58, v62
	v_add_f32_e32 v60, v64, v151
	v_mul_f32_e32 v60, 0xbfb8aa3b, v60
	v_fma_f32 v62, -v148, v148, 1.0
	v_max_f32_e32 v62, 0, v62
	v_exp_f32_e32 v60, v60
	v_mul_f32_e32 v149, v59, v58
	v_sqrt_f32_e32 v63, v62
	v_add_f32_e32 v58, 1.0, v60
	v_rcp_f32_e32 v58, v58
	v_add_u32_e32 v59, -1, v63
	v_fma_f32 v60, -v59, v63, v62
	v_cmp_ge_f32_e64 s[0:1], 0, v60
	v_add_u32_e32 v60, 1, v63
	s_nop 0
	v_cndmask_b32_e64 v59, v63, v59, s[0:1]
	v_fma_f32 v63, -v60, v63, v62
	v_cmp_lt_f32_e64 s[0:1], 0, v63
	s_nop 1
	v_cndmask_b32_e64 v59, v59, v60, s[0:1]
	v_add_f32_e32 v60, 1.0, v61
	v_rcp_f32_e32 v60, v60
	s_nop 0
	v_mul_f32_e64 v60, v60, -v152
	v_exp_f32_e32 v150, v60
	v_add_f32_e32 v60, v65, v151
	v_mul_f32_e32 v61, v58, v59
	v_fma_f32 v62, -v150, v150, 1.0
	v_max_f32_e32 v62, 0, v62
	ds_read2_b32 v[58:59], v130 offset0:152 offset1:220
	v_mul_f32_e32 v60, 0xbfb8aa3b, v60
	v_exp_f32_e32 v60, v60
	v_sqrt_f32_e32 v63, v62
	s_waitcnt lgkmcnt(0)
	v_mul_f32_e32 v151, v58, v61
	v_add_f32_e32 v58, 1.0, v60
	v_add_u32_e32 v60, -1, v63
	v_fma_f32 v61, -v60, v63, v62
	v_cmp_ge_f32_e64 s[0:1], 0, v61
	v_add_u32_e32 v61, 1, v63
	v_rcp_f32_e32 v58, v58
	v_cndmask_b32_e64 v60, v63, v60, s[0:1]
	v_fma_f32 v63, -v61, v63, v62
	v_cmp_lt_f32_e64 s[0:1], 0, v63
	s_nop 1
	v_cndmask_b32_e64 v60, v60, v61, s[0:1]
	v_mul_f32_e32 v58, v58, v60
	v_mul_f32_e32 v152, v59, v58
	v_mul_f32_e32 v58, v145, v146
	v_mul_f32_e32 v58, v148, v58
	v_mul_f32_e32 v58, v150, v58
	v_mov_b32_e32 v60, v58
	v_mov_b32_e32 v61, v58
	s_nop 1
	v_permlane16_swap_b32_e32 v60, v61
	v_cndmask_b32_e64 v61, v60, v61, s[6:7]
	v_fma_f32 v59, v146, v147, v149
	v_mov_b32_e32 v62, v61
	v_fma_f32 v59, v148, v59, v151
	s_nop 0
	v_permlane32_swap_b32_e32 v61, v62
	v_fma_f32 v59, v150, v59, v152
	v_cndmask_b32_e64 v61, v61, v62, s[8:9]
	v_cndmask_b32_e64 v60, v60, v61, s[6:7]
	v_mov_b32_e32 v61, v59
	v_mov_b32_e32 v62, v59
	s_nop 1
	v_permlane16_swap_b32_e32 v61, v62
	v_cndmask_b32_e64 v62, v61, v62, s[6:7]
	v_mov_b32_e32 v63, v62
	s_nop 1
	v_permlane32_swap_b32_e32 v62, v63
	v_cndmask_b32_e64 v62, v62, v63, s[8:9]
	v_cndmask_b32_e64 v61, v61, v62, s[6:7]
	v_mul_f32_e32 v60, v58, v60
	v_fma_f32 v61, v58, v61, v59
	v_cndmask_b32_e64 v60, v60, v58, s[10:11]
	v_cndmask_b32_e64 v61, v61, v59, s[10:11]
	v_mov_b32_e32 v58, v60
	v_mov_b32_e32 v59, v60
	s_nop 1
	v_permlane32_swap_b32_e32 v58, v59
	v_cndmask_b32_e64 v58, v58, v59, s[8:9]
	v_mov_b32_e32 v59, v61
	v_mov_b32_e32 v62, v61
	s_nop 1
	v_permlane32_swap_b32_e32 v59, v62
	v_mul_f32_e32 v58, v60, v58
	v_cndmask_b32_e64 v59, v59, v62, s[8:9]
	v_cndmask_b32_e64 v154, v60, v58, s[14:15]
	v_fma_f32 v59, v60, v59, v61
	v_mov_b32_e32 v60, v154
	v_cndmask_b32_e64 v153, v61, v59, s[14:15]
	s_nop 0
	v_permlane16_swap_b32_e32 v154, v60
	v_cndmask_b32_e64 v155, v154, v60, s[6:7]
	v_mov_b32_e32 v60, v153
	s_nop 1
	v_permlane16_swap_b32_e32 v153, v60
	v_cndmask_b32_e64 v157, v153, v60, s[6:7]
	v_mov_b32_e32 v156, v155
	v_mov_b32_e32 v158, v157
	s_nop 0
	v_permlane32_swap_b32_e32 v155, v156
	v_permlane32_swap_b32_e32 v157, v158
	s_and_saveexec_b64 s[0:1], s[16:17]
	ds_write_b64 v121, v[58:59] offset:51200
	s_or_b64 exec, exec, s[0:1]
	v_add_u32_e32 v58, v90, v81
	ds_read_b128 v[58:61], v58 offset:59904
	v_add_u32_e32 v159, v90, v82
	v_add_u32_e32 v62, v91, v81
	ds_read_b32 v166, v92 offset:1024
	ds_read_b128 v[160:163], v159 offset:59904
	ds_read_b128 v[62:65], v62
	s_waitcnt lgkmcnt(3)
; __device__ __forceinline__ void ph_lru(const Ptrs& P, unsigned char* lds, int mode, int item0) {
;     ...
;             for (int ct = 0; ct < 4; ++ct) {
;                 const int e = 16 * ct + fr, ky = (e >> 1) & 7;
;                 const bf16x8 wa0 = *(const bf16x8*)(wa + e * 128 + ((fq ^ ky) << 4)), wa1 = *(const bf16x8*)(wa + e * 128 + (((4 + fq) ^ ky) << 4));
;                 const bf16x8 wx0 = *(const bf16x8*)(wx + e * 128 + ((fq ^ ky) << 4)), wx1 = *(const bf16x8*)(wx + e * 128 + (((4 + fq) ^ ky) << 4));
;                 f32x4 ga = {0.f, 0.f, 0.f, 0.f}, gx = {0.f, 0.f, 0.f, 0.f};
;                 ga = __builtin_amdgcn_mfma_f32_16x16x32_bf16(af0, wa0, ga, 0, 0, 0); ga = __builtin_amdgcn_mfma_f32_16x16x32_bf16(af1, wa1, ga, 0, 0, 0);
;                 gx = __builtin_amdgcn_mfma_f32_16x16x32_bf16(af0, wx0, gx, 0, 0, 0); gx = __builtin_amdgcn_mfma_f32_16x16x32_bf16(af1, wx1, gx, 0, 0, 0);
;                 const float bav = GBL[dir * 64 + e], bxv = GBL[128 + dir * 64 + e], c8 = GBL[256 + dir * 64 + e];
; #pragma unroll
;                 for (int j = 0; j < 4; ++j) {
;                     const float r = fsigmoid(ga[j] + bav), ig = fsigmoid(gx[j] + bxv);
;                     const float a = __builtin_amdgcn_exp2f(-c8 * r);
;                     av[dir][ct][j] = a; uv[dir][ct][j] = sqrtf(fmaxf(1.f - a * a, 0.f)) * ig * X[(16 * wid + 4 * fq + j) * 68 + e];
;                 }
;                 float Al = av[dir][ct][0] * av[dir][ct][1] * av[dir][ct][2] * av[dir][ct][3], Hl;
;                 if (dir == 0) Hl = ((uv[dir][ct][0] * av[dir][ct][1] + uv[dir][ct][1]) * av[dir][ct][2] + uv[dir][ct][2]) * av[dir][ct][3] + uv[dir][ct][3];
;                 else Hl = ((uv[dir][ct][3] * av[dir][ct][2] + uv[dir][ct][2]) * av[dir][ct][1] + uv[dir][ct][1]) * av[dir][ct][0] + uv[dir][ct][0];
;                 const int pq = dir == 0 ? fq : 3 - fq;
;                 {
;                     const float Ap = lane_shift16(Al, dir == 0), Hp = lane_shift16(Hl, dir == 0);
;                     if (pq >= 1) { Hl = Al * Hp + Hl; Al = Al * Ap; }
;                 }
;                 {
;                     const float Ap = lane_xor32(Al), Hp = lane_xor32(Hl);
;                     if (pq >= 2) { Hl = Al * Hp + Hl; Al = Al * Ap; }
;                 }
;                 {
;                     const float Ap = lane_shift16(Al, dir == 0), Hp = lane_shift16(Hl, dir == 0);
	v_mfma_f32_16x16x32_bf16 v[58:61], v[54:57], v[58:61], 0
	ds_read2st64_b32 v[164:165], v92 offset1:2
	v_add_u32_e32 v159, v91, v82
	s_waitcnt lgkmcnt(2)
	v_mfma_f32_16x16x32_bf16 v[58:61], v[50:53], v[160:163], v[58:61]
	ds_read_b128 v[160:163], v159
	s_waitcnt lgkmcnt(2)
	v_mfma_f32_16x16x32_bf16 v[62:65], v[54:57], v[62:65], 0
	s_waitcnt lgkmcnt(0)
	v_mfma_f32_16x16x32_bf16 v[62:65], v[50:53], v[160:163], v[62:65]
	s_nop 2
	v_add_f32_e32 v58, v58, v164
	v_mul_f32_e32 v58, 0xbfb8aa3b, v58
	v_exp_f32_e32 v58, v58
	v_add_f32_e32 v59, v59, v164
	v_mul_f32_e32 v59, 0xbfb8aa3b, v59
	v_add_f32_e32 v62, v62, v165
	v_add_f32_e32 v58, 1.0, v58
	v_rcp_f32_e32 v58, v58
	v_exp_f32_e32 v59, v59
	v_add_f32_e32 v63, v63, v165
	v_mul_f32_e32 v63, 0xbfb8aa3b, v63
	v_mul_f32_e64 v58, v58, -v166
	v_exp_f32_e32 v159, v58
	v_mul_f32_e32 v58, 0xbfb8aa3b, v62
	v_add_f32_e32 v59, 1.0, v59
	v_exp_f32_e32 v58, v58
	v_fma_f32 v62, -v159, v159, 1.0
	v_max_f32_e32 v62, 0, v62
	v_add_f32_e32 v58, 1.0, v58
	v_rcp_f32_e32 v58, v58
	v_sqrt_f32_e32 v160, v62
	v_add_f32_e32 v60, v60, v164
	v_exp_f32_e32 v63, v63
	v_mul_f32_e32 v60, 0xbfb8aa3b, v60
	v_add_u32_e32 v161, -1, v160
	v_add_u32_e32 v162, 1, v160
	v_fma_f32 v163, -v161, v160, v62
	v_fma_f32 v167, -v162, v160, v62
	v_cmp_ge_f32_e64 s[0:1], 0, v163
	v_exp_f32_e32 v60, v60
	v_add_f32_e32 v61, v61, v164
	v_cndmask_b32_e64 v160, v160, v161, s[0:1]
	v_cmp_lt_f32_e64 s[0:1], 0, v167
	v_add_f32_e32 v60, 1.0, v60
	v_rcp_f32_e32 v60, v60
	v_cndmask_b32_e64 v160, v160, v162, s[0:1]
	v_rcp_f32_e32 v161, v59
	v_mul_f32_e64 v60, v60, -v166
	v_mul_f32_e32 v61, 0xbfb8aa3b, v61
	v_mov_b32_e32 v59, v160
	v_mul_f32_e64 v160, v161, -v166
	v_exp_f32_e32 v160, v160
	v_mul_f32_e32 v62, v58, v59
	ds_read2_b32 v[58:59], v130 offset0:32 offset1:100
	v_exp_f32_e32 v61, v61
	v_fma_f32 v161, -v160, v160, 1.0
	v_max_f32_e32 v161, 0, v161
	v_mov_b32_e32 v162, v161
	v_sqrt_f32_e32 v163, v162
	s_waitcnt lgkmcnt(0)
	v_mul_f32_e32 v161, v58, v62
	v_add_f32_e32 v58, 1.0, v63
	v_rcp_f32_e32 v58, v58
	v_add_u32_e32 v62, -1, v163
	v_fma_f32 v63, -v62, v163, v162
	v_cmp_ge_f32_e64 s[0:1], 0, v63
	v_add_u32_e32 v63, 1, v163
	s_nop 0
	v_cndmask_b32_e64 v62, v163, v62, s[0:1]
	v_fma_f32 v163, -v63, v163, v162
	v_cmp_lt_f32_e64 s[0:1], 0, v163
	s_nop 1
	v_cndmask_b32_e64 v62, v62, v63, s[0:1]
	v_exp_f32_e32 v162, v60
	v_mul_f32_e32 v58, v58, v62
	v_add_f32_e32 v60, v64, v165
	v_mul_f32_e32 v60, 0xbfb8aa3b, v60
	v_fma_f32 v62, -v162, v162, 1.0
	v_max_f32_e32 v62, 0, v62
	v_exp_f32_e32 v60, v60
	v_mul_f32_e32 v163, v59, v58
	v_sqrt_f32_e32 v63, v62
	v_add_f32_e32 v58, 1.0, v60
	v_rcp_f32_e32 v58, v58
	v_add_u32_e32 v59, -1, v63
	v_fma_f32 v60, -v59, v63, v62
	v_cmp_ge_f32_e64 s[0:1], 0, v60
	v_add_u32_e32 v60, 1, v63
	s_nop 0
	v_cndmask_b32_e64 v59, v63, v59, s[0:1]
	v_fma_f32 v63, -v60, v63, v62
	v_cmp_lt_f32_e64 s[0:1], 0, v63
	s_nop 1
	v_cndmask_b32_e64 v59, v59, v60, s[0:1]
	v_add_f32_e32 v60, 1.0, v61
	v_rcp_f32_e32 v60, v60
	s_nop 0
	v_mul_f32_e64 v60, v60, -v166
	v_exp_f32_e32 v164, v60
	v_add_f32_e32 v60, v65, v165
	v_mul_f32_e32 v61, v58, v59
	v_fma_f32 v62, -v164, v164, 1.0
	v_max_f32_e32 v62, 0, v62
	ds_read2_b32 v[58:59], v130 offset0:168 offset1:236
	v_mul_f32_e32 v60, 0xbfb8aa3b, v60
	v_exp_f32_e32 v60, v60
	v_sqrt_f32_e32 v63, v62
	s_waitcnt lgkmcnt(0)
	v_mul_f32_e32 v165, v58, v61
	v_add_f32_e32 v58, 1.0, v60
	v_add_u32_e32 v60, -1, v63
	v_fma_f32 v61, -v60, v63, v62
	v_cmp_ge_f32_e64 s[0:1], 0, v61
	v_add_u32_e32 v61, 1, v63
	v_rcp_f32_e32 v58, v58
	v_cndmask_b32_e64 v60, v63, v60, s[0:1]
	v_fma_f32 v63, -v61, v63, v62
	v_cmp_lt_f32_e64 s[0:1], 0, v63
	s_nop 1
	v_cndmask_b32_e64 v60, v60, v61, s[0:1]
	v_mul_f32_e32 v58, v58, v60
	v_mul_f32_e32 v166, v59, v58
	v_mul_f32_e32 v58, v159, v160
	v_mul_f32_e32 v58, v162, v58
	v_mul_f32_e32 v58, v164, v58
	v_mov_b32_e32 v60, v58
	v_mov_b32_e32 v61, v58
	s_nop 1
	v_permlane16_swap_b32_e32 v60, v61
	v_cndmask_b32_e64 v61, v60, v61, s[6:7]
	v_fma_f32 v59, v160, v161, v163
	v_mov_b32_e32 v62, v61
	v_fma_f32 v59, v162, v59, v165
	s_nop 0
	v_permlane32_swap_b32_e32 v61, v62
	v_fma_f32 v59, v164, v59, v166
	v_cndmask_b32_e64 v61, v61, v62, s[8:9]
	v_cndmask_b32_e64 v60, v60, v61, s[6:7]
	v_mov_b32_e32 v61, v59
	v_mov_b32_e32 v62, v59
	s_nop 1
	v_permlane16_swap_b32_e32 v61, v62
	v_cndmask_b32_e64 v62, v61, v62, s[6:7]
	v_mov_b32_e32 v63, v62
	s_nop 1
	v_permlane32_swap_b32_e32 v62, v63
	v_cndmask_b32_e64 v62, v62, v63, s[8:9]
	v_cndmask_b32_e64 v61, v61, v62, s[6:7]
	v_mul_f32_e32 v60, v58, v60
	v_fma_f32 v61, v58, v61, v59
	v_cndmask_b32_e64 v60, v60, v58, s[10:11]
	v_cndmask_b32_e64 v61, v61, v59, s[10:11]
	v_mov_b32_e32 v58, v60
	v_mov_b32_e32 v59, v60
	s_nop 1
	v_permlane32_swap_b32_e32 v58, v59
	v_cndmask_b32_e64 v58, v58, v59, s[8:9]
	v_mov_b32_e32 v59, v61
	v_mov_b32_e32 v62, v61
	s_nop 1
	v_permlane32_swap_b32_e32 v59, v62
	v_mul_f32_e32 v58, v60, v58
	v_cndmask_b32_e64 v59, v59, v62, s[8:9]
	v_cndmask_b32_e64 v169, v60, v58, s[14:15]
	v_fma_f32 v59, v60, v59, v61
	v_mov_b32_e32 v60, v169
	v_cndmask_b32_e64 v168, v61, v59, s[14:15]
	s_nop 0
	v_permlane16_swap_b32_e32 v169, v60
	v_cndmask_b32_e64 v171, v169, v60, s[6:7]
	v_mov_b32_e32 v60, v168
	s_nop 1
	v_permlane16_swap_b32_e32 v168, v60
	v_cndmask_b32_e64 v173, v168, v60, s[6:7]
	v_mov_b32_e32 v172, v171
	v_mov_b32_e32 v175, v173
	s_nop 0
	v_permlane32_swap_b32_e32 v171, v172
	v_permlane32_swap_b32_e32 v173, v175
	s_and_saveexec_b64 s[0:1], s[16:17]
	ds_write_b64 v122, v[58:59] offset:51200
	s_or_b64 exec, exec, s[0:1]
	v_add_u32_e32 v58, v93, v81
	ds_read_b128 v[58:61], v58 offset:59904
	v_add_u32_e32 v167, v93, v82
	v_add_u32_e32 v62, v94, v81
	ds_read_b32 v185, v95 offset:1024
	ds_read_b128 v[176:179], v167 offset:59904
	ds_read_b128 v[62:65], v62
	s_waitcnt lgkmcnt(3)
; __device__ __forceinline__ void ph_lru(const Ptrs& P, unsigned char* lds, int mode, int item0) {
;     ...
;             for (int ct = 0; ct < 4; ++ct) {
;                 const int e = 16 * ct + fr, ky = (e >> 1) & 7;
;                 const bf16x8 wa0 = *(const bf16x8*)(wa + e * 128 + ((fq ^ ky) << 4)), wa1 = *(const bf16x8*)(wa + e * 128 + (((4 + fq) ^ ky) << 4));
;                 const bf16x8 wx0 = *(const bf16x8*)(wx + e * 128 + ((fq ^ ky) << 4)), wx1 = *(const bf16x8*)(wx + e * 128 + (((4 + fq) ^ ky) << 4));
;                 f32x4 ga = {0.f, 0.f, 0.f, 0.f}, gx = {0.f, 0.f, 0.f, 0.f};
;                 ga = __builtin_amdgcn_mfma_f32_16x16x32_bf16(af0, wa0, ga, 0, 0, 0); ga = __builtin_amdgcn_mfma_f32_16x16x32_bf16(af1, wa1, ga, 0, 0, 0);
;                 gx = __builtin_amdgcn_mfma_f32_16x16x32_bf16(af0, wx0, gx, 0, 0, 0); gx = __builtin_amdgcn_mfma_f32_16x16x32_bf16(af1, wx1, gx, 0, 0, 0);
;                 const float bav = GBL[dir * 64 + e], bxv = GBL[128 + dir * 64 + e], c8 = GBL[256 + dir * 64 + e];
; #pragma unroll
;                 for (int j = 0; j < 4; ++j) {
;                     const float r = fsigmoid(ga[j] + bav), ig = fsigmoid(gx[j] + bxv);
;                     const float a = __builtin_amdgcn_exp2f(-c8 * r);
;                     av[dir][ct][j] = a; uv[dir][ct][j] = sqrtf(fmaxf(1.f - a * a, 0.f)) * ig * X[(16 * wid + 4 * fq + j) * 68 + e];
;                 }
;                 float Al = av[dir][ct][0] * av[dir][ct][1] * av[dir][ct][2] * av[dir][ct][3], Hl;
;                 if (dir == 0) Hl = ((uv[dir][ct][0] * av[dir][ct][1] + uv[dir][ct][1]) * av[dir][ct][2] + uv[dir][ct][2]) * av[dir][ct][3] + uv[dir][ct][3];
;                 else Hl = ((uv[dir][ct][3] * av[dir][ct][2] + uv[dir][ct][2]) * av[dir][ct][1] + uv[dir][ct][1]) * av[dir][ct][0] + uv[dir][ct][0];
;                 const int pq = dir == 0 ? fq : 3 - fq;
;                 {
;                     const float Ap = lane_shift16(Al, dir == 0), Hp = lane_shift16(Hl, dir == 0);
;                     if (pq >= 1) { Hl = Al * Hp + Hl; Al = Al * Ap; }
;                 }
;                 {
;                     const float Ap = lane_xor32(Al), Hp = lane_xor32(Hl);
;                     if (pq >= 2) { Hl = Al * Hp + Hl; Al = Al * Ap; }
;                 }
;                 {
;                     const float Ap = lane_shift16(Al, dir == 0), Hp = lane_shift16(Hl, dir == 0);
	v_mfma_f32_16x16x32_bf16 v[58:61], v[54:57], v[58:61], 0
	ds_read2st64_b32 v[180:181], v95 offset1:2
	v_add_u32_e32 v167, v94, v82
	s_waitcnt lgkmcnt(2)
	v_mfma_f32_16x16x32_bf16 v[58:61], v[50:53], v[176:179], v[58:61]
	ds_read_b128 v[176:179], v167
	s_waitcnt lgkmcnt(2)
	v_mfma_f32_16x16x32_bf16 v[62:65], v[54:57], v[62:65], 0
	s_waitcnt lgkmcnt(0)
	v_mfma_f32_16x16x32_bf16 v[62:65], v[50:53], v[176:179], v[62:65]
	s_nop 2
	v_add_f32_e32 v58, v58, v180
	v_mul_f32_e32 v58, 0xbfb8aa3b, v58
	v_exp_f32_e32 v58, v58
	v_add_f32_e32 v59, v59, v180
	v_mul_f32_e32 v59, 0xbfb8aa3b, v59
	v_add_f32_e32 v62, v62, v181
	v_add_f32_e32 v58, 1.0, v58
	v_rcp_f32_e32 v58, v58
	v_exp_f32_e32 v59, v59
	v_add_f32_e32 v63, v63, v181
	v_mul_f32_e32 v63, 0xbfb8aa3b, v63
	v_mul_f32_e64 v58, v58, -v185
	v_exp_f32_e32 v167, v58
	v_mul_f32_e32 v58, 0xbfb8aa3b, v62
	v_add_f32_e32 v59, 1.0, v59
	v_exp_f32_e32 v58, v58
	v_fma_f32 v62, -v167, v167, 1.0
	v_max_f32_e32 v62, 0, v62
	v_add_f32_e32 v58, 1.0, v58
	v_rcp_f32_e32 v58, v58
	v_sqrt_f32_e32 v170, v62
	v_add_f32_e32 v60, v60, v180
	v_exp_f32_e32 v63, v63
	v_mul_f32_e32 v60, 0xbfb8aa3b, v60
	v_add_u32_e32 v174, -1, v170
	v_add_u32_e32 v176, 1, v170
	v_fma_f32 v177, -v174, v170, v62
	v_fma_f32 v178, -v176, v170, v62
	v_cmp_ge_f32_e64 s[0:1], 0, v177
	v_exp_f32_e32 v60, v60
	v_add_f32_e32 v61, v61, v180
	v_cndmask_b32_e64 v170, v170, v174, s[0:1]
	v_cmp_lt_f32_e64 s[0:1], 0, v178
	v_add_f32_e32 v60, 1.0, v60
	v_rcp_f32_e32 v60, v60
	v_cndmask_b32_e64 v170, v170, v176, s[0:1]
	v_rcp_f32_e32 v174, v59
	v_mul_f32_e64 v60, v60, -v185
	v_mul_f32_e32 v61, 0xbfb8aa3b, v61
	v_mov_b32_e32 v59, v170
	v_mul_f32_e64 v170, v174, -v185
	v_exp_f32_e32 v170, v170
	v_mul_f32_e32 v62, v58, v59
	ds_read2_b32 v[58:59], v130 offset0:48 offset1:116
	v_exp_f32_e32 v61, v61
	v_fma_f32 v174, -v170, v170, 1.0
	v_max_f32_e32 v174, 0, v174
	v_mov_b32_e32 v176, v174
	v_sqrt_f32_e32 v177, v176
	s_waitcnt lgkmcnt(0)
	v_mul_f32_e32 v174, v58, v62
	v_add_f32_e32 v58, 1.0, v63
	v_rcp_f32_e32 v58, v58
	v_add_u32_e32 v62, -1, v177
	v_fma_f32 v63, -v62, v177, v176
	v_cmp_ge_f32_e64 s[0:1], 0, v63
	v_add_u32_e32 v63, 1, v177
	s_nop 0
	v_cndmask_b32_e64 v62, v177, v62, s[0:1]
	v_fma_f32 v177, -v63, v177, v176
	v_cmp_lt_f32_e64 s[0:1], 0, v177
	s_nop 1
	v_cndmask_b32_e64 v62, v62, v63, s[0:1]
	v_exp_f32_e32 v176, v60
	v_mul_f32_e32 v58, v58, v62
	v_add_f32_e32 v60, v64, v181
	v_mul_f32_e32 v60, 0xbfb8aa3b, v60
	v_fma_f32 v62, -v176, v176, 1.0
	v_max_f32_e32 v62, 0, v62
	v_exp_f32_e32 v60, v60
	v_mul_f32_e32 v177, v59, v58
	v_sqrt_f32_e32 v63, v62
	v_add_f32_e32 v58, 1.0, v60
	v_rcp_f32_e32 v58, v58
	v_add_u32_e32 v59, -1, v63
	v_fma_f32 v60, -v59, v63, v62
	v_cmp_ge_f32_e64 s[0:1], 0, v60
	v_add_u32_e32 v60, 1, v63
	s_nop 0
	v_cndmask_b32_e64 v59, v63, v59, s[0:1]
	v_fma_f32 v63, -v60, v63, v62
	v_cmp_lt_f32_e64 s[0:1], 0, v63
	s_nop 1
	v_cndmask_b32_e64 v59, v59, v60, s[0:1]
	v_add_f32_e32 v60, 1.0, v61
	v_rcp_f32_e32 v60, v60
	s_nop 0
	v_mul_f32_e64 v60, v60, -v185
	v_exp_f32_e32 v178, v60
	v_add_f32_e32 v60, v65, v181
	v_mul_f32_e32 v61, v58, v59
	v_fma_f32 v62, -v178, v178, 1.0
	v_max_f32_e32 v62, 0, v62
	ds_read2_b32 v[58:59], v130 offset0:184 offset1:252
	v_mul_f32_e32 v60, 0xbfb8aa3b, v60
	v_exp_f32_e32 v60, v60
	v_sqrt_f32_e32 v63, v62
	s_waitcnt lgkmcnt(0)
	v_mul_f32_e32 v179, v58, v61
	v_add_f32_e32 v58, 1.0, v60
	v_add_u32_e32 v60, -1, v63
	v_fma_f32 v61, -v60, v63, v62
	v_cmp_ge_f32_e64 s[0:1], 0, v61
	v_add_u32_e32 v61, 1, v63
	v_rcp_f32_e32 v58, v58
	v_cndmask_b32_e64 v60, v63, v60, s[0:1]
	v_fma_f32 v63, -v61, v63, v62
	v_cmp_lt_f32_e64 s[0:1], 0, v63
	s_nop 1
	v_cndmask_b32_e64 v60, v60, v61, s[0:1]
	v_mul_f32_e32 v58, v58, v60
	v_mul_f32_e32 v180, v59, v58
	v_mul_f32_e32 v58, v167, v170
	v_mul_f32_e32 v58, v176, v58
	v_mul_f32_e32 v58, v178, v58
	v_mov_b32_e32 v60, v58
	v_mov_b32_e32 v61, v58
	s_nop 1
	v_permlane16_swap_b32_e32 v60, v61
	v_cndmask_b32_e64 v61, v60, v61, s[6:7]
	v_fma_f32 v59, v170, v174, v177
	v_mov_b32_e32 v62, v61
	v_fma_f32 v59, v176, v59, v179
	s_nop 0
	v_permlane32_swap_b32_e32 v61, v62
	v_fma_f32 v59, v178, v59, v180
	v_cndmask_b32_e64 v61, v61, v62, s[8:9]
	v_cndmask_b32_e64 v60, v60, v61, s[6:7]
	v_mov_b32_e32 v61, v59
	v_mov_b32_e32 v62, v59
	s_nop 1
	v_permlane16_swap_b32_e32 v61, v62
	v_cndmask_b32_e64 v62, v61, v62, s[6:7]
	v_mov_b32_e32 v63, v62
	s_nop 1
	v_permlane32_swap_b32_e32 v62, v63
	v_cndmask_b32_e64 v62, v62, v63, s[8:9]
	v_cndmask_b32_e64 v61, v61, v62, s[6:7]
	v_mul_f32_e32 v60, v58, v60
	v_fma_f32 v61, v58, v61, v59
	v_cndmask_b32_e64 v60, v60, v58, s[10:11]
	v_cndmask_b32_e64 v61, v61, v59, s[10:11]
	v_mov_b32_e32 v58, v60
	v_mov_b32_e32 v59, v60
	s_nop 1
	v_permlane32_swap_b32_e32 v58, v59
	v_cndmask_b32_e64 v58, v58, v59, s[8:9]
	v_mov_b32_e32 v59, v61
	v_mov_b32_e32 v62, v61
	s_nop 1
	v_permlane32_swap_b32_e32 v59, v62
	v_mul_f32_e32 v58, v60, v58
	v_cndmask_b32_e64 v59, v59, v62, s[8:9]
	v_cndmask_b32_e64 v185, v60, v58, s[14:15]
	v_fma_f32 v59, v60, v59, v61
	v_mov_b32_e32 v60, v185
	v_cndmask_b32_e64 v181, v61, v59, s[14:15]
	s_nop 0
	v_permlane16_swap_b32_e32 v185, v60
	v_cndmask_b32_e64 v186, v185, v60, s[6:7]
	v_mov_b32_e32 v60, v181
	s_nop 1
	v_permlane16_swap_b32_e32 v181, v60
	v_cndmask_b32_e64 v188, v181, v60, s[6:7]
	v_mov_b32_e32 v187, v186
	v_mov_b32_e32 v189, v188
	s_nop 0
	v_permlane32_swap_b32_e32 v186, v187
	v_permlane32_swap_b32_e32 v188, v189
	s_and_saveexec_b64 s[0:1], s[16:17]
	ds_write_b64 v123, v[58:59] offset:51200
	s_or_b64 exec, exec, s[0:1]
	v_add_u32_e32 v58, v96, v81
	ds_read_b128 v[58:61], v58
	v_add_u32_e32 v190, v96, v82
	v_add_u32_e32 v62, v97, v81
	ds_read_b32 v195, v98 offset:1024
	ds_read_b128 v[190:193], v190
	ds_read_b128 v[62:65], v62
	s_waitcnt lgkmcnt(3)
; __device__ __forceinline__ void ph_lru(const Ptrs& P, unsigned char* lds, int mode, int item0) {
;     ...
;             for (int ct = 0; ct < 4; ++ct) {
;                 const int e = 16 * ct + fr, ky = (e >> 1) & 7;
;                 const bf16x8 wa0 = *(const bf16x8*)(wa + e * 128 + ((fq ^ ky) << 4)), wa1 = *(const bf16x8*)(wa + e * 128 + (((4 + fq) ^ ky) << 4));
;                 const bf16x8 wx0 = *(const bf16x8*)(wx + e * 128 + ((fq ^ ky) << 4)), wx1 = *(const bf16x8*)(wx + e * 128 + (((4 + fq) ^ ky) << 4));
;                 f32x4 ga = {0.f, 0.f, 0.f, 0.f}, gx = {0.f, 0.f, 0.f, 0.f};
;                 ga = __builtin_amdgcn_mfma_f32_16x16x32_bf16(af0, wa0, ga, 0, 0, 0); ga = __builtin_amdgcn_mfma_f32_16x16x32_bf16(af1, wa1, ga, 0, 0, 0);
;                 gx = __builtin_amdgcn_mfma_f32_16x16x32_bf16(af0, wx0, gx, 0, 0, 0); gx = __builtin_amdgcn_mfma_f32_16x16x32_bf16(af1, wx1, gx, 0, 0, 0);
;                 const float bav = GBL[dir * 64 + e], bxv = GBL[128 + dir * 64 + e], c8 = GBL[256 + dir * 64 + e];
; #pragma unroll
;                 for (int j = 0; j < 4; ++j) {
;                     const float r = fsigmoid(ga[j] + bav), ig = fsigmoid(gx[j] + bxv);
;                     const float a = __builtin_amdgcn_exp2f(-c8 * r);
;                     av[dir][ct][j] = a; uv[dir][ct][j] = sqrtf(fmaxf(1.f - a * a, 0.f)) * ig * X[(16 * wid + 4 * fq + j) * 68 + e];
;                 }
;                 float Al = av[dir][ct][0] * av[dir][ct][1] * av[dir][ct][2] * av[dir][ct][3], Hl;
;                 if (dir == 0) Hl = ((uv[dir][ct][0] * av[dir][ct][1] + uv[dir][ct][1]) * av[dir][ct][2] + uv[dir][ct][2]) * av[dir][ct][3] + uv[dir][ct][3];
;                 else Hl = ((uv[dir][ct][3] * av[dir][ct][2] + uv[dir][ct][2]) * av[dir][ct][1] + uv[dir][ct][1]) * av[dir][ct][0] + uv[dir][ct][0];
;                 const int pq = dir == 0 ? fq : 3 - fq;
;                 {
;                     const float Ap = lane_shift16(Al, dir == 0), Hp = lane_shift16(Hl, dir == 0);
;                     if (pq >= 1) { Hl = Al * Hp + Hl; Al = Al * Ap; }
;                 }
;                 {
;                     const float Ap = lane_xor32(Al), Hp = lane_xor32(Hl);
;                     if (pq >= 2) { Hl = Al * Hp + Hl; Al = Al * Ap; }
;                 }
;                 {
;                     const float Ap = lane_shift16(Al, dir == 0), Hp = lane_shift16(Hl, dir == 0);
	v_mfma_f32_16x16x32_bf16 v[58:61], v[54:57], v[58:61], 0
	ds_read2st64_b32 v[196:197], v98 offset1:2
	v_add_u32_e32 v194, v97, v82
	s_waitcnt lgkmcnt(2)
	v_mfma_f32_16x16x32_bf16 v[58:61], v[50:53], v[190:193], v[58:61]
	ds_read_b128 v[190:193], v194
	s_waitcnt lgkmcnt(2)
	v_mfma_f32_16x16x32_bf16 v[62:65], v[54:57], v[62:65], 0
	s_waitcnt lgkmcnt(0)
	v_mfma_f32_16x16x32_bf16 v[62:65], v[50:53], v[190:193], v[62:65]
	s_nop 2
	v_add_f32_e32 v58, v58, v196
	v_mul_f32_e32 v58, 0xbfb8aa3b, v58
	v_exp_f32_e32 v58, v58
	v_add_f32_e32 v59, v59, v196
	v_mul_f32_e32 v59, 0xbfb8aa3b, v59
	v_add_f32_e32 v62, v62, v197
	v_add_f32_e32 v58, 1.0, v58
	v_rcp_f32_e32 v58, v58
	v_exp_f32_e32 v59, v59
	v_add_f32_e32 v63, v63, v197
	v_mul_f32_e32 v63, 0xbfb8aa3b, v63
	v_mul_f32_e64 v58, v58, -v195
	v_exp_f32_e32 v190, v58
	v_mul_f32_e32 v58, 0xbfb8aa3b, v62
	v_add_f32_e32 v59, 1.0, v59
	v_exp_f32_e32 v58, v58
	v_fma_f32 v62, -v190, v190, 1.0
	v_max_f32_e32 v62, 0, v62
	v_add_f32_e32 v58, 1.0, v58
	v_rcp_f32_e32 v58, v58
	v_sqrt_f32_e32 v191, v62
	v_add_f32_e32 v60, v60, v196
	v_exp_f32_e32 v63, v63
	v_mul_f32_e32 v60, 0xbfb8aa3b, v60
	v_add_u32_e32 v192, -1, v191
	v_add_u32_e32 v193, 1, v191
	v_fma_f32 v194, -v192, v191, v62
	v_fma_f32 v198, -v193, v191, v62
	v_cmp_ge_f32_e64 s[0:1], 0, v194
	v_exp_f32_e32 v60, v60
	v_add_f32_e32 v61, v61, v196
	v_cndmask_b32_e64 v191, v191, v192, s[0:1]
	v_cmp_lt_f32_e64 s[0:1], 0, v198
	v_add_f32_e32 v60, 1.0, v60
	v_rcp_f32_e32 v60, v60
	v_cndmask_b32_e64 v191, v191, v193, s[0:1]
	v_rcp_f32_e32 v192, v59
	v_mul_f32_e64 v60, v60, -v195
	v_mul_f32_e32 v61, 0xbfb8aa3b, v61
	v_mov_b32_e32 v59, v191
	v_mul_f32_e64 v191, v192, -v195
	v_exp_f32_e32 v191, v191
	v_mul_f32_e32 v62, v58, v59
	ds_read2_b32 v[58:59], v130 offset1:68
	v_exp_f32_e32 v61, v61
	v_fma_f32 v192, -v191, v191, 1.0
	v_max_f32_e32 v192, 0, v192
	v_mov_b32_e32 v193, v192
	v_sqrt_f32_e32 v194, v193
	s_waitcnt lgkmcnt(0)
	v_mul_f32_e32 v192, v58, v62
	v_add_f32_e32 v58, 1.0, v63
	v_rcp_f32_e32 v58, v58
	v_add_u32_e32 v62, -1, v194
	v_fma_f32 v63, -v62, v194, v193
	v_cmp_ge_f32_e64 s[0:1], 0, v63
	v_add_u32_e32 v63, 1, v194
	s_nop 0
	v_cndmask_b32_e64 v62, v194, v62, s[0:1]
	v_fma_f32 v194, -v63, v194, v193
	v_cmp_lt_f32_e64 s[0:1], 0, v194
	s_nop 1
	v_cndmask_b32_e64 v62, v62, v63, s[0:1]
	v_exp_f32_e32 v193, v60
	v_mul_f32_e32 v58, v58, v62
	v_add_f32_e32 v60, v64, v197
	v_mul_f32_e32 v60, 0xbfb8aa3b, v60
	v_fma_f32 v62, -v193, v193, 1.0
	v_max_f32_e32 v62, 0, v62
	v_exp_f32_e32 v60, v60
	v_mul_f32_e32 v194, v59, v58
	v_sqrt_f32_e32 v63, v62
	v_add_f32_e32 v58, 1.0, v60
	v_rcp_f32_e32 v58, v58
	v_add_u32_e32 v59, -1, v63
	v_fma_f32 v60, -v59, v63, v62
	v_cmp_ge_f32_e64 s[0:1], 0, v60
	v_add_u32_e32 v60, 1, v63
	s_nop 0
	v_cndmask_b32_e64 v59, v63, v59, s[0:1]
	v_fma_f32 v63, -v60, v63, v62
	v_cmp_lt_f32_e64 s[0:1], 0, v63
	s_nop 1
	v_cndmask_b32_e64 v59, v59, v60, s[0:1]
	v_add_f32_e32 v60, 1.0, v61
	v_rcp_f32_e32 v60, v60
	s_nop 0
	v_mul_f32_e64 v60, v60, -v195
	v_exp_f32_e32 v195, v60
	v_add_f32_e32 v60, v65, v197
	v_mul_f32_e32 v61, v58, v59
	v_fma_f32 v62, -v195, v195, 1.0
	v_max_f32_e32 v62, 0, v62
	ds_read2_b32 v[58:59], v130 offset0:136 offset1:204
	v_mul_f32_e32 v60, 0xbfb8aa3b, v60
	v_exp_f32_e32 v60, v60
	v_sqrt_f32_e32 v63, v62
	s_waitcnt lgkmcnt(0)
	v_mul_f32_e32 v196, v58, v61
	v_add_f32_e32 v58, 1.0, v60
	v_add_u32_e32 v60, -1, v63
	v_fma_f32 v61, -v60, v63, v62
	v_cmp_ge_f32_e64 s[0:1], 0, v61
	v_add_u32_e32 v61, 1, v63
	v_rcp_f32_e32 v58, v58
	v_cndmask_b32_e64 v60, v63, v60, s[0:1]
	v_fma_f32 v63, -v61, v63, v62
	v_cmp_lt_f32_e64 s[0:1], 0, v63
	s_nop 1
	v_cndmask_b32_e64 v60, v60, v61, s[0:1]
	v_mul_f32_e32 v58, v58, v60
	v_mul_f32_e32 v197, v59, v58
	v_mul_f32_e32 v58, v190, v191
	v_mul_f32_e32 v58, v193, v58
	v_mul_f32_e32 v58, v195, v58
	v_mov_b32_e32 v60, v58
	v_mov_b32_e32 v61, v58
	s_nop 1
	v_permlane16_swap_b32_e32 v60, v61
	v_cndmask_b32_e64 v60, v60, v61, s[6:7]
	v_fma_f32 v59, v193, v197, v196
	v_mov_b32_e32 v62, v60
	v_fma_f32 v59, v191, v59, v194
	s_nop 0
	v_permlane32_swap_b32_e32 v60, v62
	v_fma_f32 v59, v190, v59, v192
	v_cndmask_b32_e64 v60, v60, v62, s[8:9]
	v_cndmask_b32_e64 v60, v60, v61, s[6:7]
	v_mov_b32_e32 v61, v59
	v_mov_b32_e32 v62, v59
	s_nop 1
	v_permlane16_swap_b32_e32 v61, v62
	v_cndmask_b32_e64 v61, v61, v62, s[6:7]
	v_mov_b32_e32 v63, v61
	s_nop 1
	v_permlane32_swap_b32_e32 v61, v63
	v_cndmask_b32_e64 v61, v61, v63, s[8:9]
	v_cndmask_b32_e64 v61, v61, v62, s[6:7]
	v_mul_f32_e32 v60, v58, v60
	v_fma_f32 v61, v58, v61, v59
	v_cndmask_b32_e64 v60, v60, v58, s[16:17]
	v_cndmask_b32_e64 v61, v61, v59, s[16:17]
	v_mov_b32_e32 v58, v60
	v_mov_b32_e32 v59, v60
	s_nop 1
	v_permlane32_swap_b32_e32 v58, v59
	v_cndmask_b32_e64 v58, v58, v59, s[8:9]
	v_mov_b32_e32 v59, v61
	v_mov_b32_e32 v62, v61
	s_nop 1
	v_permlane32_swap_b32_e32 v59, v62
	v_cndmask_b32_e64 v59, v59, v62, s[8:9]
	v_fma_f32 v59, v60, v59, v61
	v_mul_f32_e32 v58, v60, v58
	v_cndmask_b32_e64 v61, v61, v59, s[18:19]
	v_cndmask_b32_e64 v60, v60, v58, s[18:19]
	v_mov_b32_e32 v198, v60
	v_mov_b32_e32 v201, v61
	s_nop 0
	v_permlane16_swap_b32_e32 v60, v198
	v_permlane16_swap_b32_e32 v61, v201
	v_cndmask_b32_e64 v199, v60, v198, s[6:7]
	v_cndmask_b32_e64 v202, v61, v201, s[6:7]
	v_mov_b32_e32 v200, v199
	v_mov_b32_e32 v203, v202
	s_nop 0
	v_permlane32_swap_b32_e32 v199, v200
	v_permlane32_swap_b32_e32 v202, v203
	s_and_saveexec_b64 s[0:1], s[10:11]
	ds_write_b64 v124, v[58:59] offset:51200
	s_or_b64 exec, exec, s[0:1]
	v_add_u32_e32 v58, v99, v81
	ds_read_b128 v[58:61], v58
	v_add_u32_e32 v204, v99, v82
	v_add_u32_e32 v62, v100, v81
	ds_read_b32 v209, v101 offset:1024
	ds_read_b128 v[204:207], v204
	ds_read_b128 v[62:65], v62
	s_waitcnt lgkmcnt(3)
; __device__ __forceinline__ void ph_lru(const Ptrs& P, unsigned char* lds, int mode, int item0) {
;     ...
;             for (int ct = 0; ct < 4; ++ct) {
;                 const int e = 16 * ct + fr, ky = (e >> 1) & 7;
;                 const bf16x8 wa0 = *(const bf16x8*)(wa + e * 128 + ((fq ^ ky) << 4)), wa1 = *(const bf16x8*)(wa + e * 128 + (((4 + fq) ^ ky) << 4));
;                 const bf16x8 wx0 = *(const bf16x8*)(wx + e * 128 + ((fq ^ ky) << 4)), wx1 = *(const bf16x8*)(wx + e * 128 + (((4 + fq) ^ ky) << 4));
;                 f32x4 ga = {0.f, 0.f, 0.f, 0.f}, gx = {0.f, 0.f, 0.f, 0.f};
;                 ga = __builtin_amdgcn_mfma_f32_16x16x32_bf16(af0, wa0, ga, 0, 0, 0); ga = __builtin_amdgcn_mfma_f32_16x16x32_bf16(af1, wa1, ga, 0, 0, 0);
;                 gx = __builtin_amdgcn_mfma_f32_16x16x32_bf16(af0, wx0, gx, 0, 0, 0); gx = __builtin_amdgcn_mfma_f32_16x16x32_bf16(af1, wx1, gx, 0, 0, 0);
;                 const float bav = GBL[dir * 64 + e], bxv = GBL[128 + dir * 64 + e], c8 = GBL[256 + dir * 64 + e];
; #pragma unroll
;                 for (int j = 0; j < 4; ++j) {
;                     const float r = fsigmoid(ga[j] + bav), ig = fsigmoid(gx[j] + bxv);
;                     const float a = __builtin_amdgcn_exp2f(-c8 * r);
;                     av[dir][ct][j] = a; uv[dir][ct][j] = sqrtf(fmaxf(1.f - a * a, 0.f)) * ig * X[(16 * wid + 4 * fq + j) * 68 + e];
;                 }
;                 float Al = av[dir][ct][0] * av[dir][ct][1] * av[dir][ct][2] * av[dir][ct][3], Hl;
;                 if (dir == 0) Hl = ((uv[dir][ct][0] * av[dir][ct][1] + uv[dir][ct][1]) * av[dir][ct][2] + uv[dir][ct][2]) * av[dir][ct][3] + uv[dir][ct][3];
;                 else Hl = ((uv[dir][ct][3] * av[dir][ct][2] + uv[dir][ct][2]) * av[dir][ct][1] + uv[dir][ct][1]) * av[dir][ct][0] + uv[dir][ct][0];
;                 const int pq = dir == 0 ? fq : 3 - fq;
;                 {
;                     const float Ap = lane_shift16(Al, dir == 0), Hp = lane_shift16(Hl, dir == 0);
;                     if (pq >= 1) { Hl = Al * Hp + Hl; Al = Al * Ap; }
;                 }
;                 {
;                     const float Ap = lane_xor32(Al), Hp = lane_xor32(Hl);
;                     if (pq >= 2) { Hl = Al * Hp + Hl; Al = Al * Ap; }
;                 }
;                 {
;                     const float Ap = lane_shift16(Al, dir == 0), Hp = lane_shift16(Hl, dir == 0);
	v_mfma_f32_16x16x32_bf16 v[58:61], v[54:57], v[58:61], 0
	ds_read2st64_b32 v[210:211], v101 offset1:2
	v_add_u32_e32 v208, v100, v82
	s_waitcnt lgkmcnt(2)
	v_mfma_f32_16x16x32_bf16 v[58:61], v[50:53], v[204:207], v[58:61]
	ds_read_b128 v[204:207], v208
	s_waitcnt lgkmcnt(2)
	v_mfma_f32_16x16x32_bf16 v[62:65], v[54:57], v[62:65], 0
	s_waitcnt lgkmcnt(0)
	v_mfma_f32_16x16x32_bf16 v[62:65], v[50:53], v[204:207], v[62:65]
	s_nop 2
	v_add_f32_e32 v58, v58, v210
	v_mul_f32_e32 v58, 0xbfb8aa3b, v58
	v_exp_f32_e32 v58, v58
	v_add_f32_e32 v59, v59, v210
	v_mul_f32_e32 v59, 0xbfb8aa3b, v59
	v_add_f32_e32 v62, v62, v211
	v_add_f32_e32 v58, 1.0, v58
	v_rcp_f32_e32 v58, v58
	v_exp_f32_e32 v59, v59
	v_add_f32_e32 v63, v63, v211
	v_mul_f32_e32 v63, 0xbfb8aa3b, v63
	v_mul_f32_e64 v58, v58, -v209
	v_exp_f32_e32 v204, v58
	v_mul_f32_e32 v58, 0xbfb8aa3b, v62
	v_add_f32_e32 v59, 1.0, v59
	v_exp_f32_e32 v58, v58
	v_fma_f32 v62, -v204, v204, 1.0
	v_max_f32_e32 v62, 0, v62
	v_add_f32_e32 v58, 1.0, v58
	v_rcp_f32_e32 v58, v58
	v_sqrt_f32_e32 v205, v62
	v_add_f32_e32 v60, v60, v210
	v_exp_f32_e32 v63, v63
	v_mul_f32_e32 v60, 0xbfb8aa3b, v60
	v_add_u32_e32 v206, -1, v205
	v_add_u32_e32 v207, 1, v205
	v_fma_f32 v208, -v206, v205, v62
	v_fma_f32 v212, -v207, v205, v62
	v_cmp_ge_f32_e64 s[0:1], 0, v208
	v_exp_f32_e32 v60, v60
	v_add_f32_e32 v61, v61, v210
	v_cndmask_b32_e64 v205, v205, v206, s[0:1]
	v_cmp_lt_f32_e64 s[0:1], 0, v212
	v_add_f32_e32 v60, 1.0, v60
	v_rcp_f32_e32 v60, v60
	v_cndmask_b32_e64 v205, v205, v207, s[0:1]
	v_rcp_f32_e32 v206, v59
	v_mul_f32_e64 v60, v60, -v209
	v_mul_f32_e32 v61, 0xbfb8aa3b, v61
	v_mov_b32_e32 v59, v205
	v_mul_f32_e64 v205, v206, -v209
	v_exp_f32_e32 v205, v205
	v_mul_f32_e32 v62, v58, v59
	ds_read2_b32 v[58:59], v130 offset0:16 offset1:84
	v_exp_f32_e32 v61, v61
	v_fma_f32 v206, -v205, v205, 1.0
	v_max_f32_e32 v206, 0, v206
	v_mov_b32_e32 v207, v206
	v_sqrt_f32_e32 v208, v207
	s_waitcnt lgkmcnt(0)
	v_mul_f32_e32 v206, v58, v62
	v_add_f32_e32 v58, 1.0, v63
	v_rcp_f32_e32 v58, v58
	v_add_u32_e32 v62, -1, v208
	v_fma_f32 v63, -v62, v208, v207
	v_cmp_ge_f32_e64 s[0:1], 0, v63
	v_add_u32_e32 v63, 1, v208
	s_nop 0
	v_cndmask_b32_e64 v62, v208, v62, s[0:1]
	v_fma_f32 v208, -v63, v208, v207
	v_cmp_lt_f32_e64 s[0:1], 0, v208
	s_nop 1
	v_cndmask_b32_e64 v62, v62, v63, s[0:1]
	v_exp_f32_e32 v207, v60
	v_mul_f32_e32 v58, v58, v62
	v_add_f32_e32 v60, v64, v211
	v_mul_f32_e32 v60, 0xbfb8aa3b, v60
	v_fma_f32 v62, -v207, v207, 1.0
	v_max_f32_e32 v62, 0, v62
	v_exp_f32_e32 v60, v60
	v_mul_f32_e32 v208, v59, v58
	v_sqrt_f32_e32 v63, v62
	v_add_f32_e32 v58, 1.0, v60
	v_rcp_f32_e32 v58, v58
	v_add_u32_e32 v59, -1, v63
	v_fma_f32 v60, -v59, v63, v62
	v_cmp_ge_f32_e64 s[0:1], 0, v60
	v_add_u32_e32 v60, 1, v63
	s_nop 0
	v_cndmask_b32_e64 v59, v63, v59, s[0:1]
	v_fma_f32 v63, -v60, v63, v62
	v_cmp_lt_f32_e64 s[0:1], 0, v63
	s_nop 1
	v_cndmask_b32_e64 v59, v59, v60, s[0:1]
	v_add_f32_e32 v60, 1.0, v61
	v_rcp_f32_e32 v60, v60
	s_nop 0
	v_mul_f32_e64 v60, v60, -v209
	v_exp_f32_e32 v209, v60
	v_add_f32_e32 v60, v65, v211
	v_mul_f32_e32 v61, v58, v59
	v_fma_f32 v62, -v209, v209, 1.0
	v_max_f32_e32 v62, 0, v62
	ds_read2_b32 v[58:59], v130 offset0:152 offset1:220
	v_mul_f32_e32 v60, 0xbfb8aa3b, v60
	v_exp_f32_e32 v60, v60
	v_sqrt_f32_e32 v63, v62
	s_waitcnt lgkmcnt(0)
	v_mul_f32_e32 v210, v58, v61
	v_add_f32_e32 v58, 1.0, v60
	v_add_u32_e32 v60, -1, v63
	v_fma_f32 v61, -v60, v63, v62
	v_cmp_ge_f32_e64 s[0:1], 0, v61
	v_add_u32_e32 v61, 1, v63
	v_rcp_f32_e32 v58, v58
	v_cndmask_b32_e64 v60, v63, v60, s[0:1]
	v_fma_f32 v63, -v61, v63, v62
	v_cmp_lt_f32_e64 s[0:1], 0, v63
	s_nop 1
	v_cndmask_b32_e64 v60, v60, v61, s[0:1]
	v_mul_f32_e32 v58, v58, v60
	v_mul_f32_e32 v211, v59, v58
	v_mul_f32_e32 v58, v204, v205
	v_mul_f32_e32 v58, v207, v58
	v_mul_f32_e32 v58, v209, v58
	v_mov_b32_e32 v60, v58
	v_mov_b32_e32 v61, v58
	s_nop 1
	v_permlane16_swap_b32_e32 v60, v61
	v_cndmask_b32_e64 v60, v60, v61, s[6:7]
	v_fma_f32 v59, v207, v211, v210
	v_mov_b32_e32 v62, v60
	v_fma_f32 v59, v205, v59, v208
	s_nop 0
	v_permlane32_swap_b32_e32 v60, v62
	v_fma_f32 v59, v204, v59, v206
	v_cndmask_b32_e64 v60, v60, v62, s[8:9]
	v_cndmask_b32_e64 v60, v60, v61, s[6:7]
	v_mov_b32_e32 v61, v59
	v_mov_b32_e32 v62, v59
	s_nop 1
	v_permlane16_swap_b32_e32 v61, v62
	v_cndmask_b32_e64 v61, v61, v62, s[6:7]
	v_mov_b32_e32 v63, v61
	s_nop 1
	v_permlane32_swap_b32_e32 v61, v63
	v_cndmask_b32_e64 v61, v61, v63, s[8:9]
	v_cndmask_b32_e64 v61, v61, v62, s[6:7]
	v_mul_f32_e32 v60, v58, v60
	v_fma_f32 v61, v58, v61, v59
	v_cndmask_b32_e64 v60, v60, v58, s[16:17]
	v_cndmask_b32_e64 v61, v61, v59, s[16:17]
	v_mov_b32_e32 v58, v60
	v_mov_b32_e32 v59, v60
	s_nop 1
	v_permlane32_swap_b32_e32 v58, v59
	v_cndmask_b32_e64 v58, v58, v59, s[8:9]
	v_mov_b32_e32 v59, v61
	v_mov_b32_e32 v62, v61
	s_nop 1
	v_permlane32_swap_b32_e32 v59, v62
	v_cndmask_b32_e64 v59, v59, v62, s[8:9]
	v_fma_f32 v59, v60, v59, v61
	v_mul_f32_e32 v58, v60, v58
	v_cndmask_b32_e64 v61, v61, v59, s[18:19]
	v_cndmask_b32_e64 v60, v60, v58, s[18:19]
	v_mov_b32_e32 v212, v60
	v_mov_b32_e32 v215, v61
	s_nop 0
	v_permlane16_swap_b32_e32 v60, v212
	v_permlane16_swap_b32_e32 v61, v215
	v_cndmask_b32_e64 v213, v60, v212, s[6:7]
	v_cndmask_b32_e64 v216, v61, v215, s[6:7]
	v_mov_b32_e32 v214, v213
	v_mov_b32_e32 v217, v216
	s_nop 0
	v_permlane32_swap_b32_e32 v213, v214
	v_permlane32_swap_b32_e32 v216, v217
	s_and_saveexec_b64 s[0:1], s[10:11]
	ds_write_b64 v125, v[58:59] offset:51200
	s_or_b64 exec, exec, s[0:1]
	v_add_u32_e32 v58, v102, v81
	ds_read_b128 v[58:61], v58
	v_add_u32_e32 v218, v102, v82
	v_add_u32_e32 v62, v103, v81
	ds_read_b32 v223, v104 offset:1024
	ds_read_b128 v[218:221], v218
	ds_read_b128 v[62:65], v62
	s_waitcnt lgkmcnt(3)
; __device__ __forceinline__ void ph_lru(const Ptrs& P, unsigned char* lds, int mode, int item0) {
;     ...
;             for (int ct = 0; ct < 4; ++ct) {
;                 const int e = 16 * ct + fr, ky = (e >> 1) & 7;
;                 const bf16x8 wa0 = *(const bf16x8*)(wa + e * 128 + ((fq ^ ky) << 4)), wa1 = *(const bf16x8*)(wa + e * 128 + (((4 + fq) ^ ky) << 4));
;                 const bf16x8 wx0 = *(const bf16x8*)(wx + e * 128 + ((fq ^ ky) << 4)), wx1 = *(const bf16x8*)(wx + e * 128 + (((4 + fq) ^ ky) << 4));
;                 f32x4 ga = {0.f, 0.f, 0.f, 0.f}, gx = {0.f, 0.f, 0.f, 0.f};
;                 ga = __builtin_amdgcn_mfma_f32_16x16x32_bf16(af0, wa0, ga, 0, 0, 0); ga = __builtin_amdgcn_mfma_f32_16x16x32_bf16(af1, wa1, ga, 0, 0, 0);
;                 gx = __builtin_amdgcn_mfma_f32_16x16x32_bf16(af0, wx0, gx, 0, 0, 0); gx = __builtin_amdgcn_mfma_f32_16x16x32_bf16(af1, wx1, gx, 0, 0, 0);
;                 const float bav = GBL[dir * 64 + e], bxv = GBL[128 + dir * 64 + e], c8 = GBL[256 + dir * 64 + e];
; #pragma unroll
;                 for (int j = 0; j < 4; ++j) {
;                     const float r = fsigmoid(ga[j] + bav), ig = fsigmoid(gx[j] + bxv);
;                     const float a = __builtin_amdgcn_exp2f(-c8 * r);
;                     av[dir][ct][j] = a; uv[dir][ct][j] = sqrtf(fmaxf(1.f - a * a, 0.f)) * ig * X[(16 * wid + 4 * fq + j) * 68 + e];
;                 }
;                 float Al = av[dir][ct][0] * av[dir][ct][1] * av[dir][ct][2] * av[dir][ct][3], Hl;
;                 if (dir == 0) Hl = ((uv[dir][ct][0] * av[dir][ct][1] + uv[dir][ct][1]) * av[dir][ct][2] + uv[dir][ct][2]) * av[dir][ct][3] + uv[dir][ct][3];
;                 else Hl = ((uv[dir][ct][3] * av[dir][ct][2] + uv[dir][ct][2]) * av[dir][ct][1] + uv[dir][ct][1]) * av[dir][ct][0] + uv[dir][ct][0];
;                 const int pq = dir == 0 ? fq : 3 - fq;
;                 {
;                     const float Ap = lane_shift16(Al, dir == 0), Hp = lane_shift16(Hl, dir == 0);
;                     if (pq >= 1) { Hl = Al * Hp + Hl; Al = Al * Ap; }
;                 }
;                 {
;                     const float Ap = lane_xor32(Al), Hp = lane_xor32(Hl);
;                     if (pq >= 2) { Hl = Al * Hp + Hl; Al = Al * Ap; }
;                 }
;                 {
;                     const float Ap = lane_shift16(Al, dir == 0), Hp = lane_shift16(Hl, dir == 0);
	v_mfma_f32_16x16x32_bf16 v[58:61], v[54:57], v[58:61], 0
	ds_read2st64_b32 v[224:225], v104 offset1:2
	v_add_u32_e32 v222, v103, v82
	s_waitcnt lgkmcnt(2)
	v_mfma_f32_16x16x32_bf16 v[58:61], v[50:53], v[218:221], v[58:61]
	ds_read_b128 v[218:221], v222
	s_waitcnt lgkmcnt(2)
	v_mfma_f32_16x16x32_bf16 v[62:65], v[54:57], v[62:65], 0
	s_waitcnt lgkmcnt(0)
	v_mfma_f32_16x16x32_bf16 v[62:65], v[50:53], v[218:221], v[62:65]
	s_nop 2
	v_add_f32_e32 v58, v58, v224
	v_mul_f32_e32 v58, 0xbfb8aa3b, v58
	v_exp_f32_e32 v58, v58
	v_add_f32_e32 v59, v59, v224
	v_mul_f32_e32 v59, 0xbfb8aa3b, v59
	v_add_f32_e32 v62, v62, v225
	v_add_f32_e32 v58, 1.0, v58
	v_rcp_f32_e32 v58, v58
	v_exp_f32_e32 v59, v59
	v_add_f32_e32 v63, v63, v225
	v_mul_f32_e32 v63, 0xbfb8aa3b, v63
	v_mul_f32_e64 v58, v58, -v223
	v_exp_f32_e32 v218, v58
	v_mul_f32_e32 v58, 0xbfb8aa3b, v62
	v_add_f32_e32 v59, 1.0, v59
	v_exp_f32_e32 v58, v58
	v_fma_f32 v62, -v218, v218, 1.0
	v_max_f32_e32 v62, 0, v62
	v_add_f32_e32 v58, 1.0, v58
	v_rcp_f32_e32 v58, v58
	v_sqrt_f32_e32 v219, v62
	v_add_f32_e32 v60, v60, v224
	v_exp_f32_e32 v63, v63
	v_mul_f32_e32 v60, 0xbfb8aa3b, v60
	v_add_u32_e32 v220, -1, v219
	v_add_u32_e32 v221, 1, v219
	v_fma_f32 v222, -v220, v219, v62
	v_fma_f32 v226, -v221, v219, v62
	v_cmp_ge_f32_e64 s[0:1], 0, v222
	v_exp_f32_e32 v60, v60
	v_add_f32_e32 v61, v61, v224
	v_cndmask_b32_e64 v219, v219, v220, s[0:1]
	v_cmp_lt_f32_e64 s[0:1], 0, v226
	v_add_f32_e32 v60, 1.0, v60
	v_rcp_f32_e32 v60, v60
	v_cndmask_b32_e64 v219, v219, v221, s[0:1]
	v_rcp_f32_e32 v220, v59
	v_mul_f32_e64 v60, v60, -v223
	v_mul_f32_e32 v61, 0xbfb8aa3b, v61
	v_mov_b32_e32 v59, v219
	v_mul_f32_e64 v219, v220, -v223
	v_exp_f32_e32 v219, v219
	v_mul_f32_e32 v62, v58, v59
	ds_read2_b32 v[58:59], v130 offset0:32 offset1:100
	v_exp_f32_e32 v61, v61
	v_fma_f32 v220, -v219, v219, 1.0
	v_max_f32_e32 v220, 0, v220
	v_mov_b32_e32 v221, v220
	v_sqrt_f32_e32 v222, v221
	s_waitcnt lgkmcnt(0)
	v_mul_f32_e32 v220, v58, v62
	v_add_f32_e32 v58, 1.0, v63
	v_rcp_f32_e32 v58, v58
	v_add_u32_e32 v62, -1, v222
	v_fma_f32 v63, -v62, v222, v221
	v_cmp_ge_f32_e64 s[0:1], 0, v63
	v_add_u32_e32 v63, 1, v222
	s_nop 0
	v_cndmask_b32_e64 v62, v222, v62, s[0:1]
	v_fma_f32 v222, -v63, v222, v221
	v_cmp_lt_f32_e64 s[0:1], 0, v222
	s_nop 1
	v_cndmask_b32_e64 v62, v62, v63, s[0:1]
	v_exp_f32_e32 v221, v60
	v_mul_f32_e32 v58, v58, v62
	v_add_f32_e32 v60, v64, v225
	v_mul_f32_e32 v60, 0xbfb8aa3b, v60
	v_fma_f32 v62, -v221, v221, 1.0
	v_max_f32_e32 v62, 0, v62
	v_exp_f32_e32 v60, v60
	v_mul_f32_e32 v222, v59, v58
	v_sqrt_f32_e32 v63, v62
	v_add_f32_e32 v58, 1.0, v60
	v_rcp_f32_e32 v58, v58
	v_add_u32_e32 v59, -1, v63
	v_fma_f32 v60, -v59, v63, v62
	v_cmp_ge_f32_e64 s[0:1], 0, v60
	v_add_u32_e32 v60, 1, v63
	s_nop 0
	v_cndmask_b32_e64 v59, v63, v59, s[0:1]
	v_fma_f32 v63, -v60, v63, v62
	v_cmp_lt_f32_e64 s[0:1], 0, v63
	s_nop 1
	v_cndmask_b32_e64 v59, v59, v60, s[0:1]
	v_add_f32_e32 v60, 1.0, v61
	v_rcp_f32_e32 v60, v60
	s_nop 0
	v_mul_f32_e64 v60, v60, -v223
	v_exp_f32_e32 v223, v60
	v_add_f32_e32 v60, v65, v225
	v_mul_f32_e32 v61, v58, v59
	v_fma_f32 v62, -v223, v223, 1.0
	v_max_f32_e32 v62, 0, v62
	ds_read2_b32 v[58:59], v130 offset0:168 offset1:236
	v_mul_f32_e32 v60, 0xbfb8aa3b, v60
	v_exp_f32_e32 v60, v60
	v_sqrt_f32_e32 v63, v62
	s_waitcnt lgkmcnt(0)
	v_mul_f32_e32 v224, v58, v61
	v_add_f32_e32 v58, 1.0, v60
	v_add_u32_e32 v60, -1, v63
	v_fma_f32 v61, -v60, v63, v62
	v_cmp_ge_f32_e64 s[0:1], 0, v61
	v_add_u32_e32 v61, 1, v63
	v_rcp_f32_e32 v58, v58
	v_cndmask_b32_e64 v60, v63, v60, s[0:1]
	v_fma_f32 v63, -v61, v63, v62
	v_cmp_lt_f32_e64 s[0:1], 0, v63
	s_nop 1
	v_cndmask_b32_e64 v60, v60, v61, s[0:1]
	v_mul_f32_e32 v58, v58, v60
	v_mul_f32_e32 v225, v59, v58
	v_mul_f32_e32 v58, v218, v219
	v_mul_f32_e32 v58, v221, v58
	v_mul_f32_e32 v58, v223, v58
	v_mov_b32_e32 v60, v58
	v_mov_b32_e32 v61, v58
	s_nop 1
	v_permlane16_swap_b32_e32 v60, v61
	v_cndmask_b32_e64 v60, v60, v61, s[6:7]
	v_fma_f32 v59, v221, v225, v224
	v_mov_b32_e32 v62, v60
	v_fma_f32 v59, v219, v59, v222
	s_nop 0
	v_permlane32_swap_b32_e32 v60, v62
	v_fma_f32 v59, v218, v59, v220
	v_cndmask_b32_e64 v60, v60, v62, s[8:9]
	v_cndmask_b32_e64 v60, v60, v61, s[6:7]
	v_mov_b32_e32 v61, v59
	v_mov_b32_e32 v62, v59
	s_nop 1
	v_permlane16_swap_b32_e32 v61, v62
	v_cndmask_b32_e64 v61, v61, v62, s[6:7]
	v_mov_b32_e32 v63, v61
	s_nop 1
	v_permlane32_swap_b32_e32 v61, v63
	v_cndmask_b32_e64 v61, v61, v63, s[8:9]
	v_cndmask_b32_e64 v61, v61, v62, s[6:7]
	v_mul_f32_e32 v60, v58, v60
	v_fma_f32 v61, v58, v61, v59
	v_cndmask_b32_e64 v60, v60, v58, s[16:17]
	v_cndmask_b32_e64 v61, v61, v59, s[16:17]
	v_mov_b32_e32 v58, v60
	v_mov_b32_e32 v59, v60
	s_nop 1
	v_permlane32_swap_b32_e32 v58, v59
	v_cndmask_b32_e64 v58, v58, v59, s[8:9]
	v_mov_b32_e32 v59, v61
	v_mov_b32_e32 v62, v61
	s_nop 1
	v_permlane32_swap_b32_e32 v59, v62
	v_cndmask_b32_e64 v59, v59, v62, s[8:9]
	v_fma_f32 v59, v60, v59, v61
	v_mul_f32_e32 v58, v60, v58
	v_cndmask_b32_e64 v61, v61, v59, s[18:19]
	v_cndmask_b32_e64 v60, v60, v58, s[18:19]
	v_mov_b32_e32 v228, v60
	v_mov_b32_e32 v232, v61
	s_nop 0
	v_permlane16_swap_b32_e32 v60, v228
	v_permlane16_swap_b32_e32 v61, v232
	v_cndmask_b32_e64 v230, v60, v228, s[6:7]
	v_cndmask_b32_e64 v233, v61, v232, s[6:7]
	v_mov_b32_e32 v231, v230
	v_mov_b32_e32 v234, v233
	s_nop 0
	v_permlane32_swap_b32_e32 v230, v231
	v_permlane32_swap_b32_e32 v233, v234
	s_and_saveexec_b64 s[0:1], s[10:11]
	ds_write_b64 v126, v[58:59] offset:51200
	s_or_b64 exec, exec, s[0:1]
	v_add_u32_e32 v58, v105, v81
	v_add_u32_e32 v62, v106, v81
	ds_read_b128 v[58:61], v58
	ds_read_b128 v[62:65], v62
	v_add_u32_e32 v226, v105, v82
	ds_read_b32 v237, v107 offset:1024
	s_waitcnt lgkmcnt(2)
; __device__ __forceinline__ void ph_lru(const Ptrs& P, unsigned char* lds, int mode, int item0) {
;     ...
;                 const bf16x8 wa0 = *(const bf16x8*)(wa + e * 128 + ((fq ^ ky) << 4)), wa1 = *(const bf16x8*)(wa + e * 128 + (((4 + fq) ^ ky) << 4));
;                 const bf16x8 wx0 = *(const bf16x8*)(wx + e * 128 + ((fq ^ ky) << 4)), wx1 = *(const bf16x8*)(wx + e * 128 + (((4 + fq) ^ ky) << 4));
;                 f32x4 ga = {0.f, 0.f, 0.f, 0.f}, gx = {0.f, 0.f, 0.f, 0.f};
;                 ga = __builtin_amdgcn_mfma_f32_16x16x32_bf16(af0, wa0, ga, 0, 0, 0); ga = __builtin_amdgcn_mfma_f32_16x16x32_bf16(af1, wa1, ga, 0, 0, 0);
;                 gx = __builtin_amdgcn_mfma_f32_16x16x32_bf16(af0, wx0, gx, 0, 0, 0); gx = __builtin_amdgcn_mfma_f32_16x16x32_bf16(af1, wx1, gx, 0, 0, 0);
;                 const float bav = GBL[dir * 64 + e], bxv = GBL[128 + dir * 64 + e], c8 = GBL[256 + dir * 64 + e];
; #pragma unroll
;                 for (int j = 0; j < 4; ++j) {
;                     const float r = fsigmoid(ga[j] + bav), ig = fsigmoid(gx[j] + bxv);
;                     const float a = __builtin_amdgcn_exp2f(-c8 * r);
;                     av[dir][ct][j] = a; uv[dir][ct][j] = sqrtf(fmaxf(1.f - a * a, 0.f)) * ig * X[(16 * wid + 4 * fq + j) * 68 + e];
;                 }
;                 float Al = av[dir][ct][0] * av[dir][ct][1] * av[dir][ct][2] * av[dir][ct][3], Hl;
;                 if (dir == 0) Hl = ((uv[dir][ct][0] * av[dir][ct][1] + uv[dir][ct][1]) * av[dir][ct][2] + uv[dir][ct][2]) * av[dir][ct][3] + uv[dir][ct][3];
;                 else Hl = ((uv[dir][ct][3] * av[dir][ct][2] + uv[dir][ct][2]) * av[dir][ct][1] + uv[dir][ct][1]) * av[dir][ct][0] + uv[dir][ct][0];
;                 const int pq = dir == 0 ? fq : 3 - fq;
;                 {
;                     const float Ap = lane_shift16(Al, dir == 0), Hp = lane_shift16(Hl, dir == 0);
;                     if (pq >= 1) { Hl = Al * Hp + Hl; Al = Al * Ap; }
;                 }
;                 {
;                     const float Ap = lane_xor32(Al), Hp = lane_xor32(Hl);
;                     if (pq >= 2) { Hl = Al * Hp + Hl; Al = Al * Ap; }
;                 }
;                 {
;                     const float Ap = lane_shift16(Al, dir == 0), Hp = lane_shift16(Hl, dir == 0);
;                     Ae[dir][ct] = pq >= 1 ? Ap : 1.f; He[dir][ct] = pq >= 1 ? Hp : 0.f;
;                 }
	v_mfma_f32_16x16x32_bf16 v[58:61], v[54:57], v[58:61], 0
	ds_read2st64_b32 v[238:239], v107 offset1:2
	s_waitcnt lgkmcnt(2)
	v_mfma_f32_16x16x32_bf16 v[54:57], v[54:57], v[62:65], 0
	ds_read_b128 v[62:65], v226
	v_add_u32_e32 v226, v106, v82
	s_waitcnt lgkmcnt(0)
	v_mfma_f32_16x16x32_bf16 v[58:61], v[50:53], v[62:65], v[58:61]
	ds_read_b128 v[62:65], v226
	s_waitcnt lgkmcnt(0)
	v_mfma_f32_16x16x32_bf16 v[50:53], v[50:53], v[62:65], v[54:57]
	s_nop 4
	v_add_f32_e32 v58, v58, v238
	v_mul_f32_e32 v58, 0xbfb8aa3b, v58
	v_exp_f32_e32 v58, v58
	v_add_f32_e32 v54, v59, v238
	v_mul_f32_e32 v54, 0xbfb8aa3b, v54
	v_exp_f32_e32 v54, v54
	v_add_f32_e32 v58, 1.0, v58
	v_rcp_f32_e32 v58, v58
	v_add_f32_e32 v50, v50, v239
	v_add_f32_e32 v54, 1.0, v54
	v_mul_f32_e32 v50, 0xbfb8aa3b, v50
	v_mul_f32_e64 v55, v58, -v237
	v_exp_f32_e32 v226, v55
	v_exp_f32_e32 v50, v50
	v_add_f32_e32 v51, v51, v239
	v_mul_f32_e32 v51, 0xbfb8aa3b, v51
	v_fma_f32 v55, -v226, v226, 1.0
	v_max_f32_e32 v55, 0, v55
	v_add_f32_e32 v50, 1.0, v50
	v_rcp_f32_e32 v50, v50
	v_sqrt_f32_e32 v56, v55
	v_exp_f32_e32 v51, v51
	v_add_f32_e32 v53, v53, v239
	v_mul_f32_e32 v53, 0xbfb8aa3b, v53
	v_add_u32_e32 v57, -1, v56
	v_add_u32_e32 v58, 1, v56
	v_fma_f32 v59, -v57, v56, v55
	v_fma_f32 v62, -v58, v56, v55
	v_cmp_ge_f32_e64 s[0:1], 0, v59
	v_exp_f32_e32 v53, v53
	s_nop 0
	v_cndmask_b32_e64 v56, v56, v57, s[0:1]
	v_cmp_lt_f32_e64 s[0:1], 0, v62
	s_nop 1
	v_cndmask_b32_e64 v56, v56, v58, s[0:1]
	v_rcp_f32_e32 v57, v54
	v_add_f32_e32 v58, v60, v238
	v_mul_f32_e32 v58, 0xbfb8aa3b, v58
	v_mov_b32_e32 v54, v56
	v_mul_f32_e64 v56, v57, -v237
	v_exp_f32_e32 v227, v56
	v_mul_f32_e32 v50, v50, v54
	ds_read2_b32 v[54:55], v130 offset0:48 offset1:116
	v_exp_f32_e32 v58, v58
	v_fma_f32 v56, -v227, v227, 1.0
	v_max_f32_e32 v56, 0, v56
	s_waitcnt lgkmcnt(0)
	v_mul_f32_e32 v229, v54, v50
	v_add_f32_e32 v50, 1.0, v51
	v_sqrt_f32_e32 v57, v56
	v_rcp_f32_e32 v50, v50
	v_add_u32_e32 v51, -1, v57
	v_fma_f32 v54, -v51, v57, v56
	v_cmp_ge_f32_e64 s[0:1], 0, v54
	v_add_u32_e32 v54, 1, v57
	s_nop 0
	v_cndmask_b32_e64 v51, v57, v51, s[0:1]
	v_fma_f32 v57, -v54, v57, v56
	v_cmp_lt_f32_e64 s[0:1], 0, v57
	s_nop 1
	v_cndmask_b32_e64 v51, v51, v54, s[0:1]
	v_add_f32_e32 v54, 1.0, v58
	v_rcp_f32_e32 v54, v54
	v_mul_f32_e32 v50, v50, v51
	v_mul_f32_e64 v51, v54, -v237
	v_exp_f32_e32 v235, v51
	v_add_f32_e32 v51, v52, v239
	v_mul_f32_e32 v51, 0xbfb8aa3b, v51
	v_exp_f32_e32 v51, v51
	v_fma_f32 v52, -v235, v235, 1.0
	v_max_f32_e32 v52, 0, v52
	v_mul_f32_e32 v236, v55, v50
	v_add_f32_e32 v50, 1.0, v51
	v_sqrt_f32_e32 v54, v52
	v_add_f32_e32 v56, v61, v238
	v_mul_f32_e32 v56, 0xbfb8aa3b, v56
	v_exp_f32_e32 v56, v56
	v_add_u32_e32 v51, -1, v54
	v_fma_f32 v55, -v51, v54, v52
	v_cmp_ge_f32_e64 s[0:1], 0, v55
	v_add_u32_e32 v55, 1, v54
	v_rcp_f32_e32 v50, v50
	v_cndmask_b32_e64 v51, v54, v51, s[0:1]
	v_fma_f32 v54, -v55, v54, v52
	v_cmp_lt_f32_e64 s[0:1], 0, v54
	s_nop 1
	v_cndmask_b32_e64 v51, v51, v55, s[0:1]
	v_add_f32_e32 v54, 1.0, v56
	v_rcp_f32_e32 v54, v54
	s_nop 0
	v_mul_f32_e64 v54, v54, -v237
	v_exp_f32_e32 v237, v54
	v_mul_f32_e32 v52, v50, v51
	ds_read2_b32 v[50:51], v130 offset0:184 offset1:252
	v_fma_f32 v54, -v237, v237, 1.0
	v_max_f32_e32 v54, 0, v54
	s_waitcnt lgkmcnt(0)
	v_mul_f32_e32 v238, v50, v52
	v_add_f32_e32 v50, 1.0, v53
	v_sqrt_f32_e32 v55, v54
	v_rcp_f32_e32 v50, v50
	v_add_u32_e32 v52, -1, v55
	v_fma_f32 v53, -v52, v55, v54
	v_cmp_ge_f32_e64 s[0:1], 0, v53
	v_add_u32_e32 v53, 1, v55
	s_nop 0
	v_cndmask_b32_e64 v52, v55, v52, s[0:1]
	v_fma_f32 v55, -v53, v55, v54
	v_cmp_lt_f32_e64 s[0:1], 0, v55
	s_nop 1
	v_cndmask_b32_e64 v52, v52, v53, s[0:1]
	v_mul_f32_e32 v50, v50, v52
	v_mul_f32_e32 v239, v51, v50
	v_mul_f32_e32 v50, v226, v227
	v_mul_f32_e32 v50, v235, v50
	v_mul_f32_e32 v50, v237, v50
	v_mov_b32_e32 v52, v50
	v_mov_b32_e32 v53, v50
	s_nop 1
	v_permlane16_swap_b32_e32 v52, v53
	v_cndmask_b32_e64 v52, v52, v53, s[6:7]
	v_fma_f32 v51, v235, v239, v238
	v_mov_b32_e32 v54, v52
	v_fma_f32 v51, v227, v51, v236
	s_nop 0
	v_permlane32_swap_b32_e32 v52, v54
	v_fma_f32 v51, v226, v51, v229
	v_cndmask_b32_e64 v52, v52, v54, s[8:9]
	v_cndmask_b32_e64 v52, v52, v53, s[6:7]
	v_mov_b32_e32 v53, v51
	v_mov_b32_e32 v54, v51
	s_nop 1
	v_permlane16_swap_b32_e32 v53, v54
	v_cndmask_b32_e64 v53, v53, v54, s[6:7]
	v_mov_b32_e32 v55, v53
	s_nop 1
	v_permlane32_swap_b32_e32 v53, v55
	v_cndmask_b32_e64 v53, v53, v55, s[8:9]
	v_cndmask_b32_e64 v53, v53, v54, s[6:7]
	v_mul_f32_e32 v52, v50, v52
	v_fma_f32 v53, v50, v53, v51
	v_cndmask_b32_e64 v52, v52, v50, s[16:17]
	v_cndmask_b32_e64 v53, v53, v51, s[16:17]
	v_mov_b32_e32 v50, v52
	v_mov_b32_e32 v51, v52
	s_nop 1
	v_permlane32_swap_b32_e32 v50, v51
	v_cndmask_b32_e64 v50, v50, v51, s[8:9]
	v_mov_b32_e32 v51, v53
	v_mov_b32_e32 v54, v53
	s_nop 1
	v_permlane32_swap_b32_e32 v51, v54
	v_cndmask_b32_e64 v51, v51, v54, s[8:9]
	v_fma_f32 v51, v52, v51, v53
	v_mul_f32_e32 v50, v52, v50
	v_cndmask_b32_e64 v53, v53, v51, s[18:19]
	v_cndmask_b32_e64 v52, v52, v50, s[18:19]
	v_mov_b32_e32 v240, v52
	v_mov_b32_e32 v243, v53
	s_nop 0
	v_permlane16_swap_b32_e32 v52, v240
	v_permlane16_swap_b32_e32 v53, v243
	v_cndmask_b32_e64 v241, v52, v240, s[6:7]
	v_cndmask_b32_e64 v244, v53, v243, s[6:7]
	v_mov_b32_e32 v242, v241
	v_mov_b32_e32 v245, v244
	s_nop 0
	v_permlane32_swap_b32_e32 v241, v242
	v_permlane32_swap_b32_e32 v244, v245
	s_and_saveexec_b64 s[0:1], s[10:11]
	ds_write_b64 v127, v[50:51] offset:51200
	s_or_b64 exec, exec, s[0:1]
	s_waitcnt lgkmcnt(0)
	s_barrier
	ds_read_b32 v53, v83 offset:59392
	s_and_saveexec_b64 s[0:1], s[12:13]
	s_cbranch_execz .LBB0_1155
	s_and_saveexec_b64 s[38:39], s[22:23]
	s_cbranch_execz .LBB0_1132
	s_mov_b32 s33, 0
	s_mov_b64 s[44:45], 0
	v_mov_b32_e32 v54, v108

; #define PSUB_AT(k) do { if (PROBE_SUB == (k) && DK == PROBE_SUBDK) sacc = __builtin_amdgcn_readfirstlane(sacc + ((unsigned)__builtin_readcyclecounter() - ps_t0_)); } while (0)
; #define SBAR() __builtin_amdgcn_sched_barrier(0)
; #define SLOAD(k0) do { const unsigned so_k = (unsigned)((k0) * ldk) * 2u, so_v = (unsigned)((k0) * ldv) * 2u; \
;         _Pragma("unroll") for (int i = 0; i < KP; ++i) ks[i] = __builtin_amdgcn_raw_buffer_load_b128(krs, kgo[i], so_k, 0); \
;         vs0 = __builtin_amdgcn_raw_buffer_load_b128(vrs, vgo, so_v, 0); vs1 = __builtin_amdgcn_raw_buffer_load_b128(vrs, vgo + vstep, so_v, 0); } while (0)
; template <int DK, bool PF, bool EARLY, bool PFD = false> ...
;     ...
;         if (EARLY && j + 1 < ntile) SLOAD((j + 1) * 64);
;         f32x16 p0, p1;
; #pragma unroll
;         for (int r = 0; r < 16; ++r) { p0[r] = negM; p1[r] = negM; }
;         const char* Kb = K_lds + cur * SHM_K;
; #pragma unroll
;         for (int d0 = 0; d0 < NQ; ++d0) {
;             const bf16x8 b0 = *reinterpret_cast<const bf16x8*>(Kb + kra_(d0 & 3) + (d0 >> 2) * 128);
;             const bf16x8 b1 = *reinterpret_cast<const bf16x8*>(Kb + kra_(d0 & 3) + (d0 >> 2) * 128 + 32 * DK * 2);
;             p0 = __builtin_amdgcn_mfma_f32_32x32x16_bf16(b0, qr[d0], p0, 0, 0, 0);
;             p1 = __builtin_amdgcn_mfma_f32_32x32x16_bf16(b1, qr[d0], p1, 0, 0, 0);
;             if ((d0 & 3) == 3) SBAR();
;         }
;         PSUB_AT(1);
;         if (!EARLY && j + 1 < ntile) SLOAD((j + 1) * 64);
;         float ps = 0.f, ps1 = 0.f;
; #pragma unroll
;         for (int r = 0; r < 16; ++r) { p0[r] = __builtin_amdgcn_exp2f(p0[r]); p1[r] = __builtin_amdgcn_exp2f(p1[r]); ps += p0[r]; asm("" : "+v"(ps)); ps1 += p1[r]; asm("" : "+v"(ps1)); }
;         l_reg += ps + ps1;
;         bf16x8 pa0, pa1, pa2, pa3;
;     ...
;         PK4(p0, 0, pa0); PK4(p0, 8, pa1); PK4(p1, 0, pa2); PK4(p1, 8, pa3);
;     ...
;         PSUB_AT(2);
;         const int vb = vb0 + cur * SHM_V;
;         pv_one<0>(o[0], vb, pa0, pa1, pa2, pa3); pv_one<1>(o[1], vb, pa0, pa1, pa2, pa3); pv_one<2>(o[2], vb, pa0, pa1, pa2, pa3); pv_one<3>(o[3], vb, pa0, pa1, pa2, pa3);
.LBB0_1200:
	s_and_b32 s23, s19, 1
	s_mul_i32 s24, s23, 0x6000
	v_add_u32_e32 v250, s24, v207
	v_add_u32_e32 v251, v250, v201
	v_add_u32_e32 v252, v250, v214
	v_add_u32_e32 v253, v250, v215
	v_add_u32_e32 v245, v250, v216
	ds_read_b128 v[162:165], v251 offset:32768
	ds_read_b128 v[166:169], v251 offset:45056
	ds_read_b128 v[170:173], v252 offset:32768
	ds_read_b128 v[174:177], v252 offset:45056
	ds_read_b128 v[178:181], v253 offset:32768
	ds_read_b128 v[246:249], v253 offset:45056
	s_waitcnt lgkmcnt(5)
	v_mfma_f32_32x32x16_bf16 v[98:113], v[162:165], v[158:161], v[66:81]
	ds_read_b128 v[162:165], v245 offset:32768
	s_waitcnt lgkmcnt(5)
	v_mfma_f32_32x32x16_bf16 v[82:97], v[166:169], v[158:161], v[66:81]
	ds_read_b128 v[166:169], v245 offset:45056
	s_waitcnt lgkmcnt(5)
	v_mfma_f32_32x32x16_bf16 v[98:113], v[170:173], v[154:157], v[98:113]
	ds_read_b128 v[170:173], v251 offset:32896
	s_waitcnt lgkmcnt(5)
	v_mfma_f32_32x32x16_bf16 v[82:97], v[174:177], v[154:157], v[82:97]
	ds_read_b128 v[174:177], v251 offset:45184
	s_waitcnt lgkmcnt(5)
	v_mfma_f32_32x32x16_bf16 v[98:113], v[178:181], v[150:153], v[98:113]
	ds_read_b128 v[178:181], v252 offset:32896
	s_waitcnt lgkmcnt(5)
	v_mfma_f32_32x32x16_bf16 v[82:97], v[246:249], v[150:153], v[82:97]
	ds_read_b128 v[246:249], v252 offset:45184
	s_waitcnt lgkmcnt(5)
	v_mfma_f32_32x32x16_bf16 v[98:113], v[162:165], v[146:149], v[98:113]
	ds_read_b128 v[162:165], v253 offset:32896
	s_waitcnt lgkmcnt(5)
	v_mfma_f32_32x32x16_bf16 v[82:97], v[166:169], v[146:149], v[82:97]
	ds_read_b128 v[166:169], v253 offset:45184
	s_waitcnt lgkmcnt(5)
	v_mfma_f32_32x32x16_bf16 v[98:113], v[170:173], v[142:145], v[98:113]
	ds_read_b128 v[170:173], v245 offset:32896
	s_waitcnt lgkmcnt(5)
	v_mfma_f32_32x32x16_bf16 v[82:97], v[174:177], v[142:145], v[82:97]
	ds_read_b128 v[174:177], v245 offset:45184
	s_waitcnt lgkmcnt(5)
	v_mfma_f32_32x32x16_bf16 v[98:113], v[178:181], v[138:141], v[98:113]
	ds_read_b128 v[178:181], v251 offset:33024
	s_waitcnt lgkmcnt(5)
	v_mfma_f32_32x32x16_bf16 v[82:97], v[246:249], v[138:141], v[82:97]
	ds_read_b128 v[246:249], v251 offset:45312
	s_waitcnt lgkmcnt(5)
	v_mfma_f32_32x32x16_bf16 v[98:113], v[162:165], v[134:137], v[98:113]
	ds_read_b128 v[162:165], v252 offset:33024
	s_waitcnt lgkmcnt(5)
	v_mfma_f32_32x32x16_bf16 v[82:97], v[166:169], v[134:137], v[82:97]
	ds_read_b128 v[166:169], v252 offset:45312
	s_waitcnt lgkmcnt(5)
	v_mfma_f32_32x32x16_bf16 v[98:113], v[170:173], v[130:133], v[98:113]
	ds_read_b128 v[170:173], v253 offset:33024
	s_waitcnt lgkmcnt(5)
	v_mfma_f32_32x32x16_bf16 v[82:97], v[174:177], v[130:133], v[82:97]
	ds_read_b128 v[174:177], v253 offset:45312
	s_waitcnt lgkmcnt(5)
	v_mfma_f32_32x32x16_bf16 v[98:113], v[178:181], v[126:129], v[98:113]
	ds_read_b128 v[178:181], v245 offset:33024
	s_waitcnt lgkmcnt(5)
	v_mfma_f32_32x32x16_bf16 v[82:97], v[246:249], v[126:129], v[82:97]
	ds_read_b128 v[246:249], v245 offset:45312
	s_waitcnt lgkmcnt(5)
	v_mfma_f32_32x32x16_bf16 v[98:113], v[162:165], v[122:125], v[98:113]
	s_waitcnt lgkmcnt(4)
	v_mfma_f32_32x32x16_bf16 v[82:97], v[166:169], v[122:125], v[82:97]
	s_waitcnt lgkmcnt(3)
	v_mfma_f32_32x32x16_bf16 v[98:113], v[170:173], v[118:121], v[98:113]
	s_waitcnt lgkmcnt(2)
	v_mfma_f32_32x32x16_bf16 v[82:97], v[174:177], v[118:121], v[82:97]
	s_waitcnt lgkmcnt(1)
	v_mfma_f32_32x32x16_bf16 v[98:113], v[178:181], v[114:117], v[98:113]
	s_waitcnt lgkmcnt(0)
	v_mfma_f32_32x32x16_bf16 v[82:97], v[246:249], v[114:117], v[82:97]
	buffer_load_dwordx4 v[166:169], v185, s[8:11], s20 offen
	buffer_load_dwordx4 v[162:165], v191, s[8:11], s20 offen
	buffer_load_dwordx4 v[178:181], v195, s[8:11], s20 offen
	buffer_load_dwordx4 v[170:173], v199, s[12:15], s21 offen
	buffer_load_dwordx4 v[174:177], v203, s[12:15], s21 offen
	s_lshl_b32 s33, s23, 14
	v_add_u32_e32 v245, s33, v209
	ds_read_b64_tr_b16 v[246:247], v245 offset:0x0
	ds_read_b64_tr_b16 v[248:249], v245 offset:0x800
	ds_read_b64_tr_b16 v[250:251], v245 offset:0x1000
	ds_read_b64_tr_b16 v[252:253], v245 offset:0x1800
	s_nop 1
	v_exp_f32_e32 v240, v82
	v_exp_f32_e32 v98, v98
	v_exp_f32_e32 v242, v83
	v_exp_f32_e32 v99, v99
	v_add_f32_e32 v241, 0, v240
	v_add_f32_e32 v82, 0, v98
	v_exp_f32_e32 v83, v100
	v_add_f32_e32 v100, v242, v241
	v_exp_f32_e32 v241, v84
	v_add_f32_e32 v82, v99, v82
	v_exp_f32_e32 v84, v101
	v_exp_f32_e32 v101, v85
	v_add_f32_e32 v82, v83, v82
	v_exp_f32_e32 v85, v102
	v_add_f32_e32 v100, v241, v100
	v_exp_f32_e32 v102, v86
	v_add_f32_e32 v82, v84, v82
	v_exp_f32_e32 v86, v103
	v_add_f32_e32 v100, v101, v100
	v_exp_f32_e32 v103, v87
	v_add_f32_e32 v82, v85, v82
	v_exp_f32_e32 v87, v104
	v_add_f32_e32 v100, v102, v100
	v_exp_f32_e32 v104, v88
	v_add_f32_e32 v82, v86, v82
	v_exp_f32_e32 v88, v105
	v_add_f32_e32 v100, v103, v100
	v_exp_f32_e32 v105, v89
	v_add_f32_e32 v82, v87, v82
	v_exp_f32_e32 v89, v106
	v_add_f32_e32 v100, v104, v100
	v_exp_f32_e32 v106, v90
	v_add_f32_e32 v82, v88, v82
	v_exp_f32_e32 v90, v107
	v_add_f32_e32 v100, v105, v100
	v_exp_f32_e32 v107, v91
	v_add_f32_e32 v82, v89, v82
	v_exp_f32_e32 v91, v108
	v_add_f32_e32 v100, v106, v100
	v_exp_f32_e32 v108, v92
	v_add_f32_e32 v82, v90, v82
	v_exp_f32_e32 v92, v109
	v_add_f32_e32 v100, v107, v100
	v_exp_f32_e32 v109, v93
	v_add_f32_e32 v82, v91, v82
	v_exp_f32_e32 v93, v110
	v_add_f32_e32 v100, v108, v100
	v_exp_f32_e32 v110, v94
	v_add_f32_e32 v82, v92, v82
	v_exp_f32_e32 v94, v111
	v_add_f32_e32 v100, v109, v100
	v_exp_f32_e32 v111, v95
	v_add_f32_e32 v82, v93, v82
	v_exp_f32_e32 v95, v112
	v_add_f32_e32 v100, v110, v100
	v_exp_f32_e32 v112, v96
	v_add_f32_e32 v82, v94, v82
	v_exp_f32_e32 v96, v113
	v_add_f32_e32 v100, v111, v100
	v_exp_f32_e32 v97, v97
	v_add_f32_e32 v82, v95, v82
	v_add_f32_e32 v100, v112, v100
	v_add_f32_e32 v82, v96, v82
	v_add_f32_e32 v100, v97, v100
	s_lshl_b32 s24, s23, 14
	v_add_f32_e32 v82, v82, v100
	v_add_f32_e32 v188, v188, v82
	v_cvt_pk_bf16_f32 v82, v98, v99
	v_cvt_pk_bf16_f32 v83, v83, v84
	v_cvt_pk_bf16_f32 v84, v85, v86
	v_cvt_pk_bf16_f32 v85, v87, v88
	v_cvt_pk_bf16_f32 v86, v89, v90
	v_cvt_pk_bf16_f32 v87, v91, v92
	v_cvt_pk_bf16_f32 v88, v93, v94
	v_cvt_pk_bf16_f32 v89, v95, v96
	v_cvt_pk_bf16_f32 v90, v240, v242
	v_cvt_pk_bf16_f32 v91, v241, v101
	v_cvt_pk_bf16_f32 v92, v102, v103
	v_cvt_pk_bf16_f32 v93, v104, v105
	v_cvt_pk_bf16_f32 v94, v106, v107
	v_cvt_pk_bf16_f32 v95, v108, v109
	v_cvt_pk_bf16_f32 v96, v110, v111
	v_cvt_pk_bf16_f32 v97, v112, v97
	v_add_u32_e32 v244, s24, v209
	ds_read_b64_tr_b16 v[106:107], v244 offset:0x2000
	ds_read_b64_tr_b16 v[108:109], v244 offset:0x2800
	ds_read_b64_tr_b16 v[110:111], v244 offset:0x3000
	ds_read_b64_tr_b16 v[112:113], v244 offset:0x3800
	s_add_i32 s19, s19, 1
	v_permlane32_swap_b32_e32 v82, v84
	v_permlane32_swap_b32_e32 v83, v85
	v_permlane32_swap_b32_e32 v86, v88
	v_permlane32_swap_b32_e32 v87, v89
	v_permlane32_swap_b32_e32 v90, v92
	v_permlane32_swap_b32_e32 v91, v93
	v_permlane32_swap_b32_e32 v94, v96
	v_permlane32_swap_b32_e32 v95, v97
	s_waitcnt lgkmcnt(4)
; #define PSUB_AT(k) do { if (PROBE_SUB == (k) && DK == PROBE_SUBDK) sacc = __builtin_amdgcn_readfirstlane(sacc + ((unsigned)__builtin_readcyclecounter() - ps_t0_)); } while (0)
; #define SBAR() __builtin_amdgcn_sched_barrier(0)
; #define SLOAD(k0) do { const unsigned so_k = (unsigned)((k0) * ldk) * 2u, so_v = (unsigned)((k0) * ldv) * 2u; \
;         _Pragma("unroll") for (int i = 0; i < KP; ++i) ks[i] = __builtin_amdgcn_raw_buffer_load_b128(krs, kgo[i], so_k, 0); \
;         vs0 = __builtin_amdgcn_raw_buffer_load_b128(vrs, vgo, so_v, 0); vs1 = __builtin_amdgcn_raw_buffer_load_b128(vrs, vgo + vstep, so_v, 0); } while (0)
; #define SWRITE(b) do { _Pragma("unroll") for (int i = 0; i < KP; ++i) *reinterpret_cast<u32x4*>(K_lds + (b) * SHM_K + kst[i]) = ks[i]; \
;         *reinterpret_cast<u32x4*>(V_lds + (b) * SHM_V + vst0) = vs0; *reinterpret_cast<u32x4*>(V_lds + (b) * SHM_V + vst0 + vst1d) = vs1; } while (0)
; template <int DK, bool PF, bool EARLY, bool PFD = false> ...
;     ...
;         for (int d0 = 0; d0 < NQ; ++d0) {
;             const bf16x8 b0 = *reinterpret_cast<const bf16x8*>(Kb + kra_(d0 & 3) + (d0 >> 2) * 128);
;             const bf16x8 b1 = *reinterpret_cast<const bf16x8*>(Kb + kra_(d0 & 3) + (d0 >> 2) * 128 + 32 * DK * 2);
;             p0 = __builtin_amdgcn_mfma_f32_32x32x16_bf16(b0, qr[d0], p0, 0, 0, 0);
;             p1 = __builtin_amdgcn_mfma_f32_32x32x16_bf16(b1, qr[d0], p1, 0, 0, 0);
;             if ((d0 & 3) == 3) SBAR();
;         }
;         PSUB_AT(1);
;         if (!EARLY && j + 1 < ntile) SLOAD((j + 1) * 64);
;         float ps = 0.f, ps1 = 0.f;
; #pragma unroll
;         for (int r = 0; r < 16; ++r) { p0[r] = __builtin_amdgcn_exp2f(p0[r]); p1[r] = __builtin_amdgcn_exp2f(p1[r]); ps += p0[r]; asm("" : "+v"(ps)); ps1 += p1[r]; asm("" : "+v"(ps1)); }
;         l_reg += ps + ps1;
;         bf16x8 pa0, pa1, pa2, pa3;
;     ...
;         PK4(p0, 0, pa0); PK4(p0, 8, pa1); PK4(p1, 0, pa2); PK4(p1, 8, pa3);
;     ...
;         PSUB_AT(2);
;         const int vb = vb0 + cur * SHM_V;
;         pv_one<0>(o[0], vb, pa0, pa1, pa2, pa3); pv_one<1>(o[1], vb, pa0, pa1, pa2, pa3); pv_one<2>(o[2], vb, pa0, pa1, pa2, pa3); pv_one<3>(o[3], vb, pa0, pa1, pa2, pa3);
;         PSUB_AT(3);
;         if (j + 1 < ntile) SWRITE(cur ^ 1);
;         if (j + 3 < ntile) PREFETCH(j + 3);
;         __syncthreads();
	v_mfma_f32_32x32x16_bf16 v[2:17], v[82:85], v[246:249], v[2:17]
	ds_read_b64_tr_b16 v[98:99], v244 offset:0x200
	ds_read_b64_tr_b16 v[100:101], v244 offset:0xa00
	v_mfma_f32_32x32x16_bf16 v[2:17], v[86:89], v[250:253], v[2:17]
	ds_read_b64_tr_b16 v[102:103], v244 offset:0x1200
	ds_read_b64_tr_b16 v[104:105], v244 offset:0x1a00
	s_waitcnt lgkmcnt(6)
	v_mfma_f32_32x32x16_bf16 v[2:17], v[90:93], v[106:109], v[2:17]
	ds_read_b64_tr_b16 v[106:107], v244 offset:0x2200
	ds_read_b64_tr_b16 v[108:109], v244 offset:0x2a00
	ds_read_b64_tr_b16 v[240:241], v244 offset:0x3200
	ds_read_b64_tr_b16 v[242:243], v244 offset:0x3a00
	s_waitcnt lgkmcnt(8)
	v_mfma_f32_32x32x16_bf16 v[2:17], v[94:97], v[110:113], v[2:17]
	s_waitcnt lgkmcnt(6)
	v_mfma_f32_32x32x16_bf16 v[18:33], v[82:85], v[98:101], v[18:33]
	ds_read_b64_tr_b16 v[98:99], v244 offset:0x400
	ds_read_b64_tr_b16 v[100:101], v244 offset:0xc00
	s_waitcnt lgkmcnt(6)
	v_mfma_f32_32x32x16_bf16 v[18:33], v[86:89], v[102:105], v[18:33]
	ds_read_b64_tr_b16 v[102:103], v244 offset:0x1400
	ds_read_b64_tr_b16 v[104:105], v244 offset:0x1c00
	s_waitcnt lgkmcnt(6)
	v_mfma_f32_32x32x16_bf16 v[18:33], v[90:93], v[106:109], v[18:33]
	ds_read_b64_tr_b16 v[106:107], v244 offset:0x2400
	ds_read_b64_tr_b16 v[108:109], v244 offset:0x2c00
	ds_read_b64_tr_b16 v[110:111], v244 offset:0x3400
	ds_read_b64_tr_b16 v[112:113], v244 offset:0x3c00
	s_waitcnt lgkmcnt(8)
	v_mfma_f32_32x32x16_bf16 v[18:33], v[94:97], v[240:243], v[18:33]
	s_waitcnt lgkmcnt(6)
	v_mfma_f32_32x32x16_bf16 v[34:49], v[82:85], v[98:101], v[34:49]
	ds_read_b64_tr_b16 v[98:99], v244 offset:0x600
	ds_read_b64_tr_b16 v[100:101], v244 offset:0xe00
	s_waitcnt lgkmcnt(6)
	v_mfma_f32_32x32x16_bf16 v[34:49], v[86:89], v[102:105], v[34:49]
	ds_read_b64_tr_b16 v[102:103], v244 offset:0x1600
	ds_read_b64_tr_b16 v[104:105], v244 offset:0x1e00
	s_waitcnt lgkmcnt(6)
	v_mfma_f32_32x32x16_bf16 v[34:49], v[90:93], v[106:109], v[34:49]
	ds_read_b64_tr_b16 v[106:107], v244 offset:0x2600
	ds_read_b64_tr_b16 v[108:109], v244 offset:0x2e00
	ds_read_b64_tr_b16 v[240:241], v244 offset:0x3600
	ds_read_b64_tr_b16 v[242:243], v244 offset:0x3e00
	s_waitcnt lgkmcnt(8)
	v_mfma_f32_32x32x16_bf16 v[34:49], v[94:97], v[110:113], v[34:49]
	s_waitcnt lgkmcnt(6)
	v_mfma_f32_32x32x16_bf16 v[50:65], v[82:85], v[98:101], v[50:65]
	s_waitcnt lgkmcnt(0)
	s_xor_b32 s23, s23, 1
	s_mulk_i32 s23, 0x6000
	s_add_i32 s23, s23, 0
	v_add_u32_e32 v82, s23, v187
	s_waitcnt vmcnt(4)
	ds_write_b128 v82, v[166:169] offset:32768
	v_add_u32_e32 v82, s23, v193
	s_waitcnt vmcnt(3)
	ds_write_b128 v82, v[162:165] offset:32768
	v_mfma_f32_32x32x16_bf16 v[50:65], v[86:89], v[102:105], v[50:65]
	v_add_u32_e32 v82, s23, v197
	s_xor_b32 s23, s24, 0x4000
	s_add_i32 s20, s20, 0x18000
	s_add_i32 s21, s21, 0x10000
	v_add_u32_e32 v83, s23, v205
	s_cmp_eq_u32 s20, 0x660000
	s_waitcnt vmcnt(2)
	ds_write_b128 v82, v[178:181] offset:32768
	v_mfma_f32_32x32x16_bf16 v[50:65], v[90:93], v[106:109], v[50:65]
	s_waitcnt vmcnt(1)
	ds_write_b128 v83, v[170:173]
	s_waitcnt vmcnt(0)
	ds_write_b128 v83, v[174:177] offset:8192
	s_waitcnt lgkmcnt(0)
	s_barrier
	v_mfma_f32_32x32x16_bf16 v[50:65], v[94:97], v[240:243], v[50:65]
	s_cbranch_scc0 .LBB0_1200
	ds_read_b128 v[98:101], v217 offset:57344
	ds_read_b128 v[102:105], v218 offset:12288
	s_waitcnt lgkmcnt(1)
	v_mfma_f32_32x32x16_bf16 v[82:97], v[98:101], v[158:161], v[66:81]
	ds_read_b128 v[98:101], v219 offset:57344
	s_waitcnt lgkmcnt(1)
	v_mfma_f32_32x32x16_bf16 v[66:81], v[102:105], v[158:161], v[66:81]
	s_waitcnt lgkmcnt(0)
	v_mfma_f32_32x32x16_bf16 v[82:97], v[98:101], v[154:157], v[82:97]
	ds_read_b128 v[98:101], v220 offset:12288
	s_waitcnt lgkmcnt(0)
	v_mfma_f32_32x32x16_bf16 v[66:81], v[98:101], v[154:157], v[66:81]
	ds_read_b128 v[98:101], v221 offset:57344
	s_waitcnt lgkmcnt(0)
	v_mfma_f32_32x32x16_bf16 v[82:97], v[98:101], v[150:153], v[82:97]
	ds_read_b128 v[98:101], v222 offset:12288
	s_waitcnt lgkmcnt(0)
	v_mfma_f32_32x32x16_bf16 v[66:81], v[98:101], v[150:153], v[66:81]
	ds_read_b128 v[98:101], v223 offset:57344
	s_waitcnt lgkmcnt(0)
	v_mfma_f32_32x32x16_bf16 v[82:97], v[98:101], v[146:149], v[82:97]
	ds_read_b128 v[98:101], v224 offset:12288
	s_waitcnt lgkmcnt(0)
	v_mfma_f32_32x32x16_bf16 v[66:81], v[98:101], v[146:149], v[66:81]
	ds_read_b128 v[98:101], v217 offset:57472
	ds_read_b128 v[102:105], v218 offset:12416
	s_waitcnt lgkmcnt(1)
	v_mfma_f32_32x32x16_bf16 v[82:97], v[98:101], v[142:145], v[82:97]
	ds_read_b128 v[98:101], v219 offset:57472
	s_waitcnt lgkmcnt(1)
	v_mfma_f32_32x32x16_bf16 v[66:81], v[102:105], v[142:145], v[66:81]
	s_waitcnt lgkmcnt(0)
	v_mfma_f32_32x32x16_bf16 v[82:97], v[98:101], v[138:141], v[82:97]
	ds_read_b128 v[98:101], v220 offset:12416
	s_waitcnt lgkmcnt(0)
	v_mfma_f32_32x32x16_bf16 v[66:81], v[98:101], v[138:141], v[66:81]
	ds_read_b128 v[98:101], v221 offset:57472
	s_waitcnt lgkmcnt(0)
	v_mfma_f32_32x32x16_bf16 v[82:97], v[98:101], v[134:137], v[82:97]
	ds_read_b128 v[98:101], v222 offset:12416
	s_waitcnt lgkmcnt(0)
	v_mfma_f32_32x32x16_bf16 v[66:81], v[98:101], v[134:137], v[66:81]
	ds_read_b128 v[98:101], v223 offset:57472
	s_waitcnt lgkmcnt(0)
	v_mfma_f32_32x32x16_bf16 v[82:97], v[98:101], v[130:133], v[82:97]
	ds_read_b128 v[98:101], v224 offset:12416
	s_waitcnt lgkmcnt(0)
	v_mfma_f32_32x32x16_bf16 v[66:81], v[98:101], v[130:133], v[66:81]
	ds_read_b128 v[98:101], v217 offset:57600
	ds_read_b128 v[102:105], v218 offset:12544
	s_waitcnt lgkmcnt(1)
	v_mfma_f32_32x32x16_bf16 v[82:97], v[98:101], v[126:129], v[82:97]
	ds_read_b128 v[98:101], v219 offset:57600
	s_waitcnt lgkmcnt(1)
	v_mfma_f32_32x32x16_bf16 v[66:81], v[102:105], v[126:129], v[66:81]
	s_waitcnt lgkmcnt(0)
; #define PSUB_AT(k) do { if (PROBE_SUB == (k) && DK == PROBE_SUBDK) sacc = __builtin_amdgcn_readfirstlane(sacc + ((unsigned)__builtin_readcyclecounter() - ps_t0_)); } while (0)
; #define SBAR() __builtin_amdgcn_sched_barrier(0)
; __device__ __forceinline__ int crow(int r, int hi) { return (r & 3) + 8 * (r >> 2) + 4 * hi; }
; #define SWRITE(b) do { _Pragma("unroll") for (int i = 0; i < KP; ++i) *reinterpret_cast<u32x4*>(K_lds + (b) * SHM_K + kst[i]) = ks[i]; \
;         *reinterpret_cast<u32x4*>(V_lds + (b) * SHM_V + vst0) = vs0; *reinterpret_cast<u32x4*>(V_lds + (b) * SHM_V + vst0 + vst1d) = vs1; } while (0)
; template <int DK, bool PF, bool EARLY, bool PFD = false> ...
;     ...
;             p0 = __builtin_amdgcn_mfma_f32_32x32x16_bf16(b0, qr[d0], p0, 0, 0, 0);
;             p1 = __builtin_amdgcn_mfma_f32_32x32x16_bf16(b1, qr[d0], p1, 0, 0, 0);
;             if ((d0 & 3) == 3) SBAR();
;         }
;         PSUB_AT(1);
;         if (!EARLY && j + 1 < ntile) SLOAD((j + 1) * 64);
;         float ps = 0.f, ps1 = 0.f;
; #pragma unroll
;         for (int r = 0; r < 16; ++r) { p0[r] = __builtin_amdgcn_exp2f(p0[r]); p1[r] = __builtin_amdgcn_exp2f(p1[r]); ps += p0[r]; asm("" : "+v"(ps)); ps1 += p1[r]; asm("" : "+v"(ps1)); }
;         l_reg += ps + ps1;
;         bf16x8 pa0, pa1, pa2, pa3;
;     ...
;         PK4(p0, 0, pa0); PK4(p0, 8, pa1); PK4(p1, 0, pa2); PK4(p1, 8, pa3);
;     ...
;         PSUB_AT(2);
;         const int vb = vb0 + cur * SHM_V;
;         pv_one<0>(o[0], vb, pa0, pa1, pa2, pa3); pv_one<1>(o[1], vb, pa0, pa1, pa2, pa3); pv_one<2>(o[2], vb, pa0, pa1, pa2, pa3); pv_one<3>(o[3], vb, pa0, pa1, pa2, pa3);
;         PSUB_AT(3);
;         if (j + 1 < ntile) SWRITE(cur ^ 1);
;         if (j + 3 < ntile) PREFETCH(j + 3);
;         __syncthreads();
;         PSUB_AT(4);
;     }
;     __builtin_amdgcn_s_setprio(0);
;     if (PF && !PFD) asm volatile("s_waitcnt vmcnt(0)" : "+v"(pf_dummy) :: "memory");
;     ...
; }
; __device__ __forceinline__ void row_recip(float l_reg, float* li_l  , int r32, int hi, float (&rli)[16]) {
;     { auto rr = __builtin_amdgcn_permlane32_swap(__float_as_uint(l_reg), __float_as_uint(l_reg), false, false); l_reg = __uint_as_float(rr[0]) + __uint_as_float(rr[1]); }
;     if (hi == 0) li_l[r32] = l_reg;
;     asm volatile("s_waitcnt lgkmcnt(0)" ::: "memory");
; #pragma unroll
;     for (int r = 0; r < 16; ++r) rli[r] = __builtin_amdgcn_rcpf(li_l[crow(r, hi)]);
	v_mfma_f32_32x32x16_bf16 v[82:97], v[98:101], v[122:125], v[82:97]
	ds_read_b128 v[98:101], v220 offset:12544
	s_waitcnt lgkmcnt(0)
	v_mfma_f32_32x32x16_bf16 v[66:81], v[98:101], v[122:125], v[66:81]
	ds_read_b128 v[98:101], v221 offset:57600
	s_waitcnt lgkmcnt(0)
	v_mfma_f32_32x32x16_bf16 v[82:97], v[98:101], v[118:121], v[82:97]
	ds_read_b128 v[98:101], v222 offset:12544
	s_waitcnt lgkmcnt(0)
	v_mfma_f32_32x32x16_bf16 v[66:81], v[98:101], v[118:121], v[66:81]
	ds_read_b128 v[98:101], v223 offset:57600
	s_waitcnt lgkmcnt(0)
	v_mfma_f32_32x32x16_bf16 v[82:97], v[98:101], v[114:117], v[82:97]
	ds_read_b128 v[98:101], v224 offset:12544
	s_waitcnt lgkmcnt(0)
	v_mfma_f32_32x32x16_bf16 v[66:81], v[98:101], v[114:117], v[66:81]
	s_nop 11
	v_exp_f32_e32 v98, v66
	v_exp_f32_e32 v82, v82
	v_exp_f32_e32 v67, v67
	v_exp_f32_e32 v83, v83
	v_add_f32_e32 v99, 0, v98
	v_exp_f32_e32 v100, v68
	v_add_f32_e32 v66, 0, v82
	v_exp_f32_e32 v84, v84
	v_add_f32_e32 v99, v67, v99
	v_exp_f32_e32 v85, v85
	v_add_f32_e32 v66, v83, v66
	v_add_f32_e32 v68, v100, v99
	v_exp_f32_e32 v99, v69
	v_exp_f32_e32 v86, v86
	v_add_f32_e32 v66, v84, v66
	v_exp_f32_e32 v101, v70
	v_exp_f32_e32 v70, v87
	v_add_f32_e32 v66, v85, v66
	v_add_f32_e32 v68, v99, v68
	v_exp_f32_e32 v87, v71
	v_exp_f32_e32 v71, v88
	v_add_f32_e32 v66, v86, v66
	v_add_f32_e32 v68, v101, v68
	v_exp_f32_e32 v88, v72
	v_exp_f32_e32 v72, v89
	v_add_f32_e32 v66, v70, v66
	v_add_f32_e32 v68, v87, v68
	v_exp_f32_e32 v89, v73
	v_exp_f32_e32 v73, v90
	v_add_f32_e32 v66, v71, v66
	v_add_f32_e32 v68, v88, v68
	v_exp_f32_e32 v90, v74
	v_exp_f32_e32 v74, v91
	v_add_f32_e32 v66, v72, v66
	v_add_f32_e32 v68, v89, v68
	v_exp_f32_e32 v91, v75
	v_exp_f32_e32 v75, v92
	v_add_f32_e32 v66, v73, v66
	v_add_f32_e32 v68, v90, v68
	v_exp_f32_e32 v92, v76
	v_exp_f32_e32 v76, v93
	v_add_f32_e32 v66, v74, v66
	v_add_f32_e32 v68, v91, v68
	v_exp_f32_e32 v93, v77
	v_exp_f32_e32 v77, v94
	v_add_f32_e32 v66, v75, v66
	v_add_f32_e32 v68, v92, v68
	v_exp_f32_e32 v94, v78
	v_exp_f32_e32 v78, v95
	v_add_f32_e32 v66, v76, v66
	v_add_f32_e32 v68, v93, v68
	v_exp_f32_e32 v95, v79
	v_exp_f32_e32 v79, v96
	v_add_f32_e32 v66, v77, v66
	v_add_f32_e32 v68, v94, v68
	v_exp_f32_e32 v96, v80
	v_exp_f32_e32 v80, v97
	v_add_f32_e32 v66, v78, v66
	v_add_f32_e32 v68, v95, v68
	v_exp_f32_e32 v97, v81
	s_nop 0
	v_add_f32_e32 v66, v79, v66
	v_add_f32_e32 v68, v96, v68
	s_nop 0
	v_add_f32_e32 v66, v80, v66
	v_add_f32_e32 v68, v97, v68
	s_nop 0
	v_add_f32_e32 v66, v66, v68
	v_cvt_pk_bf16_f32 v68, v82, v83
	v_cvt_pk_bf16_f32 v69, v84, v85
	v_cvt_pk_bf16_f32 v70, v86, v70
	v_cvt_pk_bf16_f32 v71, v71, v72
	v_cvt_pk_bf16_f32 v72, v73, v74
	v_cvt_pk_bf16_f32 v73, v75, v76
	v_cvt_pk_bf16_f32 v74, v77, v78
	v_cvt_pk_bf16_f32 v75, v79, v80
	v_cvt_pk_bf16_f32 v76, v98, v67
	v_cvt_pk_bf16_f32 v77, v100, v99
	v_cvt_pk_bf16_f32 v78, v101, v87
	v_cvt_pk_bf16_f32 v79, v88, v89
	v_cvt_pk_bf16_f32 v80, v90, v91
	v_cvt_pk_bf16_f32 v81, v92, v93
	v_cvt_pk_bf16_f32 v82, v94, v95
	v_cvt_pk_bf16_f32 v83, v96, v97
	ds_read_b64_tr_b16 v[84:85], v225 offset:0
	ds_read_b64_tr_b16 v[86:87], v225 offset:0x800
	ds_read_b64_tr_b16 v[88:89], v225 offset:0x1000
	ds_read_b64_tr_b16 v[90:91], v225 offset:0x1800
	ds_read_b64_tr_b16 v[92:93], v225 offset:0x2000
	ds_read_b64_tr_b16 v[94:95], v225 offset:0x2800
	ds_read_b64_tr_b16 v[96:97], v225 offset:0x3000
	ds_read_b64_tr_b16 v[98:99], v225 offset:0x3800
	s_waitcnt lgkmcnt(0)
	v_add_f32_e32 v66, v188, v66
	v_permlane32_swap_b32_e32 v68, v70
	v_permlane32_swap_b32_e32 v69, v71
	v_permlane32_swap_b32_e32 v72, v74
	v_permlane32_swap_b32_e32 v73, v75
	v_permlane32_swap_b32_e32 v76, v78
	v_permlane32_swap_b32_e32 v77, v79
	v_permlane32_swap_b32_e32 v80, v82
	v_permlane32_swap_b32_e32 v81, v83
	v_mfma_f32_32x32x16_bf16 v[2:17], v[68:71], v[84:87], v[2:17]
	ds_read_b64_tr_b16 v[84:85], v225 offset:0x200
	ds_read_b64_tr_b16 v[86:87], v225 offset:0xa00
	v_mfma_f32_32x32x16_bf16 v[2:17], v[72:75], v[88:91], v[2:17]
	ds_read_b64_tr_b16 v[88:89], v225 offset:0x1200
	ds_read_b64_tr_b16 v[90:91], v225 offset:0x1a00
	v_mfma_f32_32x32x16_bf16 v[2:17], v[76:79], v[92:95], v[2:17]
	ds_read_b64_tr_b16 v[92:93], v225 offset:0x2200
	ds_read_b64_tr_b16 v[94:95], v225 offset:0x2a00
	ds_read_b64_tr_b16 v[100:101], v225 offset:0x3200
	ds_read_b64_tr_b16 v[102:103], v225 offset:0x3a00
	s_waitcnt lgkmcnt(0)
	v_mfma_f32_32x32x16_bf16 v[2:17], v[80:83], v[96:99], v[2:17]
	v_mfma_f32_32x32x16_bf16 v[18:33], v[68:71], v[84:87], v[18:33]
	ds_read_b64_tr_b16 v[84:85], v225 offset:0x400
	ds_read_b64_tr_b16 v[86:87], v225 offset:0xc00
	v_mfma_f32_32x32x16_bf16 v[18:33], v[72:75], v[88:91], v[18:33]
	ds_read_b64_tr_b16 v[88:89], v225 offset:0x1400
	ds_read_b64_tr_b16 v[90:91], v225 offset:0x1c00
	v_mfma_f32_32x32x16_bf16 v[18:33], v[76:79], v[92:95], v[18:33]
	ds_read_b64_tr_b16 v[92:93], v225 offset:0x2400
	ds_read_b64_tr_b16 v[94:95], v225 offset:0x2c00
	ds_read_b64_tr_b16 v[96:97], v225 offset:0x3400
	ds_read_b64_tr_b16 v[98:99], v225 offset:0x3c00
	s_waitcnt lgkmcnt(0)
	v_mfma_f32_32x32x16_bf16 v[18:33], v[80:83], v[100:103], v[18:33]
	v_mfma_f32_32x32x16_bf16 v[34:49], v[68:71], v[84:87], v[34:49]
	ds_read_b64_tr_b16 v[84:85], v225 offset:0x600
	ds_read_b64_tr_b16 v[86:87], v225 offset:0xe00
	v_mfma_f32_32x32x16_bf16 v[34:49], v[72:75], v[88:91], v[34:49]
	ds_read_b64_tr_b16 v[88:89], v225 offset:0x1600
	ds_read_b64_tr_b16 v[90:91], v225 offset:0x1e00
	v_mfma_f32_32x32x16_bf16 v[34:49], v[76:79], v[92:95], v[34:49]
	ds_read_b64_tr_b16 v[92:93], v225 offset:0x2600
	ds_read_b64_tr_b16 v[94:95], v225 offset:0x2e00
	ds_read_b64_tr_b16 v[100:101], v225 offset:0x3600
	ds_read_b64_tr_b16 v[102:103], v225 offset:0x3e00
	s_waitcnt lgkmcnt(0)
	v_mfma_f32_32x32x16_bf16 v[34:49], v[80:83], v[96:99], v[34:49]
	v_mfma_f32_32x32x16_bf16 v[50:65], v[68:71], v[84:87], v[50:65]
	s_barrier
	v_mfma_f32_32x32x16_bf16 v[50:65], v[72:75], v[88:91], v[50:65]
	v_mfma_f32_32x32x16_bf16 v[50:65], v[76:79], v[92:95], v[50:65]
	v_mfma_f32_32x32x16_bf16 v[50:65], v[80:83], v[100:103], v[50:65]
	s_setprio 0
	v_mov_b32_e32 v67, v66
	s_nop 1
	v_permlane32_swap_b32_e32 v66, v67
	s_and_saveexec_b64 s[8:9], s[6:7]
	s_cbranch_execz .LBB0_1186
	v_add_f32_e32 v66, v66, v67
	ds_write_b32 v227, v66
	s_branch .LBB0_1186

; #define PSUB_T0() unsigned ps_t0_ = 0u; if (PROBE_SUB && DK == PROBE_SUBDK) ps_t0_ = __builtin_amdgcn_readfirstlane((unsigned)__builtin_readcyclecounter())
; #define PSUB_AT(k) do { if (PROBE_SUB == (k) && DK == PROBE_SUBDK) sacc = __builtin_amdgcn_readfirstlane(sacc + ((unsigned)__builtin_readcyclecounter() - ps_t0_)); } while (0)
; #define SBAR() __builtin_amdgcn_sched_barrier(0)
; #define SLOAD(k0) do { const unsigned so_k = (unsigned)((k0) * ldk) * 2u, so_v = (unsigned)((k0) * ldv) * 2u; \
;         _Pragma("unroll") for (int i = 0; i < KP; ++i) ks[i] = __builtin_amdgcn_raw_buffer_load_b128(krs, kgo[i], so_k, 0); \
;         vs0 = __builtin_amdgcn_raw_buffer_load_b128(vrs, vgo, so_v, 0); vs1 = __builtin_amdgcn_raw_buffer_load_b128(vrs, vgo + vstep, so_v, 0); } while (0)
; template <int DK, bool PF, bool EARLY, bool PFD = false> ...
;     ...
;     for (int j = 0; j < ntile; ++j) {
;         const int cur = j & 1;
;         PSUB_T0();
;         if (EARLY && j + 1 < ntile) SLOAD((j + 1) * 64);
;         f32x16 p0, p1;
; #pragma unroll
;         for (int r = 0; r < 16; ++r) { p0[r] = negM; p1[r] = negM; }
;         const char* Kb = K_lds + cur * SHM_K;
; #pragma unroll
;         for (int d0 = 0; d0 < NQ; ++d0) {
;             const bf16x8 b0 = *reinterpret_cast<const bf16x8*>(Kb + kra_(d0 & 3) + (d0 >> 2) * 128);
;             const bf16x8 b1 = *reinterpret_cast<const bf16x8*>(Kb + kra_(d0 & 3) + (d0 >> 2) * 128 + 32 * DK * 2);
;             p0 = __builtin_amdgcn_mfma_f32_32x32x16_bf16(b0, qr[d0], p0, 0, 0, 0);
;             p1 = __builtin_amdgcn_mfma_f32_32x32x16_bf16(b1, qr[d0], p1, 0, 0, 0);
;             if ((d0 & 3) == 3) SBAR();
;         }
;         PSUB_AT(1);
;         if (!EARLY && j + 1 < ntile) SLOAD((j + 1) * 64);
;         float ps = 0.f, ps1 = 0.f;
; #pragma unroll
;         for (int r = 0; r < 16; ++r) { p0[r] = __builtin_amdgcn_exp2f(p0[r]); p1[r] = __builtin_amdgcn_exp2f(p1[r]); ps += p0[r]; asm("" : "+v"(ps)); ps1 += p1[r]; asm("" : "+v"(ps1)); }
;         l_reg += ps + ps1;
;         bf16x8 pa0, pa1, pa2, pa3;
;     ...
;         PK4(p0, 0, pa0); PK4(p0, 8, pa1); PK4(p1, 0, pa2); PK4(p1, 8, pa3);
;     ...
;         PSUB_AT(2);
;         const int vb = vb0 + cur * SHM_V;
.LBB0_1932:
	s_and_b32 s13, s50, 1
	s_lshl_b32 s12, s13, 13
	v_add_u32_e32 v138, s12, v198
	v_add_u32_e32 v86, v138, v187
	v_add_u32_e32 v134, v138, v200
	v_add_u32_e32 v135, v138, v201
	v_add_u32_e32 v136, v138, v202
	ds_read_b128 v[226:229], v86
	ds_read_b128 v[230:233], v86 offset:4096
	ds_read_b128 v[234:237], v134
	ds_read_b128 v[238:241], v134 offset:4096
	ds_read_b128 v[242:245], v135
	ds_read_b128 v[246:249], v135 offset:4096
	ds_read_b128 v[250:253], v136
	ds_read_b128 v[218:221], v136 offset:4096
	s_add_i32 s33, s51, 0xfff40000
	buffer_load_dwordx4 v[130:133], v145, s[16:19], s33 offen
	buffer_load_dwordx4 v[134:137], v186, s[20:23], s33 offen
	buffer_load_dwordx4 v[138:141], v195, s[20:23], s33 offen
	s_waitcnt lgkmcnt(7)
	v_mfma_f32_32x32x16_bf16 v[98:113], v[226:229], v[126:129], v[2:17]
	s_waitcnt lgkmcnt(6)
	v_mfma_f32_32x32x16_bf16 v[82:97], v[230:233], v[126:129], v[2:17]
	s_waitcnt lgkmcnt(5)
	v_mfma_f32_32x32x16_bf16 v[98:113], v[234:237], v[122:125], v[98:113]
	s_waitcnt lgkmcnt(4)
	v_mfma_f32_32x32x16_bf16 v[82:97], v[238:241], v[122:125], v[82:97]
	s_waitcnt lgkmcnt(3)
	v_mfma_f32_32x32x16_bf16 v[98:113], v[242:245], v[118:121], v[98:113]
	s_waitcnt lgkmcnt(2)
	v_mfma_f32_32x32x16_bf16 v[82:97], v[246:249], v[118:121], v[82:97]
	s_waitcnt lgkmcnt(1)
	v_mfma_f32_32x32x16_bf16 v[98:113], v[250:253], v[114:117], v[98:113]
	s_waitcnt lgkmcnt(0)
	v_mfma_f32_32x32x16_bf16 v[82:97], v[218:221], v[114:117], v[82:97]
	s_lshl_b32 s13, s13, 14
	v_add_u32_e32 v253, s13, v199
	ds_read_b64_tr_b16 v[226:227], v253 offset:0x0
	ds_read_b64_tr_b16 v[228:229], v253 offset:0x800
	ds_read_b64_tr_b16 v[230:231], v253 offset:0x1000
	ds_read_b64_tr_b16 v[232:233], v253 offset:0x1800
	ds_read_b64_tr_b16 v[234:235], v253 offset:0x2000
	ds_read_b64_tr_b16 v[236:237], v253 offset:0x2800
	ds_read_b64_tr_b16 v[238:239], v253 offset:0x3000
	ds_read_b64_tr_b16 v[240:241], v253 offset:0x3800
	s_nop 0
	v_exp_f32_e32 v98, v98
	s_nop 1
	v_exp_f32_e32 v159, v82
	v_exp_f32_e32 v99, v99
	v_exp_f32_e32 v163, v83
	v_add_f32_e32 v82, 0, v98
	v_add_f32_e32 v161, 0, v159
	v_exp_f32_e32 v100, v100
	v_exp_f32_e32 v101, v101
	v_add_f32_e32 v82, v99, v82
	v_add_f32_e32 v83, v163, v161
	v_exp_f32_e32 v161, v84
	v_exp_f32_e32 v165, v85
	v_add_f32_e32 v82, v100, v82
	v_exp_f32_e32 v102, v102
	v_exp_f32_e32 v167, v86
	v_add_f32_e32 v83, v161, v83
	v_add_f32_e32 v82, v101, v82
	v_exp_f32_e32 v86, v103
	v_exp_f32_e32 v103, v87
	v_add_f32_e32 v83, v165, v83
	v_add_f32_e32 v82, v102, v82
	v_exp_f32_e32 v87, v104
	v_exp_f32_e32 v104, v88
	v_add_f32_e32 v83, v167, v83
	v_add_f32_e32 v82, v86, v82
	v_exp_f32_e32 v88, v105
	v_exp_f32_e32 v105, v89
	v_add_f32_e32 v83, v103, v83
	v_add_f32_e32 v82, v87, v82
	v_exp_f32_e32 v89, v106
	v_exp_f32_e32 v106, v90
	v_add_f32_e32 v83, v104, v83
	v_add_f32_e32 v82, v88, v82
	v_exp_f32_e32 v90, v107
	v_exp_f32_e32 v107, v91
	v_add_f32_e32 v83, v105, v83
	v_add_f32_e32 v82, v89, v82
	v_exp_f32_e32 v91, v108
	v_exp_f32_e32 v108, v92
	v_add_f32_e32 v83, v106, v83
	v_add_f32_e32 v82, v90, v82
	v_exp_f32_e32 v92, v109
	v_exp_f32_e32 v109, v93
	v_add_f32_e32 v83, v107, v83
	v_add_f32_e32 v82, v91, v82
	v_exp_f32_e32 v93, v110
	v_exp_f32_e32 v110, v94
	v_add_f32_e32 v83, v108, v83
	v_add_f32_e32 v82, v92, v82
	v_exp_f32_e32 v94, v111
	v_exp_f32_e32 v111, v95
	v_add_f32_e32 v83, v109, v83
	v_add_f32_e32 v82, v93, v82
	v_exp_f32_e32 v95, v112
	v_exp_f32_e32 v112, v96
	v_add_f32_e32 v83, v110, v83
	v_add_f32_e32 v82, v94, v82
	v_exp_f32_e32 v96, v113
	v_add_f32_e32 v83, v111, v83
	v_add_f32_e32 v82, v95, v82
	v_exp_f32_e32 v113, v97
	v_add_f32_e32 v83, v112, v83
	v_add_f32_e32 v82, v96, v82
	v_cvt_pk_bf16_f32 v84, v98, v99
	v_cvt_pk_bf16_f32 v85, v100, v101
	v_cvt_pk_bf16_f32 v86, v102, v86
	v_cvt_pk_bf16_f32 v87, v87, v88
	v_cvt_pk_bf16_f32 v88, v89, v90
	v_cvt_pk_bf16_f32 v89, v91, v92
	v_cvt_pk_bf16_f32 v90, v93, v94
	v_cvt_pk_bf16_f32 v91, v95, v96
	v_cvt_pk_bf16_f32 v92, v159, v163
	v_cvt_pk_bf16_f32 v93, v161, v165
	v_cvt_pk_bf16_f32 v94, v167, v103
	v_cvt_pk_bf16_f32 v95, v104, v105
	v_cvt_pk_bf16_f32 v96, v106, v107
	v_cvt_pk_bf16_f32 v97, v108, v109
	v_cvt_pk_bf16_f32 v98, v110, v111
	v_cvt_pk_bf16_f32 v99, v112, v113
	v_add_u32_e32 v112, s13, v199
	v_add_f32_e32 v83, v113, v83
	v_permlane32_swap_b32_e32 v84, v86
	v_permlane32_swap_b32_e32 v85, v87
	v_permlane32_swap_b32_e32 v88, v90
	v_permlane32_swap_b32_e32 v89, v91
	v_permlane32_swap_b32_e32 v92, v94
	v_permlane32_swap_b32_e32 v93, v95
	v_permlane32_swap_b32_e32 v96, v98
	v_permlane32_swap_b32_e32 v97, v99
	s_waitcnt lgkmcnt(0)
; #define PSUB_AT(k) do { if (PROBE_SUB == (k) && DK == PROBE_SUBDK) sacc = __builtin_amdgcn_readfirstlane(sacc + ((unsigned)__builtin_readcyclecounter() - ps_t0_)); } while (0)
; #define SWRITE(b) do { _Pragma("unroll") for (int i = 0; i < KP; ++i) *reinterpret_cast<u32x4*>(K_lds + (b) * SHM_K + kst[i]) = ks[i]; \
;         *reinterpret_cast<u32x4*>(V_lds + (b) * SHM_V + vst0) = vs0; *reinterpret_cast<u32x4*>(V_lds + (b) * SHM_V + vst0 + vst1d) = vs1; } while (0)
; template <int DK, bool PF, bool EARLY, bool PFD = false> ...
;     ...
;         const int vb = vb0 + cur * SHM_V;
;         pv_one<0>(o[0], vb, pa0, pa1, pa2, pa3); pv_one<1>(o[1], vb, pa0, pa1, pa2, pa3); pv_one<2>(o[2], vb, pa0, pa1, pa2, pa3); pv_one<3>(o[3], vb, pa0, pa1, pa2, pa3);
;         PSUB_AT(3);
;         if (j + 1 < ntile) SWRITE(cur ^ 1);
;         if (j + 3 < ntile) PREFETCH(j + 3);
;         __syncthreads();
	v_mfma_f32_32x32x16_bf16 v[66:81], v[84:87], v[226:229], v[66:81]
	ds_read_b64_tr_b16 v[100:101], v112 offset:0x200
	ds_read_b64_tr_b16 v[102:103], v112 offset:0xa00
	v_mfma_f32_32x32x16_bf16 v[66:81], v[88:91], v[230:233], v[66:81]
	ds_read_b64_tr_b16 v[104:105], v112 offset:0x1200
	ds_read_b64_tr_b16 v[106:107], v112 offset:0x1a00
	v_mfma_f32_32x32x16_bf16 v[66:81], v[92:95], v[234:237], v[66:81]
	ds_read_b64_tr_b16 v[108:109], v112 offset:0x2200
	ds_read_b64_tr_b16 v[110:111], v112 offset:0x2a00
	ds_read_b64_tr_b16 v[222:223], v112 offset:0x3200
	ds_read_b64_tr_b16 v[224:225], v112 offset:0x3a00
	v_mfma_f32_32x32x16_bf16 v[66:81], v[96:99], v[238:241], v[66:81]
	s_waitcnt lgkmcnt(6)
	v_mfma_f32_32x32x16_bf16 v[50:65], v[84:87], v[100:103], v[50:65]
	ds_read_b64_tr_b16 v[100:101], v112 offset:0x400
	ds_read_b64_tr_b16 v[102:103], v112 offset:0xc00
	s_waitcnt lgkmcnt(6)
	v_mfma_f32_32x32x16_bf16 v[50:65], v[88:91], v[104:107], v[50:65]
	ds_read_b64_tr_b16 v[104:105], v112 offset:0x1400
	ds_read_b64_tr_b16 v[106:107], v112 offset:0x1c00
	s_waitcnt lgkmcnt(6)
	v_mfma_f32_32x32x16_bf16 v[50:65], v[92:95], v[108:111], v[50:65]
	ds_read_b64_tr_b16 v[108:109], v112 offset:0x2400
	ds_read_b64_tr_b16 v[110:111], v112 offset:0x2c00
	ds_read_b64_tr_b16 v[218:219], v112 offset:0x3400
	ds_read_b64_tr_b16 v[220:221], v112 offset:0x3c00
	s_waitcnt lgkmcnt(8)
	v_mfma_f32_32x32x16_bf16 v[50:65], v[96:99], v[222:225], v[50:65]
	s_waitcnt lgkmcnt(6)
	v_mfma_f32_32x32x16_bf16 v[34:49], v[84:87], v[100:103], v[34:49]
	ds_read_b64_tr_b16 v[100:101], v112 offset:0x600
	ds_read_b64_tr_b16 v[102:103], v112 offset:0xe00
	s_waitcnt lgkmcnt(6)
	v_mfma_f32_32x32x16_bf16 v[34:49], v[88:91], v[104:107], v[34:49]
	ds_read_b64_tr_b16 v[104:105], v112 offset:0x1600
	ds_read_b64_tr_b16 v[106:107], v112 offset:0x1e00
	s_waitcnt lgkmcnt(6)
	v_mfma_f32_32x32x16_bf16 v[34:49], v[92:95], v[108:111], v[34:49]
	ds_read_b64_tr_b16 v[108:109], v112 offset:0x2600
	ds_read_b64_tr_b16 v[110:111], v112 offset:0x2e00
	ds_read_b64_tr_b16 v[222:223], v112 offset:0x3600
	ds_read_b64_tr_b16 v[224:225], v112 offset:0x3e00
	s_waitcnt lgkmcnt(8)
	v_mfma_f32_32x32x16_bf16 v[34:49], v[96:99], v[218:221], v[34:49]
	s_waitcnt lgkmcnt(6)
	v_mfma_f32_32x32x16_bf16 v[18:33], v[84:87], v[100:103], v[18:33]
	s_waitcnt lgkmcnt(0)
	s_xor_b32 s12, s12, 0x2000
	v_add_u32_e32 v84, s12, v196
	s_xor_b32 s12, s13, 0x4000
	s_cmpk_lt_u32 s50, 0x41
	s_waitcnt vmcnt(2)
	ds_write_b128 v84, v[130:133]
	v_add_u32_e32 v84, s12, v197
	s_cselect_b64 s[12:13], -1, 0
	v_mfma_f32_32x32x16_bf16 v[18:33], v[88:91], v[104:107], v[18:33]
	s_and_b64 s[36:37], s[6:7], s[12:13]
	s_waitcnt vmcnt(1)
	ds_write_b128 v84, v[134:137]
	s_waitcnt vmcnt(0)
	ds_write_b128 v84, v[138:141] offset:8192
	v_mfma_f32_32x32x16_bf16 v[18:33], v[92:95], v[108:111], v[18:33]
	v_mfma_f32_32x32x16_bf16 v[18:33], v[96:99], v[222:225], v[18:33]
	s_and_saveexec_b64 s[12:13], s[36:37]
	s_cbranch_execz .LBB0_1931
	s_and_saveexec_b64 s[36:37], s[26:27]
	s_xor_b64 s[36:37], exec, s[36:37]
	s_lshl_b32 s33, s50, 6
	s_addk_i32 s33, 0xc0
	v_add_u32_e32 v84, s33, v189
	v_mul_lo_u32 v84, v84, s42
	v_or_b32_e32 v84, v84, v190
	v_lshl_add_u32 v84, v84, 1, s49
	s_andn2_saveexec_b64 s[36:37], s[36:37]
	s_cbranch_execz .LBB0_1930
	v_add_u32_e32 v84, s51, v206
	s_branch .LBB0_1930
